# v4b: P10 row-index loads de-serialised; P12 gains hoisted; K-loop LDS-DMA saddr addressing (no sleep)
# speedup vs baseline: 1.0201x; 1.0201x over previous
; #define PG8_STAGE(bufoff, gbase, voff) do { _Pragma("unroll") for (int _i = 0; _i < 2; ++_i) \
;         __builtin_amdgcn_global_load_lds((const unsigned*)((const char*)(gbase) + (voff)[_i]), (LAS unsigned*)(lds + (bufoff) + ldsw + _i * 8192), 16, 0, 0); } while (0)
; #define PG8_LDA(dst, b, h) do { if constexpr (F8) { _Pragma("unroll") for (int m = 0; m < 4; ++m) dst##8[m] = PG8_LD8(lds, PG8_SA(b, h) + aoff + m * 2048); } \
;         else { _Pragma("unroll") for (int m = 0; m < 4; ++m) _Pragma("unroll") for (int k = 0; k < 2; ++k) dst[m][k] = *(const LAS bf16x8*)(lds + PG8_SA(b, h) + aoff + m * 2048 + k * 1024); } } while (0)
; #define PG8_WAIT_V(n) asm volatile("s_waitcnt vmcnt(" #n ")" ::: "memory")
; #define PG8_WAIT_L(n) asm volatile("s_waitcnt lgkmcnt(" #n ")" ::: "memory")
; #define PG8_BAR __builtin_amdgcn_s_barrier()
; #define PG8_SCHED __builtin_amdgcn_sched_barrier(0)
; template <bool GATHER, bool F8, class Epi, class Sched>
; __device__ __forceinline__ void gemm_phase(LAS unsigned char* lds, const int nt, const unsigned lda, const unsigned ldb, const Sched& S, const Epi& E) {
;     ...
;         for (int t = 0; t < nt; t += 2) {
;             const bool last = (t == nt - 2);
;             const char* a1 = cA + (size_t)(t + 1) * kstep;
;             const char* a2 = last ? nA : cA + (size_t)(t + 2) * kstep; const char* b2 = last ? nB : cB + (size_t)(t + 2) * kstep;
;             const char* a3 = a2 + kstep; const char* b3 = b2 + kstep;
;             unsigned w0[2], w1[2];
;             if constexpr (GATHER) {
; #pragma unroll
;                 for (int i = 0; i < 2; ++i) { w0[i] = last ? vN0[i] : vA0[i]; w1[i] = last ? vN1[i] : vA1[i]; }
;             } else {
; #pragma unroll
;                 for (int i = 0; i < 2; ++i) { w0[i] = voffA[i]; w1[i] = voffA[i]; }
;             }
;             PG8_LDB(B0, 0, 0); PG8_LDB(B1, 0, 1); PG8_SCHED; PG8_LDA(At, 0, 0); PG8_STAGE(PG8_SA(1, 1), a1 + hA, vA1);
;             PG8_WAIT_V(8); PG8_WAIT_L(0); PG8_BAR; PG8_MMA(0, 0, At, B0); PG8_MMA(0, 1, At, B1); PG8_BAR; PG8_SCHED;
;             PG8_LDA(At, 0, 1); PG8_STAGE(PG8_SB(0, 0), b2, voffB); PG8_STAGE(PG8_SB(0, 1), b2 + hB, voffB); PG8_STAGE(PG8_SA(0, 0), a2, w0);
;             PG8_WAIT_V(8); PG8_WAIT_L(0); PG8_BAR; PG8_MMA(1, 0, At, B0); PG8_MMA(1, 1, At, B1); PG8_BAR; PG8_SCHED;
.LBB0_247:
	ds_read_b128 v[148:151], v181
	ds_read_b128 v[152:155], v181 offset:1024
	ds_read_b128 v[156:159], v181 offset:2048
	ds_read_b128 v[160:163], v181 offset:3072
	ds_read_b128 v[190:193], v182
	ds_read_b128 v[194:197], v182 offset:1024
	ds_read_b128 v[200:203], v182 offset:2048
	ds_read_b128 v[204:207], v182 offset:3072
	s_add_u32 s34, s10, 0xfff80080
	s_addc_u32 s35, s11, -1
	s_cmp_eq_u32 s33, 28
	s_cselect_b32 s37, s1, s35
	s_cselect_b32 s36, s0, s34
	s_cselect_b32 s35, s31, s27
	s_cselect_b32 s34, s30, s14
	s_add_i32 m0, s42, 0xc000
	ds_read_b128 v[208:211], v183
	ds_read_b128 v[212:215], v183 offset:1024
	ds_read_b128 v[216:219], v183 offset:2048
	ds_read_b128 v[220:223], v183 offset:3072
	ds_read_b128 v[224:227], v183 offset:4096
	ds_read_b128 v[228:231], v183 offset:5120
	ds_read_b128 v[232:235], v183 offset:6144
	ds_read_b128 v[236:239], v183 offset:7168
	global_load_lds_dwordx4 v140, s[10:11]
	s_add_i32 m0, s42, 0xe000
	s_nop 0
	global_load_lds_dwordx4 v142, s[10:11]
	s_waitcnt vmcnt(8)
	s_waitcnt lgkmcnt(0)
	s_barrier
	s_setprio 1
	s_waitcnt lgkmcnt(0)
	v_mfma_f32_16x16x32_bf16 v[126:129], v[148:151], v[208:211], v[126:129]
	v_mfma_f32_16x16x32_bf16 v[122:125], v[156:159], v[208:211], v[122:125]
	v_mfma_f32_16x16x32_bf16 v[110:113], v[148:151], v[216:219], v[110:113]
	v_mfma_f32_16x16x32_bf16 v[106:109], v[156:159], v[216:219], v[106:109]
	v_mfma_f32_16x16x32_bf16 v[94:97], v[148:151], v[224:227], v[94:97]
	v_mfma_f32_16x16x32_bf16 v[90:93], v[156:159], v[224:227], v[90:93]
	v_mfma_f32_16x16x32_bf16 v[78:81], v[148:151], v[232:235], v[78:81]
	v_mfma_f32_16x16x32_bf16 v[74:77], v[156:159], v[232:235], v[74:77]
	v_mfma_f32_16x16x32_bf16 v[126:129], v[152:155], v[212:215], v[126:129]
	v_mfma_f32_16x16x32_bf16 v[122:125], v[160:163], v[212:215], v[122:125]
	v_mfma_f32_16x16x32_bf16 v[110:113], v[152:155], v[220:223], v[110:113]
	v_mfma_f32_16x16x32_bf16 v[106:109], v[160:163], v[220:223], v[106:109]
	v_mfma_f32_16x16x32_bf16 v[94:97], v[152:155], v[228:231], v[94:97]
	v_mfma_f32_16x16x32_bf16 v[90:93], v[160:163], v[228:231], v[90:93]
	v_mfma_f32_16x16x32_bf16 v[78:81], v[152:155], v[236:239], v[78:81]
	v_mfma_f32_16x16x32_bf16 v[74:77], v[160:163], v[236:239], v[74:77]
	s_setprio 0
	s_setprio 1
	v_mfma_f32_16x16x32_bf16 v[118:121], v[190:193], v[208:211], v[118:121]
	v_mfma_f32_16x16x32_bf16 v[114:117], v[200:203], v[208:211], v[114:117]
	v_mfma_f32_16x16x32_bf16 v[102:105], v[190:193], v[216:219], v[102:105]
	v_mfma_f32_16x16x32_bf16 v[98:101], v[200:203], v[216:219], v[98:101]
	v_mfma_f32_16x16x32_bf16 v[86:89], v[190:193], v[224:227], v[86:89]
	v_mfma_f32_16x16x32_bf16 v[82:85], v[200:203], v[224:227], v[82:85]
	v_mfma_f32_16x16x32_bf16 v[70:73], v[190:193], v[232:235], v[70:73]
	v_mfma_f32_16x16x32_bf16 v[66:69], v[200:203], v[232:235], v[66:69]
	v_mfma_f32_16x16x32_bf16 v[118:121], v[194:197], v[212:215], v[118:121]
	v_mfma_f32_16x16x32_bf16 v[114:117], v[204:207], v[212:215], v[114:117]
	v_mfma_f32_16x16x32_bf16 v[102:105], v[194:197], v[220:223], v[102:105]
	v_mfma_f32_16x16x32_bf16 v[98:101], v[204:207], v[220:223], v[98:101]
	v_mfma_f32_16x16x32_bf16 v[86:89], v[194:197], v[228:231], v[86:89]
	v_mfma_f32_16x16x32_bf16 v[82:85], v[204:207], v[228:231], v[82:85]
	v_mfma_f32_16x16x32_bf16 v[70:73], v[194:197], v[236:239], v[70:73]
	v_mfma_f32_16x16x32_bf16 v[66:69], v[204:207], v[236:239], v[66:69]
	s_setprio 0
	s_barrier
	s_add_i32 s38, s58, s29
	s_mov_b32 m0, s38
	ds_read_b128 v[208:211], v183 offset:16384
	ds_read_b128 v[212:215], v183 offset:17408
	ds_read_b128 v[216:219], v183 offset:18432
	ds_read_b128 v[220:223], v183 offset:19456
	ds_read_b128 v[224:227], v183 offset:20480
	ds_read_b128 v[228:231], v183 offset:21504
	ds_read_b128 v[232:235], v183 offset:22528
	ds_read_b128 v[236:239], v183 offset:23552
	global_load_lds_dwordx4 v132, s[34:35]
	s_add_i32 m0, s38, 0x2000
	s_add_u32 s64, s34, 0x80000
	s_addc_u32 s65, s35, 0
	s_add_i32 s38, s59, s29
	global_load_lds_dwordx4 v136, s[34:35]
	s_mov_b32 m0, s38
	s_nop 0
	global_load_lds_dwordx4 v132, s[64:65]
	s_add_i32 m0, s38, 0x2000
	s_nop 0
	global_load_lds_dwordx4 v136, s[64:65]
	s_mov_b32 m0, s42
	s_nop 0
	s_mov_b64 s[98:99], s[36:37]
	global_load_lds_dwordx4 v130, s[36:37]
	s_mov_b32 m0, s43
	s_nop 0
	global_load_lds_dwordx4 v134, s[36:37]
	s_waitcnt vmcnt(8)
	s_waitcnt lgkmcnt(0)
	s_barrier
	s_setprio 1
	s_waitcnt lgkmcnt(0)
	v_mfma_f32_16x16x32_bf16 v[62:65], v[148:151], v[208:211], v[62:65]
	v_mfma_f32_16x16x32_bf16 v[50:53], v[156:159], v[208:211], v[50:53]
	v_mfma_f32_16x16x32_bf16 v[38:41], v[148:151], v[216:219], v[38:41]
	v_mfma_f32_16x16x32_bf16 v[34:37], v[156:159], v[216:219], v[34:37]
	v_mfma_f32_16x16x32_bf16 v[22:25], v[148:151], v[224:227], v[22:25]
	v_mfma_f32_16x16x32_bf16 v[18:21], v[156:159], v[224:227], v[18:21]
	v_mfma_f32_16x16x32_bf16 v[6:9], v[148:151], v[232:235], v[6:9]
	v_mfma_f32_16x16x32_bf16 v[2:5], v[156:159], v[232:235], v[2:5]
	v_mfma_f32_16x16x32_bf16 v[62:65], v[152:155], v[212:215], v[62:65]
	v_mfma_f32_16x16x32_bf16 v[50:53], v[160:163], v[212:215], v[50:53]
	v_mfma_f32_16x16x32_bf16 v[38:41], v[152:155], v[220:223], v[38:41]
	v_mfma_f32_16x16x32_bf16 v[34:37], v[160:163], v[220:223], v[34:37]
	v_mfma_f32_16x16x32_bf16 v[22:25], v[152:155], v[228:231], v[22:25]
	v_mfma_f32_16x16x32_bf16 v[18:21], v[160:163], v[228:231], v[18:21]
	v_mfma_f32_16x16x32_bf16 v[6:9], v[152:155], v[236:239], v[6:9]
	v_mfma_f32_16x16x32_bf16 v[2:5], v[160:163], v[236:239], v[2:5]
	s_setprio 0
	s_setprio 1
	v_mfma_f32_16x16x32_bf16 v[58:61], v[190:193], v[208:211], v[58:61]
	v_mfma_f32_16x16x32_bf16 v[54:57], v[200:203], v[208:211], v[54:57]
	v_mfma_f32_16x16x32_bf16 v[46:49], v[190:193], v[216:219], v[46:49]
	v_mfma_f32_16x16x32_bf16 v[42:45], v[200:203], v[216:219], v[42:45]
	v_mfma_f32_16x16x32_bf16 v[30:33], v[190:193], v[224:227], v[30:33]
	v_mfma_f32_16x16x32_bf16 v[26:29], v[200:203], v[224:227], v[26:29]
	v_mfma_f32_16x16x32_bf16 v[14:17], v[190:193], v[232:235], v[14:17]
	v_mfma_f32_16x16x32_bf16 v[10:13], v[200:203], v[232:235], v[10:13]
	v_mfma_f32_16x16x32_bf16 v[58:61], v[194:197], v[212:215], v[58:61]
	v_mfma_f32_16x16x32_bf16 v[54:57], v[204:207], v[212:215], v[54:57]
	v_mfma_f32_16x16x32_bf16 v[46:49], v[194:197], v[220:223], v[46:49]
	v_mfma_f32_16x16x32_bf16 v[42:45], v[204:207], v[220:223], v[42:45]
	v_mfma_f32_16x16x32_bf16 v[30:33], v[194:197], v[228:231], v[30:33]
	v_mfma_f32_16x16x32_bf16 v[26:29], v[204:207], v[228:231], v[26:29]
	v_mfma_f32_16x16x32_bf16 v[14:17], v[194:197], v[236:239], v[14:17]
	v_mfma_f32_16x16x32_bf16 v[10:13], v[204:207], v[236:239], v[10:13]
	s_setprio 0
	s_barrier
; #define PG8_STAGE(bufoff, gbase, voff) do { _Pragma("unroll") for (int _i = 0; _i < 2; ++_i) \
;         __builtin_amdgcn_global_load_lds((const unsigned*)((const char*)(gbase) + (voff)[_i]), (LAS unsigned*)(lds + (bufoff) + ldsw + _i * 8192), 16, 0, 0); } while (0)
; #define PG8_LDA(dst, b, h) do { if constexpr (F8) { _Pragma("unroll") for (int m = 0; m < 4; ++m) dst##8[m] = PG8_LD8(lds, PG8_SA(b, h) + aoff + m * 2048); } \
;         else { _Pragma("unroll") for (int m = 0; m < 4; ++m) _Pragma("unroll") for (int k = 0; k < 2; ++k) dst[m][k] = *(const LAS bf16x8*)(lds + PG8_SA(b, h) + aoff + m * 2048 + k * 1024); } } while (0)
; #define PG8_LDB(dst, b, h) do { if constexpr (F8) { _Pragma("unroll") for (int n = 0; n < 2; ++n) dst##8[n] = PG8_LD8(ldsB, PG8_SBR(b, h) + boff + n * 2048); } \
;         else { _Pragma("unroll") for (int n = 0; n < 2; ++n) _Pragma("unroll") for (int k = 0; k < 2; ++k) dst[n][k] = *(const LAS bf16x8*)(ldsB + PG8_SBR(b, h) + boff + n * 2048 + k * 1024); } } while (0)
; #define PG8_WAIT_V(n) asm volatile("s_waitcnt vmcnt(" #n ")" ::: "memory")
; #define PG8_WAIT_L(n) asm volatile("s_waitcnt lgkmcnt(" #n ")" ::: "memory")
; #define PG8_BAR __builtin_amdgcn_s_barrier()
; #define PG8_SCHED __builtin_amdgcn_sched_barrier(0)
; template <bool GATHER, bool F8, class Epi, class Sched>
; __device__ __forceinline__ void gemm_phase(LAS unsigned char* lds, const int nt, const unsigned lda, const unsigned ldb, const Sched& S, const Epi& E) {
;     ...
;             PG8_LDB(B0, 1, 0); PG8_LDB(B1, 1, 1); PG8_SCHED; PG8_LDA(At, 1, 0); PG8_STAGE(PG8_SA(0, 1), a2 + hA, w1);
;             PG8_WAIT_V(8); PG8_WAIT_L(0); PG8_BAR; PG8_MMA(0, 0, At, B0); PG8_MMA(0, 1, At, B1); PG8_BAR; PG8_SCHED;
;             PG8_LDA(At, 1, 1); PG8_STAGE(PG8_SB(1, 0), b3, voffB); PG8_STAGE(PG8_SB(1, 1), b3 + hB, voffB); PG8_STAGE(PG8_SA(1, 0), a3, w0);
;             PG8_WAIT_V(8); PG8_WAIT_L(0); PG8_BAR; PG8_MMA(1, 0, At, B0); PG8_MMA(1, 1, At, B1); PG8_BAR; PG8_SCHED;
;         }
;         if (wr == 0) PG8_BAR;
	s_add_i32 s38, 0, 0x18000
	v_add_u32_e32 v138, s38, v178
	s_add_i32 s64, 0, 0x1c000
	ds_read_b128 v[148:151], v138
	ds_read_b128 v[152:155], v138 offset:1024
	ds_read_b128 v[156:159], v138 offset:2048
	ds_read_b128 v[160:163], v138 offset:3072
	v_add_u32_e32 v138, s64, v178
	ds_read_b128 v[190:193], v138
	ds_read_b128 v[194:197], v138 offset:1024
	ds_read_b128 v[200:203], v138 offset:2048
	ds_read_b128 v[204:207], v138 offset:3072
	s_add_u32 s36, s36, 0x80000
	s_addc_u32 s37, s37, 0
	s_mov_b32 m0, s44
	ds_read_b128 v[208:211], v183 offset:32768
	ds_read_b128 v[212:215], v183 offset:33792
	ds_read_b128 v[216:219], v183 offset:34816
	ds_read_b128 v[220:223], v183 offset:35840
	ds_read_b128 v[224:227], v183 offset:36864
	ds_read_b128 v[228:231], v183 offset:37888
	ds_read_b128 v[232:235], v183 offset:38912
	ds_read_b128 v[236:239], v183 offset:39936
	global_load_lds_dwordx4 v130, s[36:37]
	s_mov_b32 m0, s45
	s_nop 0
	global_load_lds_dwordx4 v134, s[36:37]
	s_waitcnt vmcnt(8)
	s_waitcnt lgkmcnt(0)
	s_barrier
	s_setprio 1
	s_waitcnt lgkmcnt(0)
	v_mfma_f32_16x16x32_bf16 v[126:129], v[148:151], v[208:211], v[126:129]
	v_mfma_f32_16x16x32_bf16 v[122:125], v[156:159], v[208:211], v[122:125]
	v_mfma_f32_16x16x32_bf16 v[110:113], v[148:151], v[216:219], v[110:113]
	v_mfma_f32_16x16x32_bf16 v[106:109], v[156:159], v[216:219], v[106:109]
	v_mfma_f32_16x16x32_bf16 v[94:97], v[148:151], v[224:227], v[94:97]
	v_mfma_f32_16x16x32_bf16 v[90:93], v[156:159], v[224:227], v[90:93]
	v_mfma_f32_16x16x32_bf16 v[78:81], v[148:151], v[232:235], v[78:81]
	v_mfma_f32_16x16x32_bf16 v[74:77], v[156:159], v[232:235], v[74:77]
	v_mfma_f32_16x16x32_bf16 v[126:129], v[152:155], v[212:215], v[126:129]
	v_mfma_f32_16x16x32_bf16 v[122:125], v[160:163], v[212:215], v[122:125]
	v_mfma_f32_16x16x32_bf16 v[110:113], v[152:155], v[220:223], v[110:113]
	v_mfma_f32_16x16x32_bf16 v[106:109], v[160:163], v[220:223], v[106:109]
	v_mfma_f32_16x16x32_bf16 v[94:97], v[152:155], v[228:231], v[94:97]
	v_mfma_f32_16x16x32_bf16 v[90:93], v[160:163], v[228:231], v[90:93]
	v_mfma_f32_16x16x32_bf16 v[78:81], v[152:155], v[236:239], v[78:81]
	v_mfma_f32_16x16x32_bf16 v[74:77], v[160:163], v[236:239], v[74:77]
	s_setprio 0
	s_setprio 1
	v_mfma_f32_16x16x32_bf16 v[118:121], v[190:193], v[208:211], v[118:121]
	v_mfma_f32_16x16x32_bf16 v[114:117], v[200:203], v[208:211], v[114:117]
	v_mfma_f32_16x16x32_bf16 v[102:105], v[190:193], v[216:219], v[102:105]
	v_mfma_f32_16x16x32_bf16 v[98:101], v[200:203], v[216:219], v[98:101]
	v_mfma_f32_16x16x32_bf16 v[86:89], v[190:193], v[224:227], v[86:89]
	v_mfma_f32_16x16x32_bf16 v[82:85], v[200:203], v[224:227], v[82:85]
	v_mfma_f32_16x16x32_bf16 v[70:73], v[190:193], v[232:235], v[70:73]
	v_mfma_f32_16x16x32_bf16 v[66:69], v[200:203], v[232:235], v[66:69]
	v_mfma_f32_16x16x32_bf16 v[118:121], v[194:197], v[212:215], v[118:121]
	v_mfma_f32_16x16x32_bf16 v[114:117], v[204:207], v[212:215], v[114:117]
	v_mfma_f32_16x16x32_bf16 v[102:105], v[194:197], v[220:223], v[102:105]
	v_mfma_f32_16x16x32_bf16 v[98:101], v[204:207], v[220:223], v[98:101]
	v_mfma_f32_16x16x32_bf16 v[86:89], v[194:197], v[228:231], v[86:89]
	v_mfma_f32_16x16x32_bf16 v[82:85], v[204:207], v[228:231], v[82:85]
	v_mfma_f32_16x16x32_bf16 v[70:73], v[194:197], v[236:239], v[70:73]
	v_mfma_f32_16x16x32_bf16 v[66:69], v[204:207], v[236:239], v[66:69]
	s_setprio 0
	s_barrier
	s_add_i32 s36, s38, s29
	s_add_i32 m0, s36, 0xffffff80
	ds_read_b128 v[208:211], v183 offset:49152
	ds_read_b128 v[212:215], v183 offset:50176
	ds_read_b128 v[216:219], v183 offset:51200
	ds_read_b128 v[220:223], v183 offset:52224
	ds_read_b128 v[224:227], v183 offset:53248
	ds_read_b128 v[228:231], v183 offset:54272
	ds_read_b128 v[232:235], v183 offset:55296
	ds_read_b128 v[236:239], v183 offset:56320
	global_load_lds_dwordx4 v132, s[34:35] offset:128
	s_add_i32 m0, s36, 0x1f80
	s_add_i32 s36, s64, s29
	global_load_lds_dwordx4 v136, s[34:35] offset:128
	s_add_u32 s34, s34, 0x80080
	s_addc_u32 s35, s35, 0
	s_mov_b32 m0, s36
	s_nop 0
	global_load_lds_dwordx4 v132, s[34:35]
	s_add_i32 m0, s36, 0x2000
	s_nop 0
	global_load_lds_dwordx4 v136, s[34:35]
	s_add_i32 m0, s46, 0xffffff80
	s_nop 0
	global_load_lds_dwordx4 v130, s[98:99] offset:128
	s_add_i32 m0, s47, 0xffffff80
	s_nop 0
	global_load_lds_dwordx4 v134, s[98:99] offset:128
	s_waitcnt vmcnt(8)
	s_waitcnt lgkmcnt(0)
	s_barrier
	s_setprio 1
	s_waitcnt lgkmcnt(0)
	v_mfma_f32_16x16x32_bf16 v[62:65], v[148:151], v[208:211], v[62:65]
	v_mfma_f32_16x16x32_bf16 v[50:53], v[156:159], v[208:211], v[50:53]
	v_mfma_f32_16x16x32_bf16 v[38:41], v[148:151], v[216:219], v[38:41]
	v_mfma_f32_16x16x32_bf16 v[34:37], v[156:159], v[216:219], v[34:37]
	v_mfma_f32_16x16x32_bf16 v[22:25], v[148:151], v[224:227], v[22:25]
	v_mfma_f32_16x16x32_bf16 v[18:21], v[156:159], v[224:227], v[18:21]
	v_mfma_f32_16x16x32_bf16 v[6:9], v[148:151], v[232:235], v[6:9]
	v_mfma_f32_16x16x32_bf16 v[2:5], v[156:159], v[232:235], v[2:5]
	v_mfma_f32_16x16x32_bf16 v[62:65], v[152:155], v[212:215], v[62:65]
	v_mfma_f32_16x16x32_bf16 v[50:53], v[160:163], v[212:215], v[50:53]
	v_mfma_f32_16x16x32_bf16 v[38:41], v[152:155], v[220:223], v[38:41]
	v_mfma_f32_16x16x32_bf16 v[34:37], v[160:163], v[220:223], v[34:37]
	v_mfma_f32_16x16x32_bf16 v[22:25], v[152:155], v[228:231], v[22:25]
	v_mfma_f32_16x16x32_bf16 v[18:21], v[160:163], v[228:231], v[18:21]
	v_mfma_f32_16x16x32_bf16 v[6:9], v[152:155], v[236:239], v[6:9]
	v_mfma_f32_16x16x32_bf16 v[2:5], v[160:163], v[236:239], v[2:5]
	s_setprio 0
	s_setprio 1
	v_mfma_f32_16x16x32_bf16 v[58:61], v[190:193], v[208:211], v[58:61]
	v_mfma_f32_16x16x32_bf16 v[54:57], v[200:203], v[208:211], v[54:57]
	v_mfma_f32_16x16x32_bf16 v[46:49], v[190:193], v[216:219], v[46:49]
	v_mfma_f32_16x16x32_bf16 v[42:45], v[200:203], v[216:219], v[42:45]
	v_mfma_f32_16x16x32_bf16 v[30:33], v[190:193], v[224:227], v[30:33]
	v_mfma_f32_16x16x32_bf16 v[26:29], v[200:203], v[224:227], v[26:29]
	v_mfma_f32_16x16x32_bf16 v[14:17], v[190:193], v[232:235], v[14:17]
	v_mfma_f32_16x16x32_bf16 v[10:13], v[200:203], v[232:235], v[10:13]
	v_mfma_f32_16x16x32_bf16 v[58:61], v[194:197], v[212:215], v[58:61]
	v_mfma_f32_16x16x32_bf16 v[54:57], v[204:207], v[212:215], v[54:57]
	v_mfma_f32_16x16x32_bf16 v[46:49], v[194:197], v[220:223], v[46:49]
	v_mfma_f32_16x16x32_bf16 v[42:45], v[204:207], v[220:223], v[42:45]
	v_mfma_f32_16x16x32_bf16 v[30:33], v[194:197], v[228:231], v[30:33]
	v_mfma_f32_16x16x32_bf16 v[26:29], v[204:207], v[228:231], v[26:29]
	v_mfma_f32_16x16x32_bf16 v[14:17], v[194:197], v[236:239], v[14:17]
	v_mfma_f32_16x16x32_bf16 v[10:13], v[204:207], v[236:239], v[10:13]
	s_setprio 0
	s_barrier
	s_add_i32 s33, s33, 2
	s_add_u32 s10, s10, 0x100
	s_addc_u32 s11, s11, 0
	s_add_u32 s14, s14, 0x100
	s_addc_u32 s27, s27, 0
	s_cmp_gt_u32 s33, 29
	s_cbranch_scc0 .LBB0_247
	s_and_b64 vcc, exec, s[20:21]
	s_cbranch_vccz .LBB0_251
	s_barrier
	v_lshl_add_u32 v148, s26, 8, v177
	s_cmp_gt_i32 s28, 11
	s_mov_b64 s[10:11], -1
	s_cbranch_scc1 .LBB0_252

; #define PG8_STAGE(bufoff, gbase, voff) do { _Pragma("unroll") for (int _i = 0; _i < 2; ++_i) \
;         __builtin_amdgcn_global_load_lds((const unsigned*)((const char*)(gbase) + (voff)[_i]), (LAS unsigned*)(lds + (bufoff) + ldsw + _i * 8192), 16, 0, 0); } while (0)
; #define PG8_LDA(dst, b, h) do { if constexpr (F8) { _Pragma("unroll") for (int m = 0; m < 4; ++m) dst##8[m] = PG8_LD8(lds, PG8_SA(b, h) + aoff + m * 2048); } \
;         else { _Pragma("unroll") for (int m = 0; m < 4; ++m) _Pragma("unroll") for (int k = 0; k < 2; ++k) dst[m][k] = *(const LAS bf16x8*)(lds + PG8_SA(b, h) + aoff + m * 2048 + k * 1024); } } while (0)
; #define PG8_WAIT_V(n) asm volatile("s_waitcnt vmcnt(" #n ")" ::: "memory")
; #define PG8_WAIT_L(n) asm volatile("s_waitcnt lgkmcnt(" #n ")" ::: "memory")
; #define PG8_BAR __builtin_amdgcn_s_barrier()
; #define PG8_SCHED __builtin_amdgcn_sched_barrier(0)
; template <bool GATHER, bool F8, class Epi, class Sched>
; __device__ __forceinline__ void gemm_phase(LAS unsigned char* lds, const int nt, const unsigned lda, const unsigned ldb, const Sched& S, const Epi& E) {
;     ...
;         for (int t = 0; t < nt; t += 2) {
;             const bool last = (t == nt - 2);
;             const char* a1 = cA + (size_t)(t + 1) * kstep;
;             const char* a2 = last ? nA : cA + (size_t)(t + 2) * kstep; const char* b2 = last ? nB : cB + (size_t)(t + 2) * kstep;
;             const char* a3 = a2 + kstep; const char* b3 = b2 + kstep;
;             unsigned w0[2], w1[2];
;             if constexpr (GATHER) {
; #pragma unroll
;                 for (int i = 0; i < 2; ++i) { w0[i] = last ? vN0[i] : vA0[i]; w1[i] = last ? vN1[i] : vA1[i]; }
;             } else {
; #pragma unroll
;                 for (int i = 0; i < 2; ++i) { w0[i] = voffA[i]; w1[i] = voffA[i]; }
;             }
;             PG8_LDB(B0, 0, 0); PG8_LDB(B1, 0, 1); PG8_SCHED; PG8_LDA(At, 0, 0); PG8_STAGE(PG8_SA(1, 1), a1 + hA, vA1);
;             PG8_WAIT_V(8); PG8_WAIT_L(0); PG8_BAR; PG8_MMA(0, 0, At, B0); PG8_MMA(0, 1, At, B1); PG8_BAR; PG8_SCHED;
;             PG8_LDA(At, 0, 1); PG8_STAGE(PG8_SB(0, 0), b2, voffB); PG8_STAGE(PG8_SB(0, 1), b2 + hB, voffB); PG8_STAGE(PG8_SA(0, 0), a2, w0);
;             PG8_WAIT_V(8); PG8_WAIT_L(0); PG8_BAR; PG8_MMA(1, 0, At, B0); PG8_MMA(1, 1, At, B1); PG8_BAR; PG8_SCHED;
.LBB0_387:
	ds_read_b128 v[18:21], v1
	ds_read_b128 v[22:25], v1 offset:1024
	ds_read_b128 v[26:29], v1 offset:2048
	ds_read_b128 v[30:33], v1 offset:3072
	ds_read_b128 v[2:5], v1 offset:16384
	ds_read_b128 v[6:9], v1 offset:17408
	ds_read_b128 v[10:13], v1 offset:18432
	ds_read_b128 v[14:17], v1 offset:19456
	s_add_u32 s26, s24, 0xfffc0080
	s_addc_u32 s27, s25, -1
	s_cmp_eq_u32 s55, 12
	s_cselect_b32 s29, s1, s27
	s_cselect_b32 s28, s0, s26
	s_cselect_b32 s27, s21, s54
	s_cselect_b32 s26, s20, s30
	s_add_i32 m0, s23, 0xc000
	ds_read_b128 v[180:183], v191
	ds_read_b128 v[184:187], v191 offset:1024
	ds_read_b128 v[200:203], v191 offset:2048
	ds_read_b128 v[204:207], v191 offset:3072
	ds_read_b128 v[208:211], v191 offset:4096
	ds_read_b128 v[212:215], v191 offset:5120
	ds_read_b128 v[216:219], v191 offset:6144
	ds_read_b128 v[220:223], v191 offset:7168
	global_load_lds_dwordx4 v172, s[24:25]
	s_add_i32 m0, s23, 0xe000
	s_nop 0
	global_load_lds_dwordx4 v174, s[24:25]
	s_waitcnt vmcnt(8)
	s_waitcnt lgkmcnt(0)
	s_barrier
	s_setprio 1
	s_waitcnt lgkmcnt(0)
	v_mfma_scale_f32_16x16x128_f8f6f4 v[158:161], v[18:25], v[180:187], v[158:161], v192, v192 op_sel_hi:[0,0,0]
	v_mfma_scale_f32_16x16x128_f8f6f4 v[150:153], v[26:33], v[180:187], v[150:153], v192, v192 op_sel_hi:[0,0,0]
	v_mfma_scale_f32_16x16x128_f8f6f4 v[142:145], v[18:25], v[200:207], v[142:145], v192, v192 op_sel_hi:[0,0,0]
	v_mfma_scale_f32_16x16x128_f8f6f4 v[134:137], v[26:33], v[200:207], v[134:137], v192, v192 op_sel_hi:[0,0,0]
	v_mfma_scale_f32_16x16x128_f8f6f4 v[126:129], v[18:25], v[208:215], v[126:129], v192, v192 op_sel_hi:[0,0,0]
	v_mfma_scale_f32_16x16x128_f8f6f4 v[118:121], v[26:33], v[208:215], v[118:121], v192, v192 op_sel_hi:[0,0,0]
	v_mfma_scale_f32_16x16x128_f8f6f4 v[110:113], v[18:25], v[216:223], v[110:113], v192, v192 op_sel_hi:[0,0,0]
	v_mfma_scale_f32_16x16x128_f8f6f4 v[102:105], v[26:33], v[216:223], v[102:105], v192, v192 op_sel_hi:[0,0,0]
	s_setprio 0
	s_setprio 1
	v_mfma_scale_f32_16x16x128_f8f6f4 v[154:157], v[2:9], v[180:187], v[154:157], v192, v192 op_sel_hi:[0,0,0]
	v_mfma_scale_f32_16x16x128_f8f6f4 v[146:149], v[10:17], v[180:187], v[146:149], v192, v192 op_sel_hi:[0,0,0]
	v_mfma_scale_f32_16x16x128_f8f6f4 v[138:141], v[2:9], v[200:207], v[138:141], v192, v192 op_sel_hi:[0,0,0]
	v_mfma_scale_f32_16x16x128_f8f6f4 v[130:133], v[10:17], v[200:207], v[130:133], v192, v192 op_sel_hi:[0,0,0]
	v_mfma_scale_f32_16x16x128_f8f6f4 v[122:125], v[2:9], v[208:215], v[122:125], v192, v192 op_sel_hi:[0,0,0]
	v_mfma_scale_f32_16x16x128_f8f6f4 v[114:117], v[10:17], v[208:215], v[114:117], v192, v192 op_sel_hi:[0,0,0]
	v_mfma_scale_f32_16x16x128_f8f6f4 v[106:109], v[2:9], v[216:223], v[106:109], v192, v192 op_sel_hi:[0,0,0]
	v_mfma_scale_f32_16x16x128_f8f6f4 v[98:101], v[10:17], v[216:223], v[98:101], v192, v192 op_sel_hi:[0,0,0]
	s_setprio 0
	s_barrier
	s_mov_b32 m0, s38
	s_add_u32 s56, s26, 0x40000
	ds_read_b128 v[200:203], v191 offset:16384
	ds_read_b128 v[204:207], v191 offset:17408
	ds_read_b128 v[208:211], v191 offset:18432
	ds_read_b128 v[212:215], v191 offset:19456
	ds_read_b128 v[216:219], v191 offset:20480
	ds_read_b128 v[220:223], v191 offset:21504
	ds_read_b128 v[224:227], v191 offset:22528
	ds_read_b128 v[228:231], v191 offset:23552
	global_load_lds_dwordx4 v166, s[26:27]
	s_mov_b32 m0, s39
	s_addc_u32 s57, s27, 0
	global_load_lds_dwordx4 v162, s[26:27]
	s_mov_b32 m0, s40
	s_nop 0
	global_load_lds_dwordx4 v166, s[56:57]
	s_mov_b32 m0, s41
	s_nop 0
	global_load_lds_dwordx4 v162, s[56:57]
	s_mov_b32 m0, s23
	s_nop 0
	s_mov_b64 s[98:99], s[28:29]
	global_load_lds_dwordx4 v168, s[28:29]
	s_mov_b32 m0, s42
	s_nop 0
	global_load_lds_dwordx4 v164, s[28:29]
	s_waitcnt vmcnt(8)
	s_waitcnt lgkmcnt(0)
	s_barrier
	s_setprio 1
	s_waitcnt lgkmcnt(0)
	v_mfma_scale_f32_16x16x128_f8f6f4 v[86:89], v[18:25], v[200:207], v[86:89], v192, v192 op_sel_hi:[0,0,0]
	v_mfma_scale_f32_16x16x128_f8f6f4 v[78:81], v[26:33], v[200:207], v[78:81], v192, v192 op_sel_hi:[0,0,0]
	v_mfma_scale_f32_16x16x128_f8f6f4 v[70:73], v[18:25], v[208:215], v[70:73], v192, v192 op_sel_hi:[0,0,0]
	v_mfma_scale_f32_16x16x128_f8f6f4 v[62:65], v[26:33], v[208:215], v[62:65], v192, v192 op_sel_hi:[0,0,0]
	v_mfma_scale_f32_16x16x128_f8f6f4 v[54:57], v[18:25], v[216:223], v[54:57], v192, v192 op_sel_hi:[0,0,0]
	v_mfma_scale_f32_16x16x128_f8f6f4 v[46:49], v[26:33], v[216:223], v[46:49], v192, v192 op_sel_hi:[0,0,0]
	v_mfma_scale_f32_16x16x128_f8f6f4 v[38:41], v[18:25], v[224:231], v[38:41], v192, v192 op_sel_hi:[0,0,0]
	v_mfma_scale_f32_16x16x128_f8f6f4 v[34:37], v[26:33], v[224:231], v[34:37], v192, v192 op_sel_hi:[0,0,0]
	s_setprio 0
	s_setprio 1
	v_mfma_scale_f32_16x16x128_f8f6f4 v[94:97], v[2:9], v[200:207], v[94:97], v192, v192 op_sel_hi:[0,0,0]
	v_mfma_scale_f32_16x16x128_f8f6f4 v[90:93], v[10:17], v[200:207], v[90:93], v192, v192 op_sel_hi:[0,0,0]
	v_mfma_scale_f32_16x16x128_f8f6f4 v[82:85], v[2:9], v[208:215], v[82:85], v192, v192 op_sel_hi:[0,0,0]
	v_mfma_scale_f32_16x16x128_f8f6f4 v[74:77], v[10:17], v[208:215], v[74:77], v192, v192 op_sel_hi:[0,0,0]
	v_mfma_scale_f32_16x16x128_f8f6f4 v[66:69], v[2:9], v[216:223], v[66:69], v192, v192 op_sel_hi:[0,0,0]
	v_mfma_scale_f32_16x16x128_f8f6f4 v[58:61], v[10:17], v[216:223], v[58:61], v192, v192 op_sel_hi:[0,0,0]
	v_mfma_scale_f32_16x16x128_f8f6f4 v[50:53], v[2:9], v[224:231], v[50:53], v192, v192 op_sel_hi:[0,0,0]
	v_mfma_scale_f32_16x16x128_f8f6f4 v[42:45], v[10:17], v[224:231], v[42:45], v192, v192 op_sel_hi:[0,0,0]
	s_setprio 0
	s_barrier
; #define PG8_STAGE(bufoff, gbase, voff) do { _Pragma("unroll") for (int _i = 0; _i < 2; ++_i) \
;         __builtin_amdgcn_global_load_lds((const unsigned*)((const char*)(gbase) + (voff)[_i]), (LAS unsigned*)(lds + (bufoff) + ldsw + _i * 8192), 16, 0, 0); } while (0)
; #define PG8_LDA(dst, b, h) do { if constexpr (F8) { _Pragma("unroll") for (int m = 0; m < 4; ++m) dst##8[m] = PG8_LD8(lds, PG8_SA(b, h) + aoff + m * 2048); } \
;         else { _Pragma("unroll") for (int m = 0; m < 4; ++m) _Pragma("unroll") for (int k = 0; k < 2; ++k) dst[m][k] = *(const LAS bf16x8*)(lds + PG8_SA(b, h) + aoff + m * 2048 + k * 1024); } } while (0)
; #define PG8_LDB(dst, b, h) do { if constexpr (F8) { _Pragma("unroll") for (int n = 0; n < 2; ++n) dst##8[n] = PG8_LD8(ldsB, PG8_SBR(b, h) + boff + n * 2048); } \
;         else { _Pragma("unroll") for (int n = 0; n < 2; ++n) _Pragma("unroll") for (int k = 0; k < 2; ++k) dst[n][k] = *(const LAS bf16x8*)(ldsB + PG8_SBR(b, h) + boff + n * 2048 + k * 1024); } } while (0)
; #define PG8_WAIT_V(n) asm volatile("s_waitcnt vmcnt(" #n ")" ::: "memory")
; #define PG8_WAIT_L(n) asm volatile("s_waitcnt lgkmcnt(" #n ")" ::: "memory")
; #define PG8_BAR __builtin_amdgcn_s_barrier()
; #define PG8_SCHED __builtin_amdgcn_sched_barrier(0)
; template <bool GATHER, bool F8, class Epi, class Sched>
; __device__ __forceinline__ void gemm_phase(LAS unsigned char* lds, const int nt, const unsigned lda, const unsigned ldb, const Sched& S, const Epi& E) {
;     ...
;             PG8_LDB(B0, 1, 0); PG8_LDB(B1, 1, 1); PG8_SCHED; PG8_LDA(At, 1, 0); PG8_STAGE(PG8_SA(0, 1), a2 + hA, w1);
;             PG8_WAIT_V(8); PG8_WAIT_L(0); PG8_BAR; PG8_MMA(0, 0, At, B0); PG8_MMA(0, 1, At, B1); PG8_BAR; PG8_SCHED;
;             PG8_LDA(At, 1, 1); PG8_STAGE(PG8_SB(1, 0), b3, voffB); PG8_STAGE(PG8_SB(1, 1), b3 + hB, voffB); PG8_STAGE(PG8_SA(1, 0), a3, w0);
;             PG8_WAIT_V(8); PG8_WAIT_L(0); PG8_BAR; PG8_MMA(1, 0, At, B0); PG8_MMA(1, 1, At, B1); PG8_BAR; PG8_SCHED;
;         }
	ds_read_b128 v[2:5], v1 offset:32768
	ds_read_b128 v[6:9], v1 offset:33792
	ds_read_b128 v[10:13], v1 offset:34816
	ds_read_b128 v[14:17], v1 offset:35840
	ds_read_b128 v[18:21], v1 offset:49152
	ds_read_b128 v[22:25], v1 offset:50176
	ds_read_b128 v[26:29], v1 offset:51200
	ds_read_b128 v[30:33], v1 offset:52224
	s_add_u32 s28, s28, 0x40000
	s_addc_u32 s29, s29, 0
	s_mov_b32 m0, s43
	ds_read_b128 v[200:203], v191 offset:32768
	ds_read_b128 v[204:207], v191 offset:33792
	ds_read_b128 v[208:211], v191 offset:34816
	ds_read_b128 v[212:215], v191 offset:35840
	ds_read_b128 v[216:219], v191 offset:36864
	ds_read_b128 v[220:223], v191 offset:37888
	ds_read_b128 v[224:227], v191 offset:38912
	ds_read_b128 v[228:231], v191 offset:39936
	global_load_lds_dwordx4 v168, s[28:29]
	s_mov_b32 m0, s44
	s_nop 0
	global_load_lds_dwordx4 v164, s[28:29]
	s_waitcnt vmcnt(8)
	s_waitcnt lgkmcnt(0)
	s_barrier
	s_setprio 1
	s_waitcnt lgkmcnt(0)
	v_mfma_scale_f32_16x16x128_f8f6f4 v[158:161], v[2:9], v[200:207], v[158:161], v192, v192 op_sel_hi:[0,0,0]
	v_mfma_scale_f32_16x16x128_f8f6f4 v[150:153], v[10:17], v[200:207], v[150:153], v192, v192 op_sel_hi:[0,0,0]
	v_mfma_scale_f32_16x16x128_f8f6f4 v[142:145], v[2:9], v[208:215], v[142:145], v192, v192 op_sel_hi:[0,0,0]
	v_mfma_scale_f32_16x16x128_f8f6f4 v[134:137], v[10:17], v[208:215], v[134:137], v192, v192 op_sel_hi:[0,0,0]
	v_mfma_scale_f32_16x16x128_f8f6f4 v[126:129], v[2:9], v[216:223], v[126:129], v192, v192 op_sel_hi:[0,0,0]
	v_mfma_scale_f32_16x16x128_f8f6f4 v[118:121], v[10:17], v[216:223], v[118:121], v192, v192 op_sel_hi:[0,0,0]
	v_mfma_scale_f32_16x16x128_f8f6f4 v[110:113], v[2:9], v[224:231], v[110:113], v192, v192 op_sel_hi:[0,0,0]
	v_mfma_scale_f32_16x16x128_f8f6f4 v[102:105], v[10:17], v[224:231], v[102:105], v192, v192 op_sel_hi:[0,0,0]
	s_setprio 0
	s_setprio 1
	v_mfma_scale_f32_16x16x128_f8f6f4 v[154:157], v[18:25], v[200:207], v[154:157], v192, v192 op_sel_hi:[0,0,0]
	v_mfma_scale_f32_16x16x128_f8f6f4 v[146:149], v[26:33], v[200:207], v[146:149], v192, v192 op_sel_hi:[0,0,0]
	v_mfma_scale_f32_16x16x128_f8f6f4 v[138:141], v[18:25], v[208:215], v[138:141], v192, v192 op_sel_hi:[0,0,0]
	v_mfma_scale_f32_16x16x128_f8f6f4 v[130:133], v[26:33], v[208:215], v[130:133], v192, v192 op_sel_hi:[0,0,0]
	v_mfma_scale_f32_16x16x128_f8f6f4 v[122:125], v[18:25], v[216:223], v[122:125], v192, v192 op_sel_hi:[0,0,0]
	v_mfma_scale_f32_16x16x128_f8f6f4 v[114:117], v[26:33], v[216:223], v[114:117], v192, v192 op_sel_hi:[0,0,0]
	v_mfma_scale_f32_16x16x128_f8f6f4 v[106:109], v[18:25], v[224:231], v[106:109], v192, v192 op_sel_hi:[0,0,0]
	v_mfma_scale_f32_16x16x128_f8f6f4 v[98:101], v[26:33], v[224:231], v[98:101], v192, v192 op_sel_hi:[0,0,0]
	s_setprio 0
	s_barrier
	s_add_i32 m0, s45, 0xffffff80
	ds_read_b128 v[200:203], v191 offset:49152
	ds_read_b128 v[204:207], v191 offset:50176
	ds_read_b128 v[208:211], v191 offset:51200
	ds_read_b128 v[212:215], v191 offset:52224
	ds_read_b128 v[216:219], v191 offset:53248
	ds_read_b128 v[220:223], v191 offset:54272
	ds_read_b128 v[224:227], v191 offset:55296
	ds_read_b128 v[228:231], v191 offset:56320
	global_load_lds_dwordx4 v166, s[26:27] offset:128
	s_add_i32 m0, s46, 0xffffff80
	s_nop 0
	global_load_lds_dwordx4 v162, s[26:27] offset:128
	s_add_u32 s26, s26, 0x40080
	s_addc_u32 s27, s27, 0
	s_mov_b32 m0, s49
	s_nop 0
	global_load_lds_dwordx4 v166, s[26:27]
	s_mov_b32 m0, s50
	s_nop 0
	global_load_lds_dwordx4 v162, s[26:27]
	s_add_i32 m0, s47, 0xffffff80
	s_nop 0
	global_load_lds_dwordx4 v168, s[98:99] offset:128
	s_add_i32 m0, s48, 0xffffff80
	s_nop 0
	global_load_lds_dwordx4 v164, s[98:99] offset:128
	s_waitcnt vmcnt(8)
	s_waitcnt lgkmcnt(0)
	s_barrier
	s_setprio 1
	s_waitcnt lgkmcnt(0)
	v_mfma_scale_f32_16x16x128_f8f6f4 v[86:89], v[2:9], v[200:207], v[86:89], v192, v192 op_sel_hi:[0,0,0]
	v_mfma_scale_f32_16x16x128_f8f6f4 v[78:81], v[10:17], v[200:207], v[78:81], v192, v192 op_sel_hi:[0,0,0]
	v_mfma_scale_f32_16x16x128_f8f6f4 v[70:73], v[2:9], v[208:215], v[70:73], v192, v192 op_sel_hi:[0,0,0]
	v_mfma_scale_f32_16x16x128_f8f6f4 v[62:65], v[10:17], v[208:215], v[62:65], v192, v192 op_sel_hi:[0,0,0]
	v_mfma_scale_f32_16x16x128_f8f6f4 v[54:57], v[2:9], v[216:223], v[54:57], v192, v192 op_sel_hi:[0,0,0]
	v_mfma_scale_f32_16x16x128_f8f6f4 v[46:49], v[10:17], v[216:223], v[46:49], v192, v192 op_sel_hi:[0,0,0]
	v_mfma_scale_f32_16x16x128_f8f6f4 v[38:41], v[2:9], v[224:231], v[38:41], v192, v192 op_sel_hi:[0,0,0]
	v_mfma_scale_f32_16x16x128_f8f6f4 v[34:37], v[10:17], v[224:231], v[34:37], v192, v192 op_sel_hi:[0,0,0]
	s_setprio 0
	s_setprio 1
	v_mfma_scale_f32_16x16x128_f8f6f4 v[94:97], v[18:25], v[200:207], v[94:97], v192, v192 op_sel_hi:[0,0,0]
	v_mfma_scale_f32_16x16x128_f8f6f4 v[90:93], v[26:33], v[200:207], v[90:93], v192, v192 op_sel_hi:[0,0,0]
	v_mfma_scale_f32_16x16x128_f8f6f4 v[82:85], v[18:25], v[208:215], v[82:85], v192, v192 op_sel_hi:[0,0,0]
	v_mfma_scale_f32_16x16x128_f8f6f4 v[74:77], v[26:33], v[208:215], v[74:77], v192, v192 op_sel_hi:[0,0,0]
	v_mfma_scale_f32_16x16x128_f8f6f4 v[66:69], v[18:25], v[216:223], v[66:69], v192, v192 op_sel_hi:[0,0,0]
	v_mfma_scale_f32_16x16x128_f8f6f4 v[58:61], v[26:33], v[216:223], v[58:61], v192, v192 op_sel_hi:[0,0,0]
	v_mfma_scale_f32_16x16x128_f8f6f4 v[50:53], v[18:25], v[224:231], v[50:53], v192, v192 op_sel_hi:[0,0,0]
	v_mfma_scale_f32_16x16x128_f8f6f4 v[42:45], v[26:33], v[224:231], v[42:45], v192, v192 op_sel_hi:[0,0,0]
	s_setprio 0
	s_barrier
	s_add_i32 s55, s55, 2
	s_add_u32 s24, s24, 0x100
	s_addc_u32 s25, s25, 0
	s_add_u32 s30, s30, 0x100
	s_addc_u32 s54, s54, 0
	s_cmp_gt_u32 s55, 13
	s_cbranch_scc0 .LBB0_387
	s_and_b64 vcc, exec, s[10:11]
	s_cbranch_vccz .LBB0_390
	s_barrier

; #define PG8_STAGE(bufoff, gbase, voff) do { _Pragma("unroll") for (int _i = 0; _i < 2; ++_i) \
;         __builtin_amdgcn_global_load_lds((const unsigned*)((const char*)(gbase) + (voff)[_i]), (LAS unsigned*)(lds + (bufoff) + ldsw + _i * 8192), 16, 0, 0); } while (0)
; #define PG8_LDA(dst, b, h) do { if constexpr (F8) { _Pragma("unroll") for (int m = 0; m < 4; ++m) dst##8[m] = PG8_LD8(lds, PG8_SA(b, h) + aoff + m * 2048); } \
;         else { _Pragma("unroll") for (int m = 0; m < 4; ++m) _Pragma("unroll") for (int k = 0; k < 2; ++k) dst[m][k] = *(const LAS bf16x8*)(lds + PG8_SA(b, h) + aoff + m * 2048 + k * 1024); } } while (0)
; #define PG8_WAIT_V(n) asm volatile("s_waitcnt vmcnt(" #n ")" ::: "memory")
; #define PG8_WAIT_L(n) asm volatile("s_waitcnt lgkmcnt(" #n ")" ::: "memory")
; #define PG8_BAR __builtin_amdgcn_s_barrier()
; #define PG8_SCHED __builtin_amdgcn_sched_barrier(0)
; template <bool GATHER, bool F8, class Epi, class Sched>
; __device__ __forceinline__ void gemm_phase(LAS unsigned char* lds, const int nt, const unsigned lda, const unsigned ldb, const Sched& S, const Epi& E) {
;     ...
;         for (int t = 0; t < nt; t += 2) {
;             const bool last = (t == nt - 2);
;             const char* a1 = cA + (size_t)(t + 1) * kstep;
;             const char* a2 = last ? nA : cA + (size_t)(t + 2) * kstep; const char* b2 = last ? nB : cB + (size_t)(t + 2) * kstep;
;             const char* a3 = a2 + kstep; const char* b3 = b2 + kstep;
;             unsigned w0[2], w1[2];
;             if constexpr (GATHER) {
; #pragma unroll
;                 for (int i = 0; i < 2; ++i) { w0[i] = last ? vN0[i] : vA0[i]; w1[i] = last ? vN1[i] : vA1[i]; }
;             } else {
; #pragma unroll
;                 for (int i = 0; i < 2; ++i) { w0[i] = voffA[i]; w1[i] = voffA[i]; }
;             }
;             PG8_LDB(B0, 0, 0); PG8_LDB(B1, 0, 1); PG8_SCHED; PG8_LDA(At, 0, 0); PG8_STAGE(PG8_SA(1, 1), a1 + hA, vA1);
;             PG8_WAIT_V(8); PG8_WAIT_L(0); PG8_BAR; PG8_MMA(0, 0, At, B0); PG8_MMA(0, 1, At, B1); PG8_BAR; PG8_SCHED;
;             PG8_LDA(At, 0, 1); PG8_STAGE(PG8_SB(0, 0), b2, voffB); PG8_STAGE(PG8_SB(0, 1), b2 + hB, voffB); PG8_STAGE(PG8_SA(0, 0), a2, w0);
;             PG8_WAIT_V(8); PG8_WAIT_L(0); PG8_BAR; PG8_MMA(1, 0, At, B0); PG8_MMA(1, 1, At, B1); PG8_BAR; PG8_SCHED;
.LBB0_891:
	v_add_u32_e32 v3, s47, v199
	ds_read_b128 v[38:41], v3
	ds_read_b128 v[42:45], v3 offset:1024
	ds_read_b128 v[70:73], v3 offset:2048
	ds_read_b128 v[74:77], v3 offset:3072
	v_add_u32_e32 v3, s48, v199
	ds_read_b128 v[102:105], v3
	ds_read_b128 v[106:109], v3 offset:1024
	ds_read_b128 v[134:137], v3 offset:2048
	ds_read_b128 v[138:141], v3 offset:3072
	s_add_u32 s28, s26, 0xfff80080
	s_addc_u32 s29, s27, -1
	s_cmp_eq_u32 s52, 12
	s_cselect_b32 s31, s1, s29
	s_cselect_b32 s30, s0, s28
	s_cselect_b32 s29, s23, s34
	s_cselect_b32 s28, s22, s25
	s_add_i32 m0, s40, 0xc000
	ds_read_b128 v[158:161], v217
	ds_read_b128 v[162:165], v217 offset:1024
	ds_read_b128 v[174:177], v217 offset:2048
	ds_read_b128 v[178:181], v217 offset:3072
	ds_read_b128 v[182:185], v217 offset:4096
	ds_read_b128 v[186:189], v217 offset:5120
	ds_read_b128 v[190:193], v217 offset:6144
	ds_read_b128 v[194:197], v217 offset:7168
	global_load_lds_dwordx4 v208, s[26:27]
	s_add_i32 m0, s40, 0xe000
	s_nop 0
	global_load_lds_dwordx4 v210, s[26:27]
	s_waitcnt vmcnt(8)
	s_waitcnt lgkmcnt(0)
	s_barrier
	s_setprio 1
	s_waitcnt lgkmcnt(0)
	v_mfma_f32_16x16x32_bf16 v[66:69], v[38:41], v[158:161], v[66:69]
	v_mfma_f32_16x16x32_bf16 v[62:65], v[70:73], v[158:161], v[62:65]
	v_mfma_f32_16x16x32_bf16 v[98:101], v[38:41], v[174:177], v[98:101]
	v_mfma_f32_16x16x32_bf16 v[94:97], v[70:73], v[174:177], v[94:97]
	v_mfma_f32_16x16x32_bf16 v[122:125], v[38:41], v[182:185], v[122:125]
	v_mfma_f32_16x16x32_bf16 v[118:121], v[70:73], v[182:185], v[118:121]
	v_mfma_f32_16x16x32_bf16 v[130:133], v[38:41], v[190:193], v[130:133]
	v_mfma_f32_16x16x32_bf16 v[126:129], v[70:73], v[190:193], v[126:129]
	v_mfma_f32_16x16x32_bf16 v[66:69], v[42:45], v[162:165], v[66:69]
	v_mfma_f32_16x16x32_bf16 v[62:65], v[74:77], v[162:165], v[62:65]
	v_mfma_f32_16x16x32_bf16 v[98:101], v[42:45], v[178:181], v[98:101]
	v_mfma_f32_16x16x32_bf16 v[94:97], v[74:77], v[178:181], v[94:97]
	v_mfma_f32_16x16x32_bf16 v[122:125], v[42:45], v[186:189], v[122:125]
	v_mfma_f32_16x16x32_bf16 v[118:121], v[74:77], v[186:189], v[118:121]
	v_mfma_f32_16x16x32_bf16 v[130:133], v[42:45], v[194:197], v[130:133]
	v_mfma_f32_16x16x32_bf16 v[126:129], v[74:77], v[194:197], v[126:129]
	s_setprio 0
	s_setprio 1
	v_mfma_f32_16x16x32_bf16 v[170:173], v[102:105], v[158:161], v[170:173]
	v_mfma_f32_16x16x32_bf16 v[154:157], v[102:105], v[174:177], v[154:157]
	v_mfma_f32_16x16x32_bf16 v[150:153], v[134:137], v[174:177], v[150:153]
	v_mfma_f32_16x16x32_bf16 v[146:149], v[102:105], v[182:185], v[146:149]
	v_mfma_f32_16x16x32_bf16 v[142:145], v[134:137], v[182:185], v[142:145]
	v_mfma_f32_16x16x32_bf16 v[114:117], v[102:105], v[190:193], v[114:117]
	v_mfma_f32_16x16x32_bf16 v[110:113], v[134:137], v[190:193], v[110:113]
	v_mfma_f32_16x16x32_bf16 v[170:173], v[106:109], v[162:165], v[170:173]
	v_mfma_f32_16x16x32_bf16 v[158:161], v[134:137], v[158:161], v[166:169]
	v_mfma_f32_16x16x32_bf16 v[154:157], v[106:109], v[178:181], v[154:157]
	v_mfma_f32_16x16x32_bf16 v[150:153], v[138:141], v[178:181], v[150:153]
	v_mfma_f32_16x16x32_bf16 v[146:149], v[106:109], v[186:189], v[146:149]
	v_mfma_f32_16x16x32_bf16 v[142:145], v[138:141], v[186:189], v[142:145]
	v_mfma_f32_16x16x32_bf16 v[114:117], v[106:109], v[194:197], v[114:117]
	v_mfma_f32_16x16x32_bf16 v[110:113], v[138:141], v[194:197], v[110:113]
	v_mfma_f32_16x16x32_bf16 v[158:161], v[138:141], v[162:165], v[158:161]
	s_setprio 0
	s_barrier
	s_add_i32 s53, s47, s39
	s_mov_b32 m0, s53
	ds_read_b128 v[162:165], v217 offset:16384
	ds_read_b128 v[166:169], v217 offset:17408
	ds_read_b128 v[174:177], v217 offset:18432
	ds_read_b128 v[178:181], v217 offset:19456
	ds_read_b128 v[182:185], v217 offset:20480
	ds_read_b128 v[186:189], v217 offset:21504
	ds_read_b128 v[190:193], v217 offset:22528
	ds_read_b128 v[194:197], v217 offset:23552
	global_load_lds_dwordx4 v202, s[28:29]
	s_add_i32 m0, s53, 0x2000
	s_add_u32 s54, s28, 0x80000
	s_addc_u32 s55, s29, 0
	s_add_i32 s53, s48, s39
	global_load_lds_dwordx4 v206, s[28:29]
	s_mov_b32 m0, s53
	s_nop 0
	global_load_lds_dwordx4 v202, s[54:55]
	s_add_i32 m0, s53, 0x2000
	s_nop 0
	global_load_lds_dwordx4 v206, s[54:55]
	s_mov_b32 m0, s40
	s_nop 0
	s_mov_b64 s[98:99], s[30:31]
	global_load_lds_dwordx4 v200, s[30:31]
	s_mov_b32 m0, s41
	s_nop 0
	global_load_lds_dwordx4 v204, s[30:31]
	s_waitcnt vmcnt(8)
	s_waitcnt lgkmcnt(0)
	s_barrier
	s_setprio 1
	s_waitcnt lgkmcnt(0)
	v_mfma_f32_16x16x32_bf16 v[90:93], v[38:41], v[162:165], v[90:93]
	v_mfma_f32_16x16x32_bf16 v[86:89], v[70:73], v[162:165], v[86:89]
	v_mfma_f32_16x16x32_bf16 v[58:61], v[38:41], v[174:177], v[58:61]
	v_mfma_f32_16x16x32_bf16 v[54:57], v[70:73], v[174:177], v[54:57]
	v_mfma_f32_16x16x32_bf16 v[34:37], v[38:41], v[182:185], v[34:37]
	v_mfma_f32_16x16x32_bf16 v[30:33], v[70:73], v[182:185], v[30:33]
	v_mfma_f32_16x16x32_bf16 v[18:21], v[38:41], v[190:193], v[18:21]
	v_mfma_f32_16x16x32_bf16 v[14:17], v[70:73], v[190:193], v[14:17]
	v_mfma_f32_16x16x32_bf16 v[90:93], v[42:45], v[166:169], v[90:93]
	v_mfma_f32_16x16x32_bf16 v[86:89], v[74:77], v[166:169], v[86:89]
	v_mfma_f32_16x16x32_bf16 v[58:61], v[42:45], v[178:181], v[58:61]
	v_mfma_f32_16x16x32_bf16 v[54:57], v[74:77], v[178:181], v[54:57]
	v_mfma_f32_16x16x32_bf16 v[34:37], v[42:45], v[186:189], v[34:37]
	v_mfma_f32_16x16x32_bf16 v[30:33], v[74:77], v[186:189], v[30:33]
	v_mfma_f32_16x16x32_bf16 v[18:21], v[42:45], v[194:197], v[18:21]
	v_mfma_f32_16x16x32_bf16 v[14:17], v[74:77], v[194:197], v[14:17]
	s_setprio 0
	s_setprio 1
	v_mfma_f32_16x16x32_bf16 v[46:49], v[102:105], v[174:177], v[46:49]
	v_mfma_f32_16x16x32_bf16 v[50:53], v[134:137], v[174:177], v[50:53]
	v_mfma_f32_16x16x32_bf16 v[22:25], v[102:105], v[182:185], v[22:25]
	v_mfma_f32_16x16x32_bf16 v[26:29], v[134:137], v[182:185], v[26:29]
	v_mfma_f32_16x16x32_bf16 v[4:7], v[102:105], v[190:193], v[6:9]
	v_mfma_f32_16x16x32_bf16 v[8:11], v[134:137], v[190:193], v[10:13]
	v_mfma_f32_16x16x32_bf16 v[38:41], v[102:105], v[162:165], v[78:81]
	v_mfma_f32_16x16x32_bf16 v[42:45], v[134:137], v[162:165], v[82:85]
	v_mfma_f32_16x16x32_bf16 v[46:49], v[106:109], v[178:181], v[46:49]
	v_mfma_f32_16x16x32_bf16 v[50:53], v[138:141], v[178:181], v[50:53]
	v_mfma_f32_16x16x32_bf16 v[22:25], v[106:109], v[186:189], v[22:25]
	v_mfma_f32_16x16x32_bf16 v[26:29], v[138:141], v[186:189], v[26:29]
	v_mfma_f32_16x16x32_bf16 v[4:7], v[106:109], v[194:197], v[4:7]
	v_mfma_f32_16x16x32_bf16 v[10:13], v[138:141], v[194:197], v[8:11]
	v_mfma_f32_16x16x32_bf16 v[38:41], v[106:109], v[166:169], v[38:41]
	v_mfma_f32_16x16x32_bf16 v[42:45], v[138:141], v[166:169], v[42:45]
	s_setprio 0
	s_barrier
; #define PG8_STAGE(bufoff, gbase, voff) do { _Pragma("unroll") for (int _i = 0; _i < 2; ++_i) \
;         __builtin_amdgcn_global_load_lds((const unsigned*)((const char*)(gbase) + (voff)[_i]), (LAS unsigned*)(lds + (bufoff) + ldsw + _i * 8192), 16, 0, 0); } while (0)
; #define PG8_LDA(dst, b, h) do { if constexpr (F8) { _Pragma("unroll") for (int m = 0; m < 4; ++m) dst##8[m] = PG8_LD8(lds, PG8_SA(b, h) + aoff + m * 2048); } \
;         else { _Pragma("unroll") for (int m = 0; m < 4; ++m) _Pragma("unroll") for (int k = 0; k < 2; ++k) dst[m][k] = *(const LAS bf16x8*)(lds + PG8_SA(b, h) + aoff + m * 2048 + k * 1024); } } while (0)
; #define PG8_LDB(dst, b, h) do { if constexpr (F8) { _Pragma("unroll") for (int n = 0; n < 2; ++n) dst##8[n] = PG8_LD8(ldsB, PG8_SBR(b, h) + boff + n * 2048); } \
;         else { _Pragma("unroll") for (int n = 0; n < 2; ++n) _Pragma("unroll") for (int k = 0; k < 2; ++k) dst[n][k] = *(const LAS bf16x8*)(ldsB + PG8_SBR(b, h) + boff + n * 2048 + k * 1024); } } while (0)
; #define PG8_WAIT_V(n) asm volatile("s_waitcnt vmcnt(" #n ")" ::: "memory")
; #define PG8_WAIT_L(n) asm volatile("s_waitcnt lgkmcnt(" #n ")" ::: "memory")
; #define PG8_BAR __builtin_amdgcn_s_barrier()
; #define PG8_SCHED __builtin_amdgcn_sched_barrier(0)
; template <bool GATHER, bool F8, class Epi, class Sched>
; __device__ __forceinline__ void gemm_phase(LAS unsigned char* lds, const int nt, const unsigned lda, const unsigned ldb, const Sched& S, const Epi& E) {
;     ...
;             PG8_LDB(B0, 1, 0); PG8_LDB(B1, 1, 1); PG8_SCHED; PG8_LDA(At, 1, 0); PG8_STAGE(PG8_SA(0, 1), a2 + hA, w1);
;             PG8_WAIT_V(8); PG8_WAIT_L(0); PG8_BAR; PG8_MMA(0, 0, At, B0); PG8_MMA(0, 1, At, B1); PG8_BAR; PG8_SCHED;
;             PG8_LDA(At, 1, 1); PG8_STAGE(PG8_SB(1, 0), b3, voffB); PG8_STAGE(PG8_SB(1, 1), b3 + hB, voffB); PG8_STAGE(PG8_SA(1, 0), a3, w0);
;             PG8_WAIT_V(8); PG8_WAIT_L(0); PG8_BAR; PG8_MMA(1, 0, At, B0); PG8_MMA(1, 1, At, B1); PG8_BAR; PG8_SCHED;
;         }
;         if (wr == 0) PG8_BAR;
	s_add_i32 s53, 0, 0x18000
	v_add_u32_e32 v3, s53, v199
	s_add_i32 s54, 0, 0x1c000
	ds_read_b128 v[70:73], v3
	ds_read_b128 v[74:77], v3 offset:1024
	ds_read_b128 v[78:81], v3 offset:2048
	ds_read_b128 v[82:85], v3 offset:3072
	v_add_u32_e32 v3, s54, v199
	ds_read_b128 v[102:105], v3
	ds_read_b128 v[106:109], v3 offset:1024
	ds_read_b128 v[134:137], v3 offset:2048
	ds_read_b128 v[138:141], v3 offset:3072
	s_add_u32 s30, s30, 0x80000
	s_addc_u32 s31, s31, 0
	s_mov_b32 m0, s42
	ds_read_b128 v[162:165], v217 offset:32768
	ds_read_b128 v[166:169], v217 offset:33792
	ds_read_b128 v[174:177], v217 offset:34816
	ds_read_b128 v[178:181], v217 offset:35840
	ds_read_b128 v[182:185], v217 offset:36864
	ds_read_b128 v[186:189], v217 offset:37888
	ds_read_b128 v[190:193], v217 offset:38912
	ds_read_b128 v[194:197], v217 offset:39936
	global_load_lds_dwordx4 v200, s[30:31]
	s_mov_b32 m0, s43
	s_nop 0
	global_load_lds_dwordx4 v204, s[30:31]
	s_waitcnt vmcnt(8)
	s_waitcnt lgkmcnt(0)
	s_barrier
	s_setprio 1
	s_waitcnt lgkmcnt(0)
	v_mfma_f32_16x16x32_bf16 v[66:69], v[70:73], v[162:165], v[66:69]
	v_mfma_f32_16x16x32_bf16 v[62:65], v[78:81], v[162:165], v[62:65]
	v_mfma_f32_16x16x32_bf16 v[98:101], v[70:73], v[174:177], v[98:101]
	v_mfma_f32_16x16x32_bf16 v[94:97], v[78:81], v[174:177], v[94:97]
	v_mfma_f32_16x16x32_bf16 v[122:125], v[70:73], v[182:185], v[122:125]
	v_mfma_f32_16x16x32_bf16 v[118:121], v[78:81], v[182:185], v[118:121]
	v_mfma_f32_16x16x32_bf16 v[130:133], v[70:73], v[190:193], v[130:133]
	v_mfma_f32_16x16x32_bf16 v[126:129], v[78:81], v[190:193], v[126:129]
	v_mfma_f32_16x16x32_bf16 v[66:69], v[74:77], v[166:169], v[66:69]
	v_mfma_f32_16x16x32_bf16 v[62:65], v[82:85], v[166:169], v[62:65]
	v_mfma_f32_16x16x32_bf16 v[98:101], v[74:77], v[178:181], v[98:101]
	v_mfma_f32_16x16x32_bf16 v[94:97], v[82:85], v[178:181], v[94:97]
	v_mfma_f32_16x16x32_bf16 v[122:125], v[74:77], v[186:189], v[122:125]
	v_mfma_f32_16x16x32_bf16 v[118:121], v[82:85], v[186:189], v[118:121]
	v_mfma_f32_16x16x32_bf16 v[130:133], v[74:77], v[194:197], v[130:133]
	v_mfma_f32_16x16x32_bf16 v[126:129], v[82:85], v[194:197], v[126:129]
	s_setprio 0
	s_setprio 1
	v_mfma_f32_16x16x32_bf16 v[170:173], v[102:105], v[162:165], v[170:173]
	v_mfma_f32_16x16x32_bf16 v[158:161], v[134:137], v[162:165], v[158:161]
	v_mfma_f32_16x16x32_bf16 v[154:157], v[102:105], v[174:177], v[154:157]
	v_mfma_f32_16x16x32_bf16 v[150:153], v[134:137], v[174:177], v[150:153]
	v_mfma_f32_16x16x32_bf16 v[146:149], v[102:105], v[182:185], v[146:149]
	v_mfma_f32_16x16x32_bf16 v[142:145], v[134:137], v[182:185], v[142:145]
	v_mfma_f32_16x16x32_bf16 v[114:117], v[102:105], v[190:193], v[114:117]
	v_mfma_f32_16x16x32_bf16 v[110:113], v[134:137], v[190:193], v[110:113]
	v_mfma_f32_16x16x32_bf16 v[170:173], v[106:109], v[166:169], v[170:173]
	v_mfma_f32_16x16x32_bf16 v[166:169], v[138:141], v[166:169], v[158:161]
	v_mfma_f32_16x16x32_bf16 v[154:157], v[106:109], v[178:181], v[154:157]
	v_mfma_f32_16x16x32_bf16 v[150:153], v[138:141], v[178:181], v[150:153]
	v_mfma_f32_16x16x32_bf16 v[146:149], v[106:109], v[186:189], v[146:149]
	v_mfma_f32_16x16x32_bf16 v[142:145], v[138:141], v[186:189], v[142:145]
	v_mfma_f32_16x16x32_bf16 v[114:117], v[106:109], v[194:197], v[114:117]
	v_mfma_f32_16x16x32_bf16 v[110:113], v[138:141], v[194:197], v[110:113]
	s_setprio 0
	s_barrier
	s_add_i32 s30, s53, s39
	s_add_i32 m0, s30, 0xffffff80
	ds_read_b128 v[158:161], v217 offset:49152
	ds_read_b128 v[162:165], v217 offset:50176
	ds_read_b128 v[174:177], v217 offset:51200
	ds_read_b128 v[178:181], v217 offset:52224
	ds_read_b128 v[182:185], v217 offset:53248
	ds_read_b128 v[186:189], v217 offset:54272
	ds_read_b128 v[190:193], v217 offset:55296
	ds_read_b128 v[194:197], v217 offset:56320
	global_load_lds_dwordx4 v202, s[28:29] offset:128
	s_add_i32 m0, s30, 0x1f80
	s_add_i32 s30, s54, s39
	global_load_lds_dwordx4 v206, s[28:29] offset:128
	s_add_u32 s28, s28, 0x80080
	s_addc_u32 s29, s29, 0
	s_mov_b32 m0, s30
	s_nop 0
	global_load_lds_dwordx4 v202, s[28:29]
	s_add_i32 m0, s30, 0x2000
	s_nop 0
	global_load_lds_dwordx4 v206, s[28:29]
	s_add_i32 m0, s45, 0xffffff80
	s_nop 0
	global_load_lds_dwordx4 v200, s[98:99] offset:128
	s_add_i32 m0, s46, 0xffffff80
	s_nop 0
	global_load_lds_dwordx4 v204, s[98:99] offset:128
	s_waitcnt vmcnt(8)
	s_waitcnt lgkmcnt(0)
	s_barrier
	s_setprio 1
	s_waitcnt lgkmcnt(0)
	v_mfma_f32_16x16x32_bf16 v[90:93], v[70:73], v[158:161], v[90:93]
	v_mfma_f32_16x16x32_bf16 v[86:89], v[78:81], v[158:161], v[86:89]
	v_mfma_f32_16x16x32_bf16 v[58:61], v[70:73], v[174:177], v[58:61]
	v_mfma_f32_16x16x32_bf16 v[54:57], v[78:81], v[174:177], v[54:57]
	v_mfma_f32_16x16x32_bf16 v[34:37], v[70:73], v[182:185], v[34:37]
	v_mfma_f32_16x16x32_bf16 v[30:33], v[78:81], v[182:185], v[30:33]
	v_mfma_f32_16x16x32_bf16 v[18:21], v[70:73], v[190:193], v[18:21]
	v_mfma_f32_16x16x32_bf16 v[14:17], v[78:81], v[190:193], v[14:17]
	v_mfma_f32_16x16x32_bf16 v[90:93], v[74:77], v[162:165], v[90:93]
	v_mfma_f32_16x16x32_bf16 v[86:89], v[82:85], v[162:165], v[86:89]
	v_mfma_f32_16x16x32_bf16 v[58:61], v[74:77], v[178:181], v[58:61]
	v_mfma_f32_16x16x32_bf16 v[54:57], v[82:85], v[178:181], v[54:57]
	v_mfma_f32_16x16x32_bf16 v[34:37], v[74:77], v[186:189], v[34:37]
	v_mfma_f32_16x16x32_bf16 v[30:33], v[82:85], v[186:189], v[30:33]
	v_mfma_f32_16x16x32_bf16 v[18:21], v[74:77], v[194:197], v[18:21]
	v_mfma_f32_16x16x32_bf16 v[14:17], v[82:85], v[194:197], v[14:17]
	s_setprio 0
	s_setprio 1
	v_mfma_f32_16x16x32_bf16 v[38:41], v[102:105], v[158:161], v[38:41]
	v_mfma_f32_16x16x32_bf16 v[78:81], v[106:109], v[162:165], v[38:41]
	v_mfma_f32_16x16x32_bf16 v[38:41], v[134:137], v[158:161], v[42:45]
	v_mfma_f32_16x16x32_bf16 v[82:85], v[138:141], v[162:165], v[38:41]
	v_mfma_f32_16x16x32_bf16 v[38:41], v[102:105], v[174:177], v[46:49]
	v_mfma_f32_16x16x32_bf16 v[46:49], v[106:109], v[178:181], v[38:41]
	v_mfma_f32_16x16x32_bf16 v[38:41], v[134:137], v[174:177], v[50:53]
	v_mfma_f32_16x16x32_bf16 v[22:25], v[102:105], v[182:185], v[22:25]
	v_mfma_f32_16x16x32_bf16 v[26:29], v[134:137], v[182:185], v[26:29]
	v_mfma_f32_16x16x32_bf16 v[4:7], v[102:105], v[190:193], v[4:7]
	v_mfma_f32_16x16x32_bf16 v[10:13], v[134:137], v[190:193], v[10:13]
	v_mfma_f32_16x16x32_bf16 v[50:53], v[138:141], v[178:181], v[38:41]
	v_mfma_f32_16x16x32_bf16 v[22:25], v[106:109], v[186:189], v[22:25]
	v_mfma_f32_16x16x32_bf16 v[26:29], v[138:141], v[186:189], v[26:29]
	v_mfma_f32_16x16x32_bf16 v[6:9], v[106:109], v[194:197], v[4:7]
	v_mfma_f32_16x16x32_bf16 v[10:13], v[138:141], v[194:197], v[10:13]
	s_setprio 0
	s_barrier
	s_add_i32 s52, s52, 2
	s_add_u32 s26, s26, 0x100
	s_addc_u32 s27, s27, 0
	s_add_u32 s25, s25, 0x100
	s_addc_u32 s34, s34, 0
	s_cmp_gt_u32 s52, 13
	s_cbranch_scc0 .LBB0_891
	s_and_b64 vcc, exec, s[12:13]
	s_cbranch_vccz .LBB0_894
	s_barrier

; #define PG8_STAGE(bufoff, gbase, voff) do { _Pragma("unroll") for (int _i = 0; _i < 2; ++_i) \
;         __builtin_amdgcn_global_load_lds((const unsigned*)((const char*)(gbase) + (voff)[_i]), (LAS unsigned*)(lds + (bufoff) + ldsw + _i * 8192), 16, 0, 0); } while (0)
; #define PG8_LDA(dst, b, h) do { if constexpr (F8) { _Pragma("unroll") for (int m = 0; m < 4; ++m) dst##8[m] = PG8_LD8(lds, PG8_SA(b, h) + aoff + m * 2048); } \
;         else { _Pragma("unroll") for (int m = 0; m < 4; ++m) _Pragma("unroll") for (int k = 0; k < 2; ++k) dst[m][k] = *(const LAS bf16x8*)(lds + PG8_SA(b, h) + aoff + m * 2048 + k * 1024); } } while (0)
; #define PG8_WAIT_V(n) asm volatile("s_waitcnt vmcnt(" #n ")" ::: "memory")
; #define PG8_WAIT_L(n) asm volatile("s_waitcnt lgkmcnt(" #n ")" ::: "memory")
; #define PG8_BAR __builtin_amdgcn_s_barrier()
; #define PG8_SCHED __builtin_amdgcn_sched_barrier(0)
; template <bool GATHER, bool F8, class Epi, class Sched>
; __device__ __forceinline__ void gemm_phase(LAS unsigned char* lds, const int nt, const unsigned lda, const unsigned ldb, const Sched& S, const Epi& E) {
;     ...
;         for (int t = 0; t < nt; t += 2) {
;             const bool last = (t == nt - 2);
;             const char* a1 = cA + (size_t)(t + 1) * kstep;
;             const char* a2 = last ? nA : cA + (size_t)(t + 2) * kstep; const char* b2 = last ? nB : cB + (size_t)(t + 2) * kstep;
;             const char* a3 = a2 + kstep; const char* b3 = b2 + kstep;
;             unsigned w0[2], w1[2];
;             if constexpr (GATHER) {
; #pragma unroll
;                 for (int i = 0; i < 2; ++i) { w0[i] = last ? vN0[i] : vA0[i]; w1[i] = last ? vN1[i] : vA1[i]; }
;             } else {
; #pragma unroll
;                 for (int i = 0; i < 2; ++i) { w0[i] = voffA[i]; w1[i] = voffA[i]; }
;             }
;             PG8_LDB(B0, 0, 0); PG8_LDB(B1, 0, 1); PG8_SCHED; PG8_LDA(At, 0, 0); PG8_STAGE(PG8_SA(1, 1), a1 + hA, vA1);
;             PG8_WAIT_V(8); PG8_WAIT_L(0); PG8_BAR; PG8_MMA(0, 0, At, B0); PG8_MMA(0, 1, At, B1); PG8_BAR; PG8_SCHED;
;             PG8_LDA(At, 0, 1); PG8_STAGE(PG8_SB(0, 0), b2, voffB); PG8_STAGE(PG8_SB(0, 1), b2 + hB, voffB); PG8_STAGE(PG8_SA(0, 0), a2, w0);
;             PG8_WAIT_V(8); PG8_WAIT_L(0); PG8_BAR; PG8_MMA(1, 0, At, B0); PG8_MMA(1, 1, At, B1); PG8_BAR; PG8_SCHED;
.LBB0_1034:
	ds_read_b128 v[130:133], v209
	ds_read_b128 v[134:137], v209 offset:1024
	ds_read_b128 v[138:141], v209 offset:2048
	ds_read_b128 v[142:145], v209 offset:3072
	ds_read_b128 v[146:149], v210
	ds_read_b128 v[150:153], v210 offset:1024
	ds_read_b128 v[154:157], v210 offset:2048
	ds_read_b128 v[158:161], v210 offset:3072
	s_add_u32 s24, s22, 0xfff80080
	s_addc_u32 s25, s23, -1
	s_cmp_eq_u32 s48, 28
	s_cselect_b32 s27, s1, s25
	s_cselect_b32 s26, s0, s24
	s_cselect_b32 s25, s19, s28
	s_cselect_b32 s24, s18, s21
	s_add_i32 m0, s36, 0xc000
	ds_read_b128 v[162:165], v211
	ds_read_b128 v[166:169], v211 offset:1024
	ds_read_b128 v[170:173], v211 offset:2048
	ds_read_b128 v[174:177], v211 offset:3072
	ds_read_b128 v[194:197], v211 offset:4096
	ds_read_b128 v[200:203], v211 offset:5120
	ds_read_b128 v[204:207], v211 offset:6144
	ds_read_b128 v[214:217], v211 offset:7168
	global_load_lds_dwordx4 v186, s[22:23]
	s_add_i32 m0, s36, 0xe000
	s_nop 0
	global_load_lds_dwordx4 v188, s[22:23]
	s_waitcnt vmcnt(8)
	s_waitcnt lgkmcnt(0)
	s_barrier
	s_setprio 1
	s_waitcnt lgkmcnt(0)
	v_mfma_f32_16x16x32_bf16 v[126:129], v[130:133], v[162:165], v[126:129]
	v_mfma_f32_16x16x32_bf16 v[122:125], v[138:141], v[162:165], v[122:125]
	v_mfma_f32_16x16x32_bf16 v[110:113], v[130:133], v[170:173], v[110:113]
	v_mfma_f32_16x16x32_bf16 v[106:109], v[138:141], v[170:173], v[106:109]
	v_mfma_f32_16x16x32_bf16 v[94:97], v[130:133], v[194:197], v[94:97]
	v_mfma_f32_16x16x32_bf16 v[90:93], v[138:141], v[194:197], v[90:93]
	v_mfma_f32_16x16x32_bf16 v[78:81], v[130:133], v[204:207], v[78:81]
	v_mfma_f32_16x16x32_bf16 v[74:77], v[138:141], v[204:207], v[74:77]
	v_mfma_f32_16x16x32_bf16 v[126:129], v[134:137], v[166:169], v[126:129]
	v_mfma_f32_16x16x32_bf16 v[122:125], v[142:145], v[166:169], v[122:125]
	v_mfma_f32_16x16x32_bf16 v[110:113], v[134:137], v[174:177], v[110:113]
	v_mfma_f32_16x16x32_bf16 v[106:109], v[142:145], v[174:177], v[106:109]
	v_mfma_f32_16x16x32_bf16 v[94:97], v[134:137], v[200:203], v[94:97]
	v_mfma_f32_16x16x32_bf16 v[90:93], v[142:145], v[200:203], v[90:93]
	v_mfma_f32_16x16x32_bf16 v[78:81], v[134:137], v[214:217], v[78:81]
	v_mfma_f32_16x16x32_bf16 v[74:77], v[142:145], v[214:217], v[74:77]
	s_setprio 0
	s_setprio 1
	v_mfma_f32_16x16x32_bf16 v[118:121], v[146:149], v[162:165], v[118:121]
	v_mfma_f32_16x16x32_bf16 v[114:117], v[154:157], v[162:165], v[114:117]
	v_mfma_f32_16x16x32_bf16 v[102:105], v[146:149], v[170:173], v[102:105]
	v_mfma_f32_16x16x32_bf16 v[98:101], v[154:157], v[170:173], v[98:101]
	v_mfma_f32_16x16x32_bf16 v[86:89], v[146:149], v[194:197], v[86:89]
	v_mfma_f32_16x16x32_bf16 v[82:85], v[154:157], v[194:197], v[82:85]
	v_mfma_f32_16x16x32_bf16 v[70:73], v[146:149], v[204:207], v[70:73]
	v_mfma_f32_16x16x32_bf16 v[66:69], v[154:157], v[204:207], v[66:69]
	v_mfma_f32_16x16x32_bf16 v[118:121], v[150:153], v[166:169], v[118:121]
	v_mfma_f32_16x16x32_bf16 v[114:117], v[158:161], v[166:169], v[114:117]
	v_mfma_f32_16x16x32_bf16 v[102:105], v[150:153], v[174:177], v[102:105]
	v_mfma_f32_16x16x32_bf16 v[98:101], v[158:161], v[174:177], v[98:101]
	v_mfma_f32_16x16x32_bf16 v[86:89], v[150:153], v[200:203], v[86:89]
	v_mfma_f32_16x16x32_bf16 v[82:85], v[158:161], v[200:203], v[82:85]
	v_mfma_f32_16x16x32_bf16 v[70:73], v[150:153], v[214:217], v[70:73]
	v_mfma_f32_16x16x32_bf16 v[66:69], v[158:161], v[214:217], v[66:69]
	s_setprio 0
	s_barrier
	s_add_i32 s49, s44, s35
	s_mov_b32 m0, s49
	ds_read_b128 v[162:165], v211 offset:16384
	ds_read_b128 v[166:169], v211 offset:17408
	ds_read_b128 v[170:173], v211 offset:18432
	ds_read_b128 v[174:177], v211 offset:19456
	ds_read_b128 v[194:197], v211 offset:20480
	ds_read_b128 v[200:203], v211 offset:21504
	ds_read_b128 v[204:207], v211 offset:22528
	ds_read_b128 v[214:217], v211 offset:23552
	global_load_lds_dwordx4 v180, s[24:25]
	s_add_i32 m0, s49, 0x2000
	s_add_u32 s50, s24, 0x80000
	s_addc_u32 s51, s25, 0
	s_add_i32 s49, s45, s35
	global_load_lds_dwordx4 v184, s[24:25]
	s_mov_b32 m0, s49
	s_nop 0
	global_load_lds_dwordx4 v180, s[50:51]
	s_add_i32 m0, s49, 0x2000
	s_nop 0
	global_load_lds_dwordx4 v184, s[50:51]
	s_mov_b32 m0, s36
	s_nop 0
	s_mov_b64 s[98:99], s[26:27]
	global_load_lds_dwordx4 v178, s[26:27]
	s_mov_b32 m0, s37
	s_nop 0
	global_load_lds_dwordx4 v182, s[26:27]
	s_waitcnt vmcnt(8)
	s_waitcnt lgkmcnt(0)
	s_barrier
	s_setprio 1
	s_waitcnt lgkmcnt(0)
	v_mfma_f32_16x16x32_bf16 v[54:57], v[130:133], v[162:165], v[54:57]
	v_mfma_f32_16x16x32_bf16 v[50:53], v[138:141], v[162:165], v[50:53]
	v_mfma_f32_16x16x32_bf16 v[38:41], v[130:133], v[170:173], v[38:41]
	v_mfma_f32_16x16x32_bf16 v[34:37], v[138:141], v[170:173], v[34:37]
	v_mfma_f32_16x16x32_bf16 v[22:25], v[130:133], v[194:197], v[22:25]
	v_mfma_f32_16x16x32_bf16 v[18:21], v[138:141], v[194:197], v[18:21]
	v_mfma_f32_16x16x32_bf16 v[6:9], v[130:133], v[204:207], v[6:9]
	v_mfma_f32_16x16x32_bf16 v[2:5], v[138:141], v[204:207], v[2:5]
	v_mfma_f32_16x16x32_bf16 v[54:57], v[134:137], v[166:169], v[54:57]
	v_mfma_f32_16x16x32_bf16 v[50:53], v[142:145], v[166:169], v[50:53]
	v_mfma_f32_16x16x32_bf16 v[38:41], v[134:137], v[174:177], v[38:41]
	v_mfma_f32_16x16x32_bf16 v[34:37], v[142:145], v[174:177], v[34:37]
	v_mfma_f32_16x16x32_bf16 v[22:25], v[134:137], v[200:203], v[22:25]
	v_mfma_f32_16x16x32_bf16 v[18:21], v[142:145], v[200:203], v[18:21]
	v_mfma_f32_16x16x32_bf16 v[6:9], v[134:137], v[214:217], v[6:9]
	v_mfma_f32_16x16x32_bf16 v[2:5], v[142:145], v[214:217], v[2:5]
	s_setprio 0
	s_setprio 1
	v_mfma_f32_16x16x32_bf16 v[62:65], v[146:149], v[162:165], v[62:65]
	v_mfma_f32_16x16x32_bf16 v[58:61], v[154:157], v[162:165], v[58:61]
	v_mfma_f32_16x16x32_bf16 v[46:49], v[146:149], v[170:173], v[46:49]
	v_mfma_f32_16x16x32_bf16 v[42:45], v[154:157], v[170:173], v[42:45]
	v_mfma_f32_16x16x32_bf16 v[30:33], v[146:149], v[194:197], v[30:33]
	v_mfma_f32_16x16x32_bf16 v[26:29], v[154:157], v[194:197], v[26:29]
	v_mfma_f32_16x16x32_bf16 v[14:17], v[146:149], v[204:207], v[14:17]
	v_mfma_f32_16x16x32_bf16 v[10:13], v[154:157], v[204:207], v[10:13]
	v_mfma_f32_16x16x32_bf16 v[62:65], v[150:153], v[166:169], v[62:65]
	v_mfma_f32_16x16x32_bf16 v[58:61], v[158:161], v[166:169], v[58:61]
	v_mfma_f32_16x16x32_bf16 v[46:49], v[150:153], v[174:177], v[46:49]
	v_mfma_f32_16x16x32_bf16 v[42:45], v[158:161], v[174:177], v[42:45]
	v_mfma_f32_16x16x32_bf16 v[30:33], v[150:153], v[200:203], v[30:33]
	v_mfma_f32_16x16x32_bf16 v[26:29], v[158:161], v[200:203], v[26:29]
	v_mfma_f32_16x16x32_bf16 v[14:17], v[150:153], v[214:217], v[14:17]
	v_mfma_f32_16x16x32_bf16 v[10:13], v[158:161], v[214:217], v[10:13]
	s_setprio 0
	s_barrier
; #define PG8_STAGE(bufoff, gbase, voff) do { _Pragma("unroll") for (int _i = 0; _i < 2; ++_i) \
;         __builtin_amdgcn_global_load_lds((const unsigned*)((const char*)(gbase) + (voff)[_i]), (LAS unsigned*)(lds + (bufoff) + ldsw + _i * 8192), 16, 0, 0); } while (0)
; #define PG8_LDA(dst, b, h) do { if constexpr (F8) { _Pragma("unroll") for (int m = 0; m < 4; ++m) dst##8[m] = PG8_LD8(lds, PG8_SA(b, h) + aoff + m * 2048); } \
;         else { _Pragma("unroll") for (int m = 0; m < 4; ++m) _Pragma("unroll") for (int k = 0; k < 2; ++k) dst[m][k] = *(const LAS bf16x8*)(lds + PG8_SA(b, h) + aoff + m * 2048 + k * 1024); } } while (0)
; #define PG8_LDB(dst, b, h) do { if constexpr (F8) { _Pragma("unroll") for (int n = 0; n < 2; ++n) dst##8[n] = PG8_LD8(ldsB, PG8_SBR(b, h) + boff + n * 2048); } \
;         else { _Pragma("unroll") for (int n = 0; n < 2; ++n) _Pragma("unroll") for (int k = 0; k < 2; ++k) dst[n][k] = *(const LAS bf16x8*)(ldsB + PG8_SBR(b, h) + boff + n * 2048 + k * 1024); } } while (0)
; #define PG8_WAIT_V(n) asm volatile("s_waitcnt vmcnt(" #n ")" ::: "memory")
; #define PG8_WAIT_L(n) asm volatile("s_waitcnt lgkmcnt(" #n ")" ::: "memory")
; #define PG8_BAR __builtin_amdgcn_s_barrier()
; #define PG8_SCHED __builtin_amdgcn_sched_barrier(0)
; template <bool GATHER, bool F8, class Epi, class Sched>
; __device__ __forceinline__ void gemm_phase(LAS unsigned char* lds, const int nt, const unsigned lda, const unsigned ldb, const Sched& S, const Epi& E) {
;     ...
;             PG8_LDB(B0, 1, 0); PG8_LDB(B1, 1, 1); PG8_SCHED; PG8_LDA(At, 1, 0); PG8_STAGE(PG8_SA(0, 1), a2 + hA, w1);
;             PG8_WAIT_V(8); PG8_WAIT_L(0); PG8_BAR; PG8_MMA(0, 0, At, B0); PG8_MMA(0, 1, At, B1); PG8_BAR; PG8_SCHED;
;             PG8_LDA(At, 1, 1); PG8_STAGE(PG8_SB(1, 0), b3, voffB); PG8_STAGE(PG8_SB(1, 1), b3 + hB, voffB); PG8_STAGE(PG8_SA(1, 0), a3, w0);
;             PG8_WAIT_V(8); PG8_WAIT_L(0); PG8_BAR; PG8_MMA(1, 0, At, B0); PG8_MMA(1, 1, At, B1); PG8_BAR; PG8_SCHED;
;         }
;         if (wr == 0) PG8_BAR;
	s_add_i32 s49, 0, 0x18000
	s_add_i32 s50, 0, 0x1c000
	v_add_u32_e32 v142, s49, v199
	v_add_u32_e32 v158, s50, v199
	ds_read_b128 v[130:133], v142
	ds_read_b128 v[134:137], v142 offset:1024
	ds_read_b128 v[138:141], v142 offset:2048
	ds_read_b128 v[142:145], v142 offset:3072
	ds_read_b128 v[146:149], v158
	ds_read_b128 v[150:153], v158 offset:1024
	ds_read_b128 v[154:157], v158 offset:2048
	ds_read_b128 v[158:161], v158 offset:3072
	s_add_u32 s26, s26, 0x80000
	s_addc_u32 s27, s27, 0
	s_mov_b32 m0, s38
	ds_read_b128 v[162:165], v211 offset:32768
	ds_read_b128 v[166:169], v211 offset:33792
	ds_read_b128 v[170:173], v211 offset:34816
	ds_read_b128 v[174:177], v211 offset:35840
	ds_read_b128 v[194:197], v211 offset:36864
	ds_read_b128 v[200:203], v211 offset:37888
	ds_read_b128 v[204:207], v211 offset:38912
	ds_read_b128 v[214:217], v211 offset:39936
	global_load_lds_dwordx4 v178, s[26:27]
	s_mov_b32 m0, s39
	s_nop 0
	global_load_lds_dwordx4 v182, s[26:27]
	s_waitcnt vmcnt(8)
	s_waitcnt lgkmcnt(0)
	s_barrier
	s_setprio 1
	s_waitcnt lgkmcnt(0)
	v_mfma_f32_16x16x32_bf16 v[126:129], v[130:133], v[162:165], v[126:129]
	v_mfma_f32_16x16x32_bf16 v[122:125], v[138:141], v[162:165], v[122:125]
	v_mfma_f32_16x16x32_bf16 v[110:113], v[130:133], v[170:173], v[110:113]
	v_mfma_f32_16x16x32_bf16 v[106:109], v[138:141], v[170:173], v[106:109]
	v_mfma_f32_16x16x32_bf16 v[94:97], v[130:133], v[194:197], v[94:97]
	v_mfma_f32_16x16x32_bf16 v[90:93], v[138:141], v[194:197], v[90:93]
	v_mfma_f32_16x16x32_bf16 v[78:81], v[130:133], v[204:207], v[78:81]
	v_mfma_f32_16x16x32_bf16 v[74:77], v[138:141], v[204:207], v[74:77]
	v_mfma_f32_16x16x32_bf16 v[126:129], v[134:137], v[166:169], v[126:129]
	v_mfma_f32_16x16x32_bf16 v[122:125], v[142:145], v[166:169], v[122:125]
	v_mfma_f32_16x16x32_bf16 v[110:113], v[134:137], v[174:177], v[110:113]
	v_mfma_f32_16x16x32_bf16 v[106:109], v[142:145], v[174:177], v[106:109]
	v_mfma_f32_16x16x32_bf16 v[94:97], v[134:137], v[200:203], v[94:97]
	v_mfma_f32_16x16x32_bf16 v[90:93], v[142:145], v[200:203], v[90:93]
	v_mfma_f32_16x16x32_bf16 v[78:81], v[134:137], v[214:217], v[78:81]
	v_mfma_f32_16x16x32_bf16 v[74:77], v[142:145], v[214:217], v[74:77]
	s_setprio 0
	s_setprio 1
	v_mfma_f32_16x16x32_bf16 v[118:121], v[146:149], v[162:165], v[118:121]
	v_mfma_f32_16x16x32_bf16 v[114:117], v[154:157], v[162:165], v[114:117]
	v_mfma_f32_16x16x32_bf16 v[102:105], v[146:149], v[170:173], v[102:105]
	v_mfma_f32_16x16x32_bf16 v[98:101], v[154:157], v[170:173], v[98:101]
	v_mfma_f32_16x16x32_bf16 v[86:89], v[146:149], v[194:197], v[86:89]
	v_mfma_f32_16x16x32_bf16 v[82:85], v[154:157], v[194:197], v[82:85]
	v_mfma_f32_16x16x32_bf16 v[70:73], v[146:149], v[204:207], v[70:73]
	v_mfma_f32_16x16x32_bf16 v[66:69], v[154:157], v[204:207], v[66:69]
	v_mfma_f32_16x16x32_bf16 v[118:121], v[150:153], v[166:169], v[118:121]
	v_mfma_f32_16x16x32_bf16 v[114:117], v[158:161], v[166:169], v[114:117]
	v_mfma_f32_16x16x32_bf16 v[102:105], v[150:153], v[174:177], v[102:105]
	v_mfma_f32_16x16x32_bf16 v[98:101], v[158:161], v[174:177], v[98:101]
	v_mfma_f32_16x16x32_bf16 v[86:89], v[150:153], v[200:203], v[86:89]
	v_mfma_f32_16x16x32_bf16 v[82:85], v[158:161], v[200:203], v[82:85]
	v_mfma_f32_16x16x32_bf16 v[70:73], v[150:153], v[214:217], v[70:73]
	v_mfma_f32_16x16x32_bf16 v[66:69], v[158:161], v[214:217], v[66:69]
	s_setprio 0
	s_barrier
	s_add_i32 s26, s49, s35
	s_add_i32 m0, s26, 0xffffff80
	ds_read_b128 v[162:165], v211 offset:49152
	ds_read_b128 v[166:169], v211 offset:50176
	ds_read_b128 v[170:173], v211 offset:51200
	ds_read_b128 v[174:177], v211 offset:52224
	ds_read_b128 v[194:197], v211 offset:53248
	ds_read_b128 v[200:203], v211 offset:54272
	ds_read_b128 v[204:207], v211 offset:55296
	ds_read_b128 v[214:217], v211 offset:56320
	global_load_lds_dwordx4 v180, s[24:25] offset:128
	s_add_i32 m0, s26, 0x1f80
	s_add_i32 s26, s50, s35
	global_load_lds_dwordx4 v184, s[24:25] offset:128
	s_add_u32 s24, s24, 0x80080
	s_addc_u32 s25, s25, 0
	s_mov_b32 m0, s26
	s_nop 0
	global_load_lds_dwordx4 v180, s[24:25]
	s_add_i32 m0, s26, 0x2000
	s_nop 0
	global_load_lds_dwordx4 v184, s[24:25]
	s_add_i32 m0, s41, 0xffffff80
	s_nop 0
	global_load_lds_dwordx4 v178, s[98:99] offset:128
	s_add_i32 m0, s42, 0xffffff80
	s_nop 0
	global_load_lds_dwordx4 v182, s[98:99] offset:128
	s_waitcnt vmcnt(8)
	s_waitcnt lgkmcnt(0)
	s_barrier
	s_setprio 1
	s_waitcnt lgkmcnt(0)
	v_mfma_f32_16x16x32_bf16 v[54:57], v[130:133], v[162:165], v[54:57]
	v_mfma_f32_16x16x32_bf16 v[50:53], v[138:141], v[162:165], v[50:53]
	v_mfma_f32_16x16x32_bf16 v[38:41], v[130:133], v[170:173], v[38:41]
	v_mfma_f32_16x16x32_bf16 v[34:37], v[138:141], v[170:173], v[34:37]
	v_mfma_f32_16x16x32_bf16 v[22:25], v[130:133], v[194:197], v[22:25]
	v_mfma_f32_16x16x32_bf16 v[18:21], v[138:141], v[194:197], v[18:21]
	v_mfma_f32_16x16x32_bf16 v[6:9], v[130:133], v[204:207], v[6:9]
	v_mfma_f32_16x16x32_bf16 v[2:5], v[138:141], v[204:207], v[2:5]
	v_mfma_f32_16x16x32_bf16 v[54:57], v[134:137], v[166:169], v[54:57]
	v_mfma_f32_16x16x32_bf16 v[50:53], v[142:145], v[166:169], v[50:53]
	v_mfma_f32_16x16x32_bf16 v[38:41], v[134:137], v[174:177], v[38:41]
	v_mfma_f32_16x16x32_bf16 v[34:37], v[142:145], v[174:177], v[34:37]
	v_mfma_f32_16x16x32_bf16 v[22:25], v[134:137], v[200:203], v[22:25]
	v_mfma_f32_16x16x32_bf16 v[18:21], v[142:145], v[200:203], v[18:21]
	v_mfma_f32_16x16x32_bf16 v[6:9], v[134:137], v[214:217], v[6:9]
	v_mfma_f32_16x16x32_bf16 v[2:5], v[142:145], v[214:217], v[2:5]
	s_setprio 0
	s_setprio 1
	v_mfma_f32_16x16x32_bf16 v[62:65], v[146:149], v[162:165], v[62:65]
	v_mfma_f32_16x16x32_bf16 v[58:61], v[154:157], v[162:165], v[58:61]
	v_mfma_f32_16x16x32_bf16 v[46:49], v[146:149], v[170:173], v[46:49]
	v_mfma_f32_16x16x32_bf16 v[42:45], v[154:157], v[170:173], v[42:45]
	v_mfma_f32_16x16x32_bf16 v[30:33], v[146:149], v[194:197], v[30:33]
	v_mfma_f32_16x16x32_bf16 v[26:29], v[154:157], v[194:197], v[26:29]
	v_mfma_f32_16x16x32_bf16 v[14:17], v[146:149], v[204:207], v[14:17]
	v_mfma_f32_16x16x32_bf16 v[10:13], v[154:157], v[204:207], v[10:13]
	v_mfma_f32_16x16x32_bf16 v[62:65], v[150:153], v[166:169], v[62:65]
	v_mfma_f32_16x16x32_bf16 v[58:61], v[158:161], v[166:169], v[58:61]
	v_mfma_f32_16x16x32_bf16 v[46:49], v[150:153], v[174:177], v[46:49]
	v_mfma_f32_16x16x32_bf16 v[42:45], v[158:161], v[174:177], v[42:45]
	v_mfma_f32_16x16x32_bf16 v[30:33], v[150:153], v[200:203], v[30:33]
	v_mfma_f32_16x16x32_bf16 v[26:29], v[158:161], v[200:203], v[26:29]
	v_mfma_f32_16x16x32_bf16 v[14:17], v[150:153], v[214:217], v[14:17]
	v_mfma_f32_16x16x32_bf16 v[10:13], v[158:161], v[214:217], v[10:13]
	s_setprio 0
	s_barrier
	s_add_i32 s48, s48, 2
	s_add_u32 s22, s22, 0x100
	s_addc_u32 s23, s23, 0
	s_add_u32 s21, s21, 0x100
	s_addc_u32 s28, s28, 0
	s_cmp_gt_u32 s48, 29
	s_cbranch_scc0 .LBB0_1034
	s_and_b64 vcc, exec, s[16:17]
	s_cbranch_vccz .LBB0_1037
	s_barrier

; #define PG8_STAGE(bufoff, gbase, voff) do { _Pragma("unroll") for (int _i = 0; _i < 2; ++_i) \
;         __builtin_amdgcn_global_load_lds((const unsigned*)((const char*)(gbase) + (voff)[_i]), (LAS unsigned*)(lds + (bufoff) + ldsw + _i * 8192), 16, 0, 0); } while (0)
; #define PG8_LDA(dst, b, h) do { if constexpr (F8) { _Pragma("unroll") for (int m = 0; m < 4; ++m) dst##8[m] = PG8_LD8(lds, PG8_SA(b, h) + aoff + m * 2048); } \
;         else { _Pragma("unroll") for (int m = 0; m < 4; ++m) _Pragma("unroll") for (int k = 0; k < 2; ++k) dst[m][k] = *(const LAS bf16x8*)(lds + PG8_SA(b, h) + aoff + m * 2048 + k * 1024); } } while (0)
; #define PG8_WAIT_V(n) asm volatile("s_waitcnt vmcnt(" #n ")" ::: "memory")
; #define PG8_WAIT_L(n) asm volatile("s_waitcnt lgkmcnt(" #n ")" ::: "memory")
; #define PG8_BAR __builtin_amdgcn_s_barrier()
; #define PG8_SCHED __builtin_amdgcn_sched_barrier(0)
; template <bool GATHER, bool F8, class Epi, class Sched>
; __device__ __forceinline__ void gemm_phase(LAS unsigned char* lds, const int nt, const unsigned lda, const unsigned ldb, const Sched& S, const Epi& E) {
;     ...
;         for (int t = 0; t < nt; t += 2) {
;             const bool last = (t == nt - 2);
;             const char* a1 = cA + (size_t)(t + 1) * kstep;
;             const char* a2 = last ? nA : cA + (size_t)(t + 2) * kstep; const char* b2 = last ? nB : cB + (size_t)(t + 2) * kstep;
;             const char* a3 = a2 + kstep; const char* b3 = b2 + kstep;
;             unsigned w0[2], w1[2];
;             if constexpr (GATHER) {
; #pragma unroll
;                 for (int i = 0; i < 2; ++i) { w0[i] = last ? vN0[i] : vA0[i]; w1[i] = last ? vN1[i] : vA1[i]; }
;             } else {
; #pragma unroll
;                 for (int i = 0; i < 2; ++i) { w0[i] = voffA[i]; w1[i] = voffA[i]; }
;             }
;             PG8_LDB(B0, 0, 0); PG8_LDB(B1, 0, 1); PG8_SCHED; PG8_LDA(At, 0, 0); PG8_STAGE(PG8_SA(1, 1), a1 + hA, vA1);
;             PG8_WAIT_V(8); PG8_WAIT_L(0); PG8_BAR; PG8_MMA(0, 0, At, B0); PG8_MMA(0, 1, At, B1); PG8_BAR; PG8_SCHED;
;             PG8_LDA(At, 0, 1); PG8_STAGE(PG8_SB(0, 0), b2, voffB); PG8_STAGE(PG8_SB(0, 1), b2 + hB, voffB); PG8_STAGE(PG8_SA(0, 0), a2, w0);
;             PG8_WAIT_V(8); PG8_WAIT_L(0); PG8_BAR; PG8_MMA(1, 0, At, B0); PG8_MMA(1, 1, At, B1); PG8_BAR; PG8_SCHED;
.LBB0_1432:
	ds_read_b128 v[130:133], v184
	ds_read_b128 v[134:137], v184 offset:1024
	ds_read_b128 v[138:141], v184 offset:2048
	ds_read_b128 v[142:145], v184 offset:3072
	ds_read_b128 v[146:149], v185
	ds_read_b128 v[150:153], v185 offset:1024
	ds_read_b128 v[170:173], v185 offset:2048
	ds_read_b128 v[174:177], v185 offset:3072
	s_add_u32 s28, s26, 0xfffe0080
	s_addc_u32 s29, s27, -1
	s_cmp_eq_u32 s53, 4
	s_cselect_b32 s31, s1, s29
	s_cselect_b32 s30, s0, s28
	s_cselect_b32 s29, s23, s34
	s_cselect_b32 s28, s22, s25
	s_add_i32 m0, s40, 0xc000
	ds_read_b128 v[178:181], v186
	ds_read_b128 v[190:193], v186 offset:1024
	ds_read_b128 v[194:197], v186 offset:2048
	ds_read_b128 v[200:203], v186 offset:3072
	ds_read_b128 v[204:207], v186 offset:4096
	ds_read_b128 v[208:211], v186 offset:5120
	ds_read_b128 v[212:215], v186 offset:6144
	ds_read_b128 v[216:219], v186 offset:7168
	global_load_lds_dwordx4 v162, s[26:27]
	s_add_i32 m0, s40, 0xe000
	s_nop 0
	global_load_lds_dwordx4 v164, s[26:27]
	s_waitcnt vmcnt(8)
	s_waitcnt lgkmcnt(0)
	s_barrier
	s_setprio 1
	s_waitcnt lgkmcnt(0)
	v_mfma_f32_16x16x32_bf16 v[126:129], v[130:133], v[178:181], v[126:129]
	v_mfma_f32_16x16x32_bf16 v[122:125], v[138:141], v[178:181], v[122:125]
	v_mfma_f32_16x16x32_bf16 v[110:113], v[130:133], v[194:197], v[110:113]
	v_mfma_f32_16x16x32_bf16 v[106:109], v[138:141], v[194:197], v[106:109]
	v_mfma_f32_16x16x32_bf16 v[94:97], v[130:133], v[204:207], v[94:97]
	v_mfma_f32_16x16x32_bf16 v[90:93], v[138:141], v[204:207], v[90:93]
	v_mfma_f32_16x16x32_bf16 v[78:81], v[130:133], v[212:215], v[78:81]
	v_mfma_f32_16x16x32_bf16 v[74:77], v[138:141], v[212:215], v[74:77]
	v_mfma_f32_16x16x32_bf16 v[126:129], v[134:137], v[190:193], v[126:129]
	v_mfma_f32_16x16x32_bf16 v[122:125], v[142:145], v[190:193], v[122:125]
	v_mfma_f32_16x16x32_bf16 v[110:113], v[134:137], v[200:203], v[110:113]
	v_mfma_f32_16x16x32_bf16 v[106:109], v[142:145], v[200:203], v[106:109]
	v_mfma_f32_16x16x32_bf16 v[94:97], v[134:137], v[208:211], v[94:97]
	v_mfma_f32_16x16x32_bf16 v[90:93], v[142:145], v[208:211], v[90:93]
	v_mfma_f32_16x16x32_bf16 v[78:81], v[134:137], v[216:219], v[78:81]
	v_mfma_f32_16x16x32_bf16 v[74:77], v[142:145], v[216:219], v[74:77]
	s_setprio 0
	s_setprio 1
	v_mfma_f32_16x16x32_bf16 v[118:121], v[146:149], v[178:181], v[118:121]
	v_mfma_f32_16x16x32_bf16 v[114:117], v[170:173], v[178:181], v[114:117]
	v_mfma_f32_16x16x32_bf16 v[102:105], v[146:149], v[194:197], v[102:105]
	v_mfma_f32_16x16x32_bf16 v[98:101], v[170:173], v[194:197], v[98:101]
	v_mfma_f32_16x16x32_bf16 v[86:89], v[146:149], v[204:207], v[86:89]
	v_mfma_f32_16x16x32_bf16 v[82:85], v[170:173], v[204:207], v[82:85]
	v_mfma_f32_16x16x32_bf16 v[70:73], v[146:149], v[212:215], v[70:73]
	v_mfma_f32_16x16x32_bf16 v[66:69], v[170:173], v[212:215], v[66:69]
	v_mfma_f32_16x16x32_bf16 v[118:121], v[150:153], v[190:193], v[118:121]
	v_mfma_f32_16x16x32_bf16 v[114:117], v[174:177], v[190:193], v[114:117]
	v_mfma_f32_16x16x32_bf16 v[102:105], v[150:153], v[200:203], v[102:105]
	v_mfma_f32_16x16x32_bf16 v[98:101], v[174:177], v[200:203], v[98:101]
	v_mfma_f32_16x16x32_bf16 v[86:89], v[150:153], v[208:211], v[86:89]
	v_mfma_f32_16x16x32_bf16 v[82:85], v[174:177], v[208:211], v[82:85]
	v_mfma_f32_16x16x32_bf16 v[70:73], v[150:153], v[216:219], v[70:73]
	v_mfma_f32_16x16x32_bf16 v[66:69], v[174:177], v[216:219], v[66:69]
	s_setprio 0
	s_barrier
	s_add_i32 s54, s48, s39
	s_mov_b32 m0, s54
	ds_read_b128 v[178:181], v186 offset:16384
	ds_read_b128 v[190:193], v186 offset:17408
	ds_read_b128 v[194:197], v186 offset:18432
	ds_read_b128 v[200:203], v186 offset:19456
	ds_read_b128 v[204:207], v186 offset:20480
	ds_read_b128 v[208:211], v186 offset:21504
	ds_read_b128 v[212:215], v186 offset:22528
	ds_read_b128 v[216:219], v186 offset:23552
	global_load_lds_dwordx4 v156, s[28:29]
	s_add_i32 m0, s54, 0x2000
	s_add_u32 s54, s28, 0x20000
	s_addc_u32 s55, s29, 0
	s_add_i32 s56, s49, s39
	global_load_lds_dwordx4 v160, s[28:29]
	s_mov_b32 m0, s56
	s_nop 0
	global_load_lds_dwordx4 v156, s[54:55]
	s_add_i32 m0, s56, 0x2000
	s_nop 0
	global_load_lds_dwordx4 v160, s[54:55]
	s_mov_b32 m0, s40
	s_nop 0
	s_mov_b64 s[98:99], s[30:31]
	global_load_lds_dwordx4 v154, s[30:31]
	s_mov_b32 m0, s41
	s_nop 0
	global_load_lds_dwordx4 v158, s[30:31]
	s_waitcnt vmcnt(8)
	s_waitcnt lgkmcnt(0)
	s_barrier
	s_setprio 1
	s_waitcnt lgkmcnt(0)
	v_mfma_f32_16x16x32_bf16 v[54:57], v[130:133], v[178:181], v[54:57]
	v_mfma_f32_16x16x32_bf16 v[50:53], v[138:141], v[178:181], v[50:53]
	v_mfma_f32_16x16x32_bf16 v[46:49], v[130:133], v[194:197], v[46:49]
	v_mfma_f32_16x16x32_bf16 v[34:37], v[138:141], v[194:197], v[34:37]
	v_mfma_f32_16x16x32_bf16 v[22:25], v[130:133], v[204:207], v[22:25]
	v_mfma_f32_16x16x32_bf16 v[18:21], v[138:141], v[204:207], v[18:21]
	v_mfma_f32_16x16x32_bf16 v[6:9], v[130:133], v[212:215], v[6:9]
	v_mfma_f32_16x16x32_bf16 v[2:5], v[138:141], v[212:215], v[2:5]
	v_mfma_f32_16x16x32_bf16 v[54:57], v[134:137], v[190:193], v[54:57]
	v_mfma_f32_16x16x32_bf16 v[50:53], v[142:145], v[190:193], v[50:53]
	v_mfma_f32_16x16x32_bf16 v[46:49], v[134:137], v[200:203], v[46:49]
	v_mfma_f32_16x16x32_bf16 v[34:37], v[142:145], v[200:203], v[34:37]
	v_mfma_f32_16x16x32_bf16 v[22:25], v[134:137], v[208:211], v[22:25]
	v_mfma_f32_16x16x32_bf16 v[18:21], v[142:145], v[208:211], v[18:21]
	v_mfma_f32_16x16x32_bf16 v[6:9], v[134:137], v[216:219], v[6:9]
	v_mfma_f32_16x16x32_bf16 v[2:5], v[142:145], v[216:219], v[2:5]
	s_setprio 0
	s_setprio 1
	v_mfma_f32_16x16x32_bf16 v[62:65], v[146:149], v[178:181], v[62:65]
	v_mfma_f32_16x16x32_bf16 v[58:61], v[170:173], v[178:181], v[58:61]
	v_mfma_f32_16x16x32_bf16 v[42:45], v[146:149], v[194:197], v[42:45]
	v_mfma_f32_16x16x32_bf16 v[38:41], v[170:173], v[194:197], v[38:41]
	v_mfma_f32_16x16x32_bf16 v[30:33], v[146:149], v[204:207], v[30:33]
	v_mfma_f32_16x16x32_bf16 v[26:29], v[170:173], v[204:207], v[26:29]
	v_mfma_f32_16x16x32_bf16 v[14:17], v[146:149], v[212:215], v[14:17]
	v_mfma_f32_16x16x32_bf16 v[10:13], v[170:173], v[212:215], v[10:13]
	v_mfma_f32_16x16x32_bf16 v[62:65], v[150:153], v[190:193], v[62:65]
	v_mfma_f32_16x16x32_bf16 v[58:61], v[174:177], v[190:193], v[58:61]
	v_mfma_f32_16x16x32_bf16 v[42:45], v[150:153], v[200:203], v[42:45]
	v_mfma_f32_16x16x32_bf16 v[38:41], v[174:177], v[200:203], v[38:41]
	v_mfma_f32_16x16x32_bf16 v[30:33], v[150:153], v[208:211], v[30:33]
	v_mfma_f32_16x16x32_bf16 v[26:29], v[174:177], v[208:211], v[26:29]
	v_mfma_f32_16x16x32_bf16 v[14:17], v[150:153], v[216:219], v[14:17]
	v_mfma_f32_16x16x32_bf16 v[10:13], v[174:177], v[216:219], v[10:13]
	s_setprio 0
	s_barrier
; #define PG8_STAGE(bufoff, gbase, voff) do { _Pragma("unroll") for (int _i = 0; _i < 2; ++_i) \
;         __builtin_amdgcn_global_load_lds((const unsigned*)((const char*)(gbase) + (voff)[_i]), (LAS unsigned*)(lds + (bufoff) + ldsw + _i * 8192), 16, 0, 0); } while (0)
; #define PG8_LDA(dst, b, h) do { if constexpr (F8) { _Pragma("unroll") for (int m = 0; m < 4; ++m) dst##8[m] = PG8_LD8(lds, PG8_SA(b, h) + aoff + m * 2048); } \
;         else { _Pragma("unroll") for (int m = 0; m < 4; ++m) _Pragma("unroll") for (int k = 0; k < 2; ++k) dst[m][k] = *(const LAS bf16x8*)(lds + PG8_SA(b, h) + aoff + m * 2048 + k * 1024); } } while (0)
; #define PG8_LDB(dst, b, h) do { if constexpr (F8) { _Pragma("unroll") for (int n = 0; n < 2; ++n) dst##8[n] = PG8_LD8(ldsB, PG8_SBR(b, h) + boff + n * 2048); } \
;         else { _Pragma("unroll") for (int n = 0; n < 2; ++n) _Pragma("unroll") for (int k = 0; k < 2; ++k) dst[n][k] = *(const LAS bf16x8*)(ldsB + PG8_SBR(b, h) + boff + n * 2048 + k * 1024); } } while (0)
; #define PG8_WAIT_V(n) asm volatile("s_waitcnt vmcnt(" #n ")" ::: "memory")
; #define PG8_WAIT_L(n) asm volatile("s_waitcnt lgkmcnt(" #n ")" ::: "memory")
; #define PG8_BAR __builtin_amdgcn_s_barrier()
; #define PG8_SCHED __builtin_amdgcn_sched_barrier(0)
; template <bool GATHER, bool F8, class Epi, class Sched>
; __device__ __forceinline__ void gemm_phase(LAS unsigned char* lds, const int nt, const unsigned lda, const unsigned ldb, const Sched& S, const Epi& E) {
;     ...
;             PG8_LDB(B0, 1, 0); PG8_LDB(B1, 1, 1); PG8_SCHED; PG8_LDA(At, 1, 0); PG8_STAGE(PG8_SA(0, 1), a2 + hA, w1);
;             PG8_WAIT_V(8); PG8_WAIT_L(0); PG8_BAR; PG8_MMA(0, 0, At, B0); PG8_MMA(0, 1, At, B1); PG8_BAR; PG8_SCHED;
;             PG8_LDA(At, 1, 1); PG8_STAGE(PG8_SB(1, 0), b3, voffB); PG8_STAGE(PG8_SB(1, 1), b3 + hB, voffB); PG8_STAGE(PG8_SA(1, 0), a3, w0);
;             PG8_WAIT_V(8); PG8_WAIT_L(0); PG8_BAR; PG8_MMA(1, 0, At, B0); PG8_MMA(1, 1, At, B1); PG8_BAR; PG8_SCHED;
;         }
;         if (wr == 0) PG8_BAR;
	s_add_i32 s54, 0, 0x18000
	s_add_i32 s55, 0, 0x1c000
	v_add_u32_e32 v142, s54, v182
	v_add_u32_e32 v174, s55, v182
	ds_read_b128 v[130:133], v142
	ds_read_b128 v[134:137], v142 offset:1024
	ds_read_b128 v[138:141], v142 offset:2048
	ds_read_b128 v[142:145], v142 offset:3072
	ds_read_b128 v[146:149], v174
	ds_read_b128 v[150:153], v174 offset:1024
	ds_read_b128 v[170:173], v174 offset:2048
	ds_read_b128 v[174:177], v174 offset:3072
	s_add_u32 s30, s30, 0x20000
	s_addc_u32 s31, s31, 0
	s_mov_b32 m0, s42
	ds_read_b128 v[178:181], v186 offset:32768
	ds_read_b128 v[190:193], v186 offset:33792
	ds_read_b128 v[194:197], v186 offset:34816
	ds_read_b128 v[200:203], v186 offset:35840
	ds_read_b128 v[204:207], v186 offset:36864
	ds_read_b128 v[208:211], v186 offset:37888
	ds_read_b128 v[212:215], v186 offset:38912
	ds_read_b128 v[216:219], v186 offset:39936
	global_load_lds_dwordx4 v154, s[30:31]
	s_mov_b32 m0, s43
	s_nop 0
	global_load_lds_dwordx4 v158, s[30:31]
	s_waitcnt vmcnt(8)
	s_waitcnt lgkmcnt(0)
	s_barrier
	s_setprio 1
	s_waitcnt lgkmcnt(0)
	v_mfma_f32_16x16x32_bf16 v[126:129], v[130:133], v[178:181], v[126:129]
	v_mfma_f32_16x16x32_bf16 v[122:125], v[138:141], v[178:181], v[122:125]
	v_mfma_f32_16x16x32_bf16 v[110:113], v[130:133], v[194:197], v[110:113]
	v_mfma_f32_16x16x32_bf16 v[106:109], v[138:141], v[194:197], v[106:109]
	v_mfma_f32_16x16x32_bf16 v[94:97], v[130:133], v[204:207], v[94:97]
	v_mfma_f32_16x16x32_bf16 v[90:93], v[138:141], v[204:207], v[90:93]
	v_mfma_f32_16x16x32_bf16 v[78:81], v[130:133], v[212:215], v[78:81]
	v_mfma_f32_16x16x32_bf16 v[74:77], v[138:141], v[212:215], v[74:77]
	v_mfma_f32_16x16x32_bf16 v[126:129], v[134:137], v[190:193], v[126:129]
	v_mfma_f32_16x16x32_bf16 v[122:125], v[142:145], v[190:193], v[122:125]
	v_mfma_f32_16x16x32_bf16 v[110:113], v[134:137], v[200:203], v[110:113]
	v_mfma_f32_16x16x32_bf16 v[106:109], v[142:145], v[200:203], v[106:109]
	v_mfma_f32_16x16x32_bf16 v[94:97], v[134:137], v[208:211], v[94:97]
	v_mfma_f32_16x16x32_bf16 v[90:93], v[142:145], v[208:211], v[90:93]
	v_mfma_f32_16x16x32_bf16 v[78:81], v[134:137], v[216:219], v[78:81]
	v_mfma_f32_16x16x32_bf16 v[74:77], v[142:145], v[216:219], v[74:77]
	s_setprio 0
	s_setprio 1
	v_mfma_f32_16x16x32_bf16 v[118:121], v[146:149], v[178:181], v[118:121]
	v_mfma_f32_16x16x32_bf16 v[114:117], v[170:173], v[178:181], v[114:117]
	v_mfma_f32_16x16x32_bf16 v[102:105], v[146:149], v[194:197], v[102:105]
	v_mfma_f32_16x16x32_bf16 v[98:101], v[170:173], v[194:197], v[98:101]
	v_mfma_f32_16x16x32_bf16 v[86:89], v[146:149], v[204:207], v[86:89]
	v_mfma_f32_16x16x32_bf16 v[82:85], v[170:173], v[204:207], v[82:85]
	v_mfma_f32_16x16x32_bf16 v[70:73], v[146:149], v[212:215], v[70:73]
	v_mfma_f32_16x16x32_bf16 v[66:69], v[170:173], v[212:215], v[66:69]
	v_mfma_f32_16x16x32_bf16 v[118:121], v[150:153], v[190:193], v[118:121]
	v_mfma_f32_16x16x32_bf16 v[114:117], v[174:177], v[190:193], v[114:117]
	v_mfma_f32_16x16x32_bf16 v[102:105], v[150:153], v[200:203], v[102:105]
	v_mfma_f32_16x16x32_bf16 v[98:101], v[174:177], v[200:203], v[98:101]
	v_mfma_f32_16x16x32_bf16 v[86:89], v[150:153], v[208:211], v[86:89]
	v_mfma_f32_16x16x32_bf16 v[82:85], v[174:177], v[208:211], v[82:85]
	v_mfma_f32_16x16x32_bf16 v[70:73], v[150:153], v[216:219], v[70:73]
	v_mfma_f32_16x16x32_bf16 v[66:69], v[174:177], v[216:219], v[66:69]
	s_setprio 0
	s_barrier
	s_add_i32 s30, s54, s39
	s_add_i32 m0, s30, 0xffffff80
	ds_read_b128 v[178:181], v186 offset:49152
	ds_read_b128 v[190:193], v186 offset:50176
	ds_read_b128 v[194:197], v186 offset:51200
	ds_read_b128 v[200:203], v186 offset:52224
	ds_read_b128 v[204:207], v186 offset:53248
	ds_read_b128 v[208:211], v186 offset:54272
	ds_read_b128 v[212:215], v186 offset:55296
	ds_read_b128 v[216:219], v186 offset:56320
	global_load_lds_dwordx4 v156, s[28:29] offset:128
	s_add_i32 m0, s30, 0x1f80
	s_add_i32 s30, s55, s39
	global_load_lds_dwordx4 v160, s[28:29] offset:128
	s_add_u32 s28, s28, 0x20080
	s_addc_u32 s29, s29, 0
	s_mov_b32 m0, s30
	s_nop 0
	global_load_lds_dwordx4 v156, s[28:29]
	s_add_i32 m0, s30, 0x2000
	s_nop 0
	global_load_lds_dwordx4 v160, s[28:29]
	s_add_i32 m0, s45, 0xffffff80
	s_nop 0
	global_load_lds_dwordx4 v154, s[98:99] offset:128
	s_add_i32 m0, s46, 0xffffff80
	s_nop 0
	global_load_lds_dwordx4 v158, s[98:99] offset:128
	s_waitcnt vmcnt(8)
	s_waitcnt lgkmcnt(0)
	s_barrier
	s_setprio 1
	s_waitcnt lgkmcnt(0)
	v_mfma_f32_16x16x32_bf16 v[54:57], v[130:133], v[178:181], v[54:57]
	v_mfma_f32_16x16x32_bf16 v[50:53], v[138:141], v[178:181], v[50:53]
	v_mfma_f32_16x16x32_bf16 v[46:49], v[130:133], v[194:197], v[46:49]
	v_mfma_f32_16x16x32_bf16 v[34:37], v[138:141], v[194:197], v[34:37]
	v_mfma_f32_16x16x32_bf16 v[22:25], v[130:133], v[204:207], v[22:25]
	v_mfma_f32_16x16x32_bf16 v[18:21], v[138:141], v[204:207], v[18:21]
	v_mfma_f32_16x16x32_bf16 v[6:9], v[130:133], v[212:215], v[6:9]
	v_mfma_f32_16x16x32_bf16 v[2:5], v[138:141], v[212:215], v[2:5]
	v_mfma_f32_16x16x32_bf16 v[54:57], v[134:137], v[190:193], v[54:57]
	v_mfma_f32_16x16x32_bf16 v[50:53], v[142:145], v[190:193], v[50:53]
	v_mfma_f32_16x16x32_bf16 v[46:49], v[134:137], v[200:203], v[46:49]
	v_mfma_f32_16x16x32_bf16 v[34:37], v[142:145], v[200:203], v[34:37]
	v_mfma_f32_16x16x32_bf16 v[22:25], v[134:137], v[208:211], v[22:25]
	v_mfma_f32_16x16x32_bf16 v[18:21], v[142:145], v[208:211], v[18:21]
	v_mfma_f32_16x16x32_bf16 v[6:9], v[134:137], v[216:219], v[6:9]
	v_mfma_f32_16x16x32_bf16 v[2:5], v[142:145], v[216:219], v[2:5]
	s_setprio 0
	s_setprio 1
	v_mfma_f32_16x16x32_bf16 v[62:65], v[146:149], v[178:181], v[62:65]
	v_mfma_f32_16x16x32_bf16 v[58:61], v[170:173], v[178:181], v[58:61]
	v_mfma_f32_16x16x32_bf16 v[42:45], v[146:149], v[194:197], v[42:45]
	v_mfma_f32_16x16x32_bf16 v[38:41], v[170:173], v[194:197], v[38:41]
	v_mfma_f32_16x16x32_bf16 v[30:33], v[146:149], v[204:207], v[30:33]
	v_mfma_f32_16x16x32_bf16 v[26:29], v[170:173], v[204:207], v[26:29]
	v_mfma_f32_16x16x32_bf16 v[14:17], v[146:149], v[212:215], v[14:17]
	v_mfma_f32_16x16x32_bf16 v[10:13], v[170:173], v[212:215], v[10:13]
	v_mfma_f32_16x16x32_bf16 v[62:65], v[150:153], v[190:193], v[62:65]
	v_mfma_f32_16x16x32_bf16 v[58:61], v[174:177], v[190:193], v[58:61]
	v_mfma_f32_16x16x32_bf16 v[42:45], v[150:153], v[200:203], v[42:45]
	v_mfma_f32_16x16x32_bf16 v[38:41], v[174:177], v[200:203], v[38:41]
	v_mfma_f32_16x16x32_bf16 v[30:33], v[150:153], v[208:211], v[30:33]
	v_mfma_f32_16x16x32_bf16 v[26:29], v[174:177], v[208:211], v[26:29]
	v_mfma_f32_16x16x32_bf16 v[14:17], v[150:153], v[216:219], v[14:17]
	v_mfma_f32_16x16x32_bf16 v[10:13], v[174:177], v[216:219], v[10:13]
	s_setprio 0
	s_barrier
	s_add_i32 s53, s53, 2
	s_add_u32 s26, s26, 0x100
	s_addc_u32 s27, s27, 0
	s_add_u32 s25, s25, 0x100
	s_addc_u32 s34, s34, 0
	s_cmp_gt_u32 s53, 5
	s_cbranch_scc0 .LBB0_1432
	s_and_b64 vcc, exec, s[20:21]
	s_cbranch_vccz .LBB0_1435
	s_barrier

; #define PG8_STAGE(bufoff, gbase, voff) do { _Pragma("unroll") for (int _i = 0; _i < 2; ++_i) \
;         __builtin_amdgcn_global_load_lds((const unsigned*)((const char*)(gbase) + (voff)[_i]), (LAS unsigned*)(lds + (bufoff) + ldsw + _i * 8192), 16, 0, 0); } while (0)
; #define PG8_LDA(dst, b, h) do { if constexpr (F8) { _Pragma("unroll") for (int m = 0; m < 4; ++m) dst##8[m] = PG8_LD8(lds, PG8_SA(b, h) + aoff + m * 2048); } \
;         else { _Pragma("unroll") for (int m = 0; m < 4; ++m) _Pragma("unroll") for (int k = 0; k < 2; ++k) dst[m][k] = *(const LAS bf16x8*)(lds + PG8_SA(b, h) + aoff + m * 2048 + k * 1024); } } while (0)
; #define PG8_LDB(dst, b, h) do { if constexpr (F8) { _Pragma("unroll") for (int n = 0; n < 2; ++n) dst##8[n] = PG8_LD8(ldsB, PG8_SBR(b, h) + boff + n * 2048); } \
;         else { _Pragma("unroll") for (int n = 0; n < 2; ++n) _Pragma("unroll") for (int k = 0; k < 2; ++k) dst[n][k] = *(const LAS bf16x8*)(ldsB + PG8_SBR(b, h) + boff + n * 2048 + k * 1024); } } while (0)
; template <bool GATHER, bool F8, class Epi, class Sched>
; __device__ __forceinline__ void gemm_phase(LAS unsigned char* lds, const int nt, const unsigned lda, const unsigned ldb, const Sched& S, const Epi& E) {
;     ...
;             const bool last = (t == nt - 2);
;             const char* a1 = cA + (size_t)(t + 1) * kstep;
;             const char* a2 = last ? nA : cA + (size_t)(t + 2) * kstep; const char* b2 = last ? nB : cB + (size_t)(t + 2) * kstep;
;             const char* a3 = a2 + kstep; const char* b3 = b2 + kstep;
;             unsigned w0[2], w1[2];
;             if constexpr (GATHER) {
; #pragma unroll
;                 for (int i = 0; i < 2; ++i) { w0[i] = last ? vN0[i] : vA0[i]; w1[i] = last ? vN1[i] : vA1[i]; }
;             } else {
; #pragma unroll
;                 for (int i = 0; i < 2; ++i) { w0[i] = voffA[i]; w1[i] = voffA[i]; }
;             }
;             PG8_LDB(B0, 0, 0); PG8_LDB(B1, 0, 1); PG8_SCHED; PG8_LDA(At, 0, 0); PG8_STAGE(PG8_SA(1, 1), a1 + hA, vA1);
;             PG8_WAIT_V(8); PG8_WAIT_L(0); PG8_BAR; PG8_MMA(0, 0, At, B0); PG8_MMA(0, 1, At, B1); PG8_BAR; PG8_SCHED;
;             PG8_LDA(At, 0, 1); PG8_STAGE(PG8_SB(0, 0), b2, voffB); PG8_STAGE(PG8_SB(0, 1), b2 + hB, voffB); PG8_STAGE(PG8_SA(0, 0), a2, w0);
;             PG8_WAIT_V(8); PG8_WAIT_L(0); PG8_BAR; PG8_MMA(1, 0, At, B0); PG8_MMA(1, 1, At, B1); PG8_BAR; PG8_SCHED;
.LBB0_1927:
	ds_read_b128 v[18:21], v201
	ds_read_b128 v[22:25], v201 offset:1024
	ds_read_b128 v[26:29], v201 offset:2048
	ds_read_b128 v[30:33], v201 offset:3072
	ds_read_b128 v[2:5], v201 offset:16384
	ds_read_b128 v[6:9], v201 offset:17408
	ds_read_b128 v[10:13], v201 offset:18432
	ds_read_b128 v[14:17], v201 offset:19456
	s_add_u32 s34, s28, s0
	s_addc_u32 s35, s29, s1
	s_mov_b64 s[100:101], s[34:35]
	s_add_u32 s36, s34, 0x100
	s_addc_u32 s37, s35, 0
	s_add_u32 s67, s7, s0
	s_addc_u32 s68, s38, s1
	s_cmpk_eq_i32 s0, 0x700
	s_cselect_b64 vcc, -1, 0
	s_cbranch_scc0 .Lp10_not_last
	v_lshl_or_b32 v208, v208, 11, v188
	v_lshl_or_b32 v205, v205, 11, v188
	v_lshl_or_b32 v207, v207, 11, v188
	v_lshl_or_b32 v206, v206, 11, v188
.Lp10_not_last:
	s_and_b64 s[34:35], vcc, exec
	v_cndmask_b32_e32 v164, v209, v208, vcc
	s_cselect_b32 s37, s23, s37
	s_cselect_b32 s36, s22, s36
	v_cndmask_b32_e32 v173, v172, v205, vcc
	v_cndmask_b32_e32 v242, v170, v207, vcc
	v_cndmask_b32_e32 v175, v174, v206, vcc
	s_cselect_b32 s35, s25, s68
	s_cselect_b32 s34, s24, s67
	s_add_i32 m0, s40, 0xbf80
	ds_read_b128 v[180:183], v202
	ds_read_b128 v[184:187], v202 offset:1024
	ds_read_b128 v[210:213], v202 offset:2048
	ds_read_b128 v[214:217], v202 offset:3072
	ds_read_b128 v[218:221], v202 offset:4096
	ds_read_b128 v[222:225], v202 offset:5120
	ds_read_b128 v[226:229], v202 offset:6144
	ds_read_b128 v[230:233], v202 offset:7168
	global_load_lds_dwordx4 v172, s[100:101] offset:128
	s_add_i32 m0, s40, 0xdf80
	s_nop 0
	global_load_lds_dwordx4 v174, s[100:101] offset:128
	s_waitcnt vmcnt(8)
	s_waitcnt lgkmcnt(0)
	s_barrier
	s_setprio 1
	s_waitcnt lgkmcnt(0)
	v_mfma_scale_f32_16x16x128_f8f6f4 v[158:161], v[18:25], v[180:187], v[158:161], v203, v203 op_sel_hi:[0,0,0]
	v_mfma_scale_f32_16x16x128_f8f6f4 v[150:153], v[26:33], v[180:187], v[150:153], v203, v203 op_sel_hi:[0,0,0]
	v_mfma_scale_f32_16x16x128_f8f6f4 v[142:145], v[18:25], v[210:217], v[142:145], v203, v203 op_sel_hi:[0,0,0]
	v_mfma_scale_f32_16x16x128_f8f6f4 v[134:137], v[26:33], v[210:217], v[134:137], v203, v203 op_sel_hi:[0,0,0]
	v_mfma_scale_f32_16x16x128_f8f6f4 v[126:129], v[18:25], v[218:225], v[126:129], v203, v203 op_sel_hi:[0,0,0]
	v_mfma_scale_f32_16x16x128_f8f6f4 v[118:121], v[26:33], v[218:225], v[118:121], v203, v203 op_sel_hi:[0,0,0]
	v_mfma_scale_f32_16x16x128_f8f6f4 v[110:113], v[18:25], v[226:233], v[110:113], v203, v203 op_sel_hi:[0,0,0]
	v_mfma_scale_f32_16x16x128_f8f6f4 v[102:105], v[26:33], v[226:233], v[102:105], v203, v203 op_sel_hi:[0,0,0]
	s_setprio 0
	s_setprio 1
	v_mfma_scale_f32_16x16x128_f8f6f4 v[154:157], v[2:9], v[180:187], v[154:157], v203, v203 op_sel_hi:[0,0,0]
	v_mfma_scale_f32_16x16x128_f8f6f4 v[146:149], v[10:17], v[180:187], v[146:149], v203, v203 op_sel_hi:[0,0,0]
	v_mfma_scale_f32_16x16x128_f8f6f4 v[138:141], v[2:9], v[210:217], v[138:141], v203, v203 op_sel_hi:[0,0,0]
	v_mfma_scale_f32_16x16x128_f8f6f4 v[130:133], v[10:17], v[210:217], v[130:133], v203, v203 op_sel_hi:[0,0,0]
	v_mfma_scale_f32_16x16x128_f8f6f4 v[122:125], v[2:9], v[218:225], v[122:125], v203, v203 op_sel_hi:[0,0,0]
	v_mfma_scale_f32_16x16x128_f8f6f4 v[114:117], v[10:17], v[218:225], v[114:117], v203, v203 op_sel_hi:[0,0,0]
	v_mfma_scale_f32_16x16x128_f8f6f4 v[106:109], v[2:9], v[226:233], v[106:109], v203, v203 op_sel_hi:[0,0,0]
	v_mfma_scale_f32_16x16x128_f8f6f4 v[98:101], v[10:17], v[226:233], v[98:101], v203, v203 op_sel_hi:[0,0,0]
	s_setprio 0
	s_barrier
	s_mov_b32 m0, s41
	s_add_u32 s68, s34, 0x40000
	ds_read_b128 v[210:213], v202 offset:16384
	ds_read_b128 v[214:217], v202 offset:17408
	ds_read_b128 v[218:221], v202 offset:18432
	ds_read_b128 v[222:225], v202 offset:19456
	ds_read_b128 v[226:229], v202 offset:20480
	ds_read_b128 v[230:233], v202 offset:21504
	ds_read_b128 v[234:237], v202 offset:22528
	ds_read_b128 v[238:241], v202 offset:23552
	global_load_lds_dwordx4 v166, s[34:35]
	s_mov_b32 m0, s42
	s_addc_u32 s69, s35, 0
	global_load_lds_dwordx4 v168, s[34:35]
	s_mov_b32 m0, s43
	s_nop 0
	global_load_lds_dwordx4 v166, s[68:69]
	s_mov_b32 m0, s44
	s_nop 0
	global_load_lds_dwordx4 v168, s[68:69]
	s_mov_b32 m0, s40
	s_nop 0
	global_load_lds_dwordx4 v164, s[36:37]
	s_mov_b32 m0, s45
	s_nop 0
	global_load_lds_dwordx4 v242, s[36:37]
	s_waitcnt vmcnt(8)
	s_waitcnt lgkmcnt(0)
	s_barrier
	s_setprio 1
	s_waitcnt lgkmcnt(0)
	v_mfma_scale_f32_16x16x128_f8f6f4 v[94:97], v[18:25], v[210:217], v[94:97], v203, v203 op_sel_hi:[0,0,0]
	v_mfma_scale_f32_16x16x128_f8f6f4 v[86:89], v[26:33], v[210:217], v[86:89], v203, v203 op_sel_hi:[0,0,0]
	v_mfma_scale_f32_16x16x128_f8f6f4 v[78:81], v[18:25], v[218:225], v[78:81], v203, v203 op_sel_hi:[0,0,0]
	v_mfma_scale_f32_16x16x128_f8f6f4 v[70:73], v[26:33], v[218:225], v[70:73], v203, v203 op_sel_hi:[0,0,0]
	v_mfma_scale_f32_16x16x128_f8f6f4 v[54:57], v[18:25], v[226:233], v[54:57], v203, v203 op_sel_hi:[0,0,0]
	v_mfma_scale_f32_16x16x128_f8f6f4 v[50:53], v[26:33], v[226:233], v[50:53], v203, v203 op_sel_hi:[0,0,0]
	v_mfma_scale_f32_16x16x128_f8f6f4 v[38:41], v[18:25], v[234:241], v[38:41], v203, v203 op_sel_hi:[0,0,0]
	v_mfma_scale_f32_16x16x128_f8f6f4 v[34:37], v[26:33], v[234:241], v[34:37], v203, v203 op_sel_hi:[0,0,0]
	s_setprio 0
	s_setprio 1
	v_mfma_scale_f32_16x16x128_f8f6f4 v[90:93], v[2:9], v[210:217], v[90:93], v203, v203 op_sel_hi:[0,0,0]
	v_mfma_scale_f32_16x16x128_f8f6f4 v[82:85], v[10:17], v[210:217], v[82:85], v203, v203 op_sel_hi:[0,0,0]
	v_mfma_scale_f32_16x16x128_f8f6f4 v[74:77], v[2:9], v[218:225], v[74:77], v203, v203 op_sel_hi:[0,0,0]
	v_mfma_scale_f32_16x16x128_f8f6f4 v[62:65], v[10:17], v[218:225], v[62:65], v203, v203 op_sel_hi:[0,0,0]
	v_mfma_scale_f32_16x16x128_f8f6f4 v[66:69], v[2:9], v[226:233], v[66:69], v203, v203 op_sel_hi:[0,0,0]
	v_mfma_scale_f32_16x16x128_f8f6f4 v[58:61], v[10:17], v[226:233], v[58:61], v203, v203 op_sel_hi:[0,0,0]
	v_mfma_scale_f32_16x16x128_f8f6f4 v[46:49], v[2:9], v[234:241], v[46:49], v203, v203 op_sel_hi:[0,0,0]
	v_mfma_scale_f32_16x16x128_f8f6f4 v[42:45], v[10:17], v[234:241], v[42:45], v203, v203 op_sel_hi:[0,0,0]
	s_setprio 0
	s_barrier
; #define PG8_STAGE(bufoff, gbase, voff) do { _Pragma("unroll") for (int _i = 0; _i < 2; ++_i) \
;         __builtin_amdgcn_global_load_lds((const unsigned*)((const char*)(gbase) + (voff)[_i]), (LAS unsigned*)(lds + (bufoff) + ldsw + _i * 8192), 16, 0, 0); } while (0)
; #define PG8_LDA(dst, b, h) do { if constexpr (F8) { _Pragma("unroll") for (int m = 0; m < 4; ++m) dst##8[m] = PG8_LD8(lds, PG8_SA(b, h) + aoff + m * 2048); } \
;         else { _Pragma("unroll") for (int m = 0; m < 4; ++m) _Pragma("unroll") for (int k = 0; k < 2; ++k) dst[m][k] = *(const LAS bf16x8*)(lds + PG8_SA(b, h) + aoff + m * 2048 + k * 1024); } } while (0)
; #define PG8_LDB(dst, b, h) do { if constexpr (F8) { _Pragma("unroll") for (int n = 0; n < 2; ++n) dst##8[n] = PG8_LD8(ldsB, PG8_SBR(b, h) + boff + n * 2048); } \
;         else { _Pragma("unroll") for (int n = 0; n < 2; ++n) _Pragma("unroll") for (int k = 0; k < 2; ++k) dst[n][k] = *(const LAS bf16x8*)(ldsB + PG8_SBR(b, h) + boff + n * 2048 + k * 1024); } } while (0)
; #define PG8_WAIT_V(n) asm volatile("s_waitcnt vmcnt(" #n ")" ::: "memory")
; #define PG8_WAIT_L(n) asm volatile("s_waitcnt lgkmcnt(" #n ")" ::: "memory")
; #define PG8_BAR __builtin_amdgcn_s_barrier()
; #define PG8_SCHED __builtin_amdgcn_sched_barrier(0)
; template <bool GATHER, bool F8, class Epi, class Sched>
; __device__ __forceinline__ void gemm_phase(LAS unsigned char* lds, const int nt, const unsigned lda, const unsigned ldb, const Sched& S, const Epi& E) {
;     ...
;             PG8_LDB(B0, 1, 0); PG8_LDB(B1, 1, 1); PG8_SCHED; PG8_LDA(At, 1, 0); PG8_STAGE(PG8_SA(0, 1), a2 + hA, w1);
;             PG8_WAIT_V(8); PG8_WAIT_L(0); PG8_BAR; PG8_MMA(0, 0, At, B0); PG8_MMA(0, 1, At, B1); PG8_BAR; PG8_SCHED;
;             PG8_LDA(At, 1, 1); PG8_STAGE(PG8_SB(1, 0), b3, voffB); PG8_STAGE(PG8_SB(1, 1), b3 + hB, voffB); PG8_STAGE(PG8_SA(1, 0), a3, w0);
;             PG8_WAIT_V(8); PG8_WAIT_L(0); PG8_BAR; PG8_MMA(1, 0, At, B0); PG8_MMA(1, 1, At, B1); PG8_BAR; PG8_SCHED;
;         }
;         if (wr == 0) PG8_BAR;
	ds_read_b128 v[2:5], v201 offset:32768
	ds_read_b128 v[6:9], v201 offset:33792
	ds_read_b128 v[10:13], v201 offset:34816
	ds_read_b128 v[14:17], v201 offset:35840
	ds_read_b128 v[18:21], v201 offset:49152
	ds_read_b128 v[22:25], v201 offset:50176
	ds_read_b128 v[26:29], v201 offset:51200
	ds_read_b128 v[30:33], v201 offset:52224
	s_mov_b32 m0, s46
	ds_read_b128 v[210:213], v202 offset:32768
	ds_read_b128 v[214:217], v202 offset:33792
	ds_read_b128 v[218:221], v202 offset:34816
	ds_read_b128 v[222:225], v202 offset:35840
	ds_read_b128 v[226:229], v202 offset:36864
	ds_read_b128 v[230:233], v202 offset:37888
	ds_read_b128 v[234:237], v202 offset:38912
	ds_read_b128 v[238:241], v202 offset:39936
	global_load_lds_dwordx4 v173, s[36:37]
	s_mov_b32 m0, s47
	s_nop 0
	global_load_lds_dwordx4 v175, s[36:37]
	s_waitcnt vmcnt(8)
	s_waitcnt lgkmcnt(0)
	s_barrier
	s_setprio 1
	s_waitcnt lgkmcnt(0)
	v_mfma_scale_f32_16x16x128_f8f6f4 v[158:161], v[2:9], v[210:217], v[158:161], v203, v203 op_sel_hi:[0,0,0]
	v_mfma_scale_f32_16x16x128_f8f6f4 v[150:153], v[10:17], v[210:217], v[150:153], v203, v203 op_sel_hi:[0,0,0]
	v_mfma_scale_f32_16x16x128_f8f6f4 v[142:145], v[2:9], v[218:225], v[142:145], v203, v203 op_sel_hi:[0,0,0]
	v_mfma_scale_f32_16x16x128_f8f6f4 v[134:137], v[10:17], v[218:225], v[134:137], v203, v203 op_sel_hi:[0,0,0]
	v_mfma_scale_f32_16x16x128_f8f6f4 v[126:129], v[2:9], v[226:233], v[126:129], v203, v203 op_sel_hi:[0,0,0]
	v_mfma_scale_f32_16x16x128_f8f6f4 v[118:121], v[10:17], v[226:233], v[118:121], v203, v203 op_sel_hi:[0,0,0]
	v_mfma_scale_f32_16x16x128_f8f6f4 v[110:113], v[2:9], v[234:241], v[110:113], v203, v203 op_sel_hi:[0,0,0]
	v_mfma_scale_f32_16x16x128_f8f6f4 v[102:105], v[10:17], v[234:241], v[102:105], v203, v203 op_sel_hi:[0,0,0]
	s_setprio 0
	s_setprio 1
	v_mfma_scale_f32_16x16x128_f8f6f4 v[154:157], v[18:25], v[210:217], v[154:157], v203, v203 op_sel_hi:[0,0,0]
	v_mfma_scale_f32_16x16x128_f8f6f4 v[146:149], v[26:33], v[210:217], v[146:149], v203, v203 op_sel_hi:[0,0,0]
	v_mfma_scale_f32_16x16x128_f8f6f4 v[138:141], v[18:25], v[218:225], v[138:141], v203, v203 op_sel_hi:[0,0,0]
	v_mfma_scale_f32_16x16x128_f8f6f4 v[130:133], v[26:33], v[218:225], v[130:133], v203, v203 op_sel_hi:[0,0,0]
	v_mfma_scale_f32_16x16x128_f8f6f4 v[122:125], v[18:25], v[226:233], v[122:125], v203, v203 op_sel_hi:[0,0,0]
	v_mfma_scale_f32_16x16x128_f8f6f4 v[114:117], v[26:33], v[226:233], v[114:117], v203, v203 op_sel_hi:[0,0,0]
	v_mfma_scale_f32_16x16x128_f8f6f4 v[106:109], v[18:25], v[234:241], v[106:109], v203, v203 op_sel_hi:[0,0,0]
	v_mfma_scale_f32_16x16x128_f8f6f4 v[98:101], v[26:33], v[234:241], v[98:101], v203, v203 op_sel_hi:[0,0,0]
	s_setprio 0
	s_barrier
	s_add_i32 m0, s50, 0xffffff80
	ds_read_b128 v[210:213], v202 offset:49152
	ds_read_b128 v[214:217], v202 offset:50176
	ds_read_b128 v[218:221], v202 offset:51200
	ds_read_b128 v[222:225], v202 offset:52224
	ds_read_b128 v[226:229], v202 offset:53248
	ds_read_b128 v[230:233], v202 offset:54272
	ds_read_b128 v[234:237], v202 offset:55296
	ds_read_b128 v[238:241], v202 offset:56320
	global_load_lds_dwordx4 v166, s[34:35] offset:128
	s_add_i32 m0, s51, 0xffffff80
	s_nop 0
	global_load_lds_dwordx4 v168, s[34:35] offset:128
	s_add_u32 s34, s34, 0x40080
	s_addc_u32 s35, s35, 0
	s_mov_b32 m0, s54
	s_nop 0
	global_load_lds_dwordx4 v166, s[34:35]
	s_mov_b32 m0, s55
	s_nop 0
	global_load_lds_dwordx4 v168, s[34:35]
	s_add_i32 m0, s52, 0xffffff80
	s_nop 0
	global_load_lds_dwordx4 v164, s[36:37] offset:128
	s_add_i32 m0, s53, 0xffffff80
	s_nop 0
	global_load_lds_dwordx4 v242, s[36:37] offset:128
	s_waitcnt vmcnt(8)
	s_waitcnt lgkmcnt(0)
	s_barrier
	s_setprio 1
	s_waitcnt lgkmcnt(0)
	v_mfma_scale_f32_16x16x128_f8f6f4 v[94:97], v[2:9], v[210:217], v[94:97], v203, v203 op_sel_hi:[0,0,0]
	v_mfma_scale_f32_16x16x128_f8f6f4 v[86:89], v[10:17], v[210:217], v[86:89], v203, v203 op_sel_hi:[0,0,0]
	v_mfma_scale_f32_16x16x128_f8f6f4 v[78:81], v[2:9], v[218:225], v[78:81], v203, v203 op_sel_hi:[0,0,0]
	v_mfma_scale_f32_16x16x128_f8f6f4 v[70:73], v[10:17], v[218:225], v[70:73], v203, v203 op_sel_hi:[0,0,0]
	v_mfma_scale_f32_16x16x128_f8f6f4 v[54:57], v[2:9], v[226:233], v[54:57], v203, v203 op_sel_hi:[0,0,0]
	v_mfma_scale_f32_16x16x128_f8f6f4 v[50:53], v[10:17], v[226:233], v[50:53], v203, v203 op_sel_hi:[0,0,0]
	v_mfma_scale_f32_16x16x128_f8f6f4 v[38:41], v[2:9], v[234:241], v[38:41], v203, v203 op_sel_hi:[0,0,0]
	v_mfma_scale_f32_16x16x128_f8f6f4 v[34:37], v[10:17], v[234:241], v[34:37], v203, v203 op_sel_hi:[0,0,0]
	s_setprio 0
	s_setprio 1
	v_mfma_scale_f32_16x16x128_f8f6f4 v[90:93], v[18:25], v[210:217], v[90:93], v203, v203 op_sel_hi:[0,0,0]
	v_mfma_scale_f32_16x16x128_f8f6f4 v[82:85], v[26:33], v[210:217], v[82:85], v203, v203 op_sel_hi:[0,0,0]
	v_mfma_scale_f32_16x16x128_f8f6f4 v[74:77], v[18:25], v[218:225], v[74:77], v203, v203 op_sel_hi:[0,0,0]
	v_mfma_scale_f32_16x16x128_f8f6f4 v[62:65], v[26:33], v[218:225], v[62:65], v203, v203 op_sel_hi:[0,0,0]
	v_mfma_scale_f32_16x16x128_f8f6f4 v[66:69], v[18:25], v[226:233], v[66:69], v203, v203 op_sel_hi:[0,0,0]
	v_mfma_scale_f32_16x16x128_f8f6f4 v[58:61], v[26:33], v[226:233], v[58:61], v203, v203 op_sel_hi:[0,0,0]
	v_mfma_scale_f32_16x16x128_f8f6f4 v[46:49], v[18:25], v[234:241], v[46:49], v203, v203 op_sel_hi:[0,0,0]
	v_mfma_scale_f32_16x16x128_f8f6f4 v[42:45], v[26:33], v[234:241], v[42:45], v203, v203 op_sel_hi:[0,0,0]
	s_setprio 0
	s_barrier
	s_add_i32 s39, s39, 2
	s_add_u32 s0, s0, 0x100
	s_addc_u32 s1, s1, 0
	s_cmp_gt_u32 s39, 13
	s_cbranch_scc0 .LBB0_1927
	s_and_b64 vcc, exec, s[12:13]
	s_cbranch_vccz .LBB0_1930
	s_barrier

; #define PG8_STAGE(bufoff, gbase, voff) do { _Pragma("unroll") for (int _i = 0; _i < 2; ++_i) \
;         __builtin_amdgcn_global_load_lds((const unsigned*)((const char*)(gbase) + (voff)[_i]), (LAS unsigned*)(lds + (bufoff) + ldsw + _i * 8192), 16, 0, 0); } while (0)
; #define PG8_LDA(dst, b, h) do { if constexpr (F8) { _Pragma("unroll") for (int m = 0; m < 4; ++m) dst##8[m] = PG8_LD8(lds, PG8_SA(b, h) + aoff + m * 2048); } \
;         else { _Pragma("unroll") for (int m = 0; m < 4; ++m) _Pragma("unroll") for (int k = 0; k < 2; ++k) dst[m][k] = *(const LAS bf16x8*)(lds + PG8_SA(b, h) + aoff + m * 2048 + k * 1024); } } while (0)
; #define PG8_WAIT_V(n) asm volatile("s_waitcnt vmcnt(" #n ")" ::: "memory")
; #define PG8_WAIT_L(n) asm volatile("s_waitcnt lgkmcnt(" #n ")" ::: "memory")
; #define PG8_BAR __builtin_amdgcn_s_barrier()
; #define PG8_SCHED __builtin_amdgcn_sched_barrier(0)
; template <bool GATHER, bool F8, class Epi, class Sched>
; __device__ __forceinline__ void gemm_phase(LAS unsigned char* lds, const int nt, const unsigned lda, const unsigned ldb, const Sched& S, const Epi& E) {
;     ...
;         for (int t = 0; t < nt; t += 2) {
;             const bool last = (t == nt - 2);
;             const char* a1 = cA + (size_t)(t + 1) * kstep;
;             const char* a2 = last ? nA : cA + (size_t)(t + 2) * kstep; const char* b2 = last ? nB : cB + (size_t)(t + 2) * kstep;
;             const char* a3 = a2 + kstep; const char* b3 = b2 + kstep;
;             unsigned w0[2], w1[2];
;             if constexpr (GATHER) {
; #pragma unroll
;                 for (int i = 0; i < 2; ++i) { w0[i] = last ? vN0[i] : vA0[i]; w1[i] = last ? vN1[i] : vA1[i]; }
;             } else {
; #pragma unroll
;                 for (int i = 0; i < 2; ++i) { w0[i] = voffA[i]; w1[i] = voffA[i]; }
;             }
;             PG8_LDB(B0, 0, 0); PG8_LDB(B1, 0, 1); PG8_SCHED; PG8_LDA(At, 0, 0); PG8_STAGE(PG8_SA(1, 1), a1 + hA, vA1);
;             PG8_WAIT_V(8); PG8_WAIT_L(0); PG8_BAR; PG8_MMA(0, 0, At, B0); PG8_MMA(0, 1, At, B1); PG8_BAR; PG8_SCHED;
;             PG8_LDA(At, 0, 1); PG8_STAGE(PG8_SB(0, 0), b2, voffB); PG8_STAGE(PG8_SB(0, 1), b2 + hB, voffB); PG8_STAGE(PG8_SA(0, 0), a2, w0);
;             PG8_WAIT_V(8); PG8_WAIT_L(0); PG8_BAR; PG8_MMA(1, 0, At, B0); PG8_MMA(1, 1, At, B1); PG8_BAR; PG8_SCHED;
.LBB0_2018:
	ds_read_b128 v[18:21], v186
	ds_read_b128 v[22:25], v186 offset:1024
	ds_read_b128 v[26:29], v186 offset:2048
	ds_read_b128 v[30:33], v186 offset:3072
	ds_read_b128 v[2:5], v186 offset:16384
	ds_read_b128 v[6:9], v186 offset:17408
	ds_read_b128 v[10:13], v186 offset:18432
	ds_read_b128 v[14:17], v186 offset:19456
	s_add_u32 s28, s26, 0xfffc0080
	s_addc_u32 s29, s27, -1
	s_cmp_eq_u32 s58, 12
	s_cselect_b32 s31, s25, s29
	s_cselect_b32 s30, s24, s28
	s_cselect_b32 s29, s23, s12
	s_cselect_b32 s28, s22, s7
	s_add_i32 m0, s1, 0xc000
	ds_read_b128 v[174:177], v187
	ds_read_b128 v[178:181], v187 offset:1024
	ds_read_b128 v[190:193], v187 offset:2048
	ds_read_b128 v[194:197], v187 offset:3072
	ds_read_b128 v[200:203], v187 offset:4096
	ds_read_b128 v[204:207], v187 offset:5120
	ds_read_b128 v[208:211], v187 offset:6144
	ds_read_b128 v[212:215], v187 offset:7168
	global_load_lds_dwordx4 v170, s[26:27]
	s_add_i32 m0, s1, 0xe000
	s_nop 0
	global_load_lds_dwordx4 v172, s[26:27]
	s_waitcnt vmcnt(8)
	s_waitcnt lgkmcnt(0)
	s_barrier
	s_setprio 1
	s_waitcnt lgkmcnt(0)
	v_mfma_scale_f32_16x16x128_f8f6f4 v[158:161], v[18:25], v[174:181], v[158:161], v188, v188 op_sel_hi:[0,0,0]
	v_mfma_scale_f32_16x16x128_f8f6f4 v[154:157], v[26:33], v[174:181], v[154:157], v188, v188 op_sel_hi:[0,0,0]
	v_mfma_scale_f32_16x16x128_f8f6f4 v[142:145], v[18:25], v[190:197], v[142:145], v188, v188 op_sel_hi:[0,0,0]
	v_mfma_scale_f32_16x16x128_f8f6f4 v[138:141], v[26:33], v[190:197], v[138:141], v188, v188 op_sel_hi:[0,0,0]
	v_mfma_scale_f32_16x16x128_f8f6f4 v[126:129], v[18:25], v[200:207], v[126:129], v188, v188 op_sel_hi:[0,0,0]
	v_mfma_scale_f32_16x16x128_f8f6f4 v[122:125], v[26:33], v[200:207], v[122:125], v188, v188 op_sel_hi:[0,0,0]
	v_mfma_scale_f32_16x16x128_f8f6f4 v[110:113], v[18:25], v[208:215], v[110:113], v188, v188 op_sel_hi:[0,0,0]
	v_mfma_scale_f32_16x16x128_f8f6f4 v[106:109], v[26:33], v[208:215], v[106:109], v188, v188 op_sel_hi:[0,0,0]
	s_setprio 0
	s_setprio 1
	v_mfma_scale_f32_16x16x128_f8f6f4 v[150:153], v[2:9], v[174:181], v[150:153], v188, v188 op_sel_hi:[0,0,0]
	v_mfma_scale_f32_16x16x128_f8f6f4 v[146:149], v[10:17], v[174:181], v[146:149], v188, v188 op_sel_hi:[0,0,0]
	v_mfma_scale_f32_16x16x128_f8f6f4 v[134:137], v[2:9], v[190:197], v[134:137], v188, v188 op_sel_hi:[0,0,0]
	v_mfma_scale_f32_16x16x128_f8f6f4 v[130:133], v[10:17], v[190:197], v[130:133], v188, v188 op_sel_hi:[0,0,0]
	v_mfma_scale_f32_16x16x128_f8f6f4 v[118:121], v[2:9], v[200:207], v[118:121], v188, v188 op_sel_hi:[0,0,0]
	v_mfma_scale_f32_16x16x128_f8f6f4 v[114:117], v[10:17], v[200:207], v[114:117], v188, v188 op_sel_hi:[0,0,0]
	v_mfma_scale_f32_16x16x128_f8f6f4 v[102:105], v[2:9], v[208:215], v[102:105], v188, v188 op_sel_hi:[0,0,0]
	v_mfma_scale_f32_16x16x128_f8f6f4 v[98:101], v[10:17], v[208:215], v[98:101], v188, v188 op_sel_hi:[0,0,0]
	s_setprio 0
	s_barrier
	s_mov_b32 m0, s35
	s_add_u32 s60, s28, 0x40000
	ds_read_b128 v[190:193], v187 offset:16384
	ds_read_b128 v[194:197], v187 offset:17408
	ds_read_b128 v[200:203], v187 offset:18432
	ds_read_b128 v[204:207], v187 offset:19456
	ds_read_b128 v[208:211], v187 offset:20480
	ds_read_b128 v[212:215], v187 offset:21504
	ds_read_b128 v[216:219], v187 offset:22528
	ds_read_b128 v[220:223], v187 offset:23552
	global_load_lds_dwordx4 v166, s[28:29]
	s_mov_b32 m0, s36
	s_addc_u32 s61, s29, 0
	global_load_lds_dwordx4 v162, s[28:29]
	s_mov_b32 m0, s37
	s_nop 0
	global_load_lds_dwordx4 v166, s[60:61]
	s_mov_b32 m0, s38
	s_nop 0
	global_load_lds_dwordx4 v162, s[60:61]
	s_mov_b32 m0, s1
	s_nop 0
	s_mov_b64 s[98:99], s[30:31]
	global_load_lds_dwordx4 v168, s[30:31]
	s_mov_b32 m0, s39
	s_nop 0
	global_load_lds_dwordx4 v164, s[30:31]
	s_waitcnt vmcnt(8)
	s_waitcnt lgkmcnt(0)
	s_barrier
	s_setprio 1
	s_waitcnt lgkmcnt(0)
	v_mfma_scale_f32_16x16x128_f8f6f4 v[86:89], v[18:25], v[190:197], v[86:89], v188, v188 op_sel_hi:[0,0,0]
	v_mfma_scale_f32_16x16x128_f8f6f4 v[82:85], v[26:33], v[190:197], v[82:85], v188, v188 op_sel_hi:[0,0,0]
	v_mfma_scale_f32_16x16x128_f8f6f4 v[70:73], v[18:25], v[200:207], v[70:73], v188, v188 op_sel_hi:[0,0,0]
	v_mfma_scale_f32_16x16x128_f8f6f4 v[66:69], v[26:33], v[200:207], v[66:69], v188, v188 op_sel_hi:[0,0,0]
	v_mfma_scale_f32_16x16x128_f8f6f4 v[54:57], v[18:25], v[208:215], v[54:57], v188, v188 op_sel_hi:[0,0,0]
	v_mfma_scale_f32_16x16x128_f8f6f4 v[42:45], v[26:33], v[208:215], v[42:45], v188, v188 op_sel_hi:[0,0,0]
	v_mfma_scale_f32_16x16x128_f8f6f4 v[38:41], v[18:25], v[216:223], v[38:41], v188, v188 op_sel_hi:[0,0,0]
	v_mfma_scale_f32_16x16x128_f8f6f4 v[34:37], v[26:33], v[216:223], v[34:37], v188, v188 op_sel_hi:[0,0,0]
	s_setprio 0
	s_setprio 1
	v_mfma_scale_f32_16x16x128_f8f6f4 v[94:97], v[2:9], v[190:197], v[94:97], v188, v188 op_sel_hi:[0,0,0]
	v_mfma_scale_f32_16x16x128_f8f6f4 v[90:93], v[10:17], v[190:197], v[90:93], v188, v188 op_sel_hi:[0,0,0]
	v_mfma_scale_f32_16x16x128_f8f6f4 v[78:81], v[2:9], v[200:207], v[78:81], v188, v188 op_sel_hi:[0,0,0]
	v_mfma_scale_f32_16x16x128_f8f6f4 v[74:77], v[10:17], v[200:207], v[74:77], v188, v188 op_sel_hi:[0,0,0]
	v_mfma_scale_f32_16x16x128_f8f6f4 v[62:65], v[2:9], v[208:215], v[62:65], v188, v188 op_sel_hi:[0,0,0]
	v_mfma_scale_f32_16x16x128_f8f6f4 v[58:61], v[10:17], v[208:215], v[58:61], v188, v188 op_sel_hi:[0,0,0]
	v_mfma_scale_f32_16x16x128_f8f6f4 v[50:53], v[2:9], v[216:223], v[50:53], v188, v188 op_sel_hi:[0,0,0]
	v_mfma_scale_f32_16x16x128_f8f6f4 v[46:49], v[10:17], v[216:223], v[46:49], v188, v188 op_sel_hi:[0,0,0]
	s_setprio 0
	s_barrier
; #define PG8_STAGE(bufoff, gbase, voff) do { _Pragma("unroll") for (int _i = 0; _i < 2; ++_i) \
;         __builtin_amdgcn_global_load_lds((const unsigned*)((const char*)(gbase) + (voff)[_i]), (LAS unsigned*)(lds + (bufoff) + ldsw + _i * 8192), 16, 0, 0); } while (0)
; #define PG8_LDA(dst, b, h) do { if constexpr (F8) { _Pragma("unroll") for (int m = 0; m < 4; ++m) dst##8[m] = PG8_LD8(lds, PG8_SA(b, h) + aoff + m * 2048); } \
;         else { _Pragma("unroll") for (int m = 0; m < 4; ++m) _Pragma("unroll") for (int k = 0; k < 2; ++k) dst[m][k] = *(const LAS bf16x8*)(lds + PG8_SA(b, h) + aoff + m * 2048 + k * 1024); } } while (0)
; #define PG8_LDB(dst, b, h) do { if constexpr (F8) { _Pragma("unroll") for (int n = 0; n < 2; ++n) dst##8[n] = PG8_LD8(ldsB, PG8_SBR(b, h) + boff + n * 2048); } \
;         else { _Pragma("unroll") for (int n = 0; n < 2; ++n) _Pragma("unroll") for (int k = 0; k < 2; ++k) dst[n][k] = *(const LAS bf16x8*)(ldsB + PG8_SBR(b, h) + boff + n * 2048 + k * 1024); } } while (0)
; #define PG8_WAIT_V(n) asm volatile("s_waitcnt vmcnt(" #n ")" ::: "memory")
; #define PG8_WAIT_L(n) asm volatile("s_waitcnt lgkmcnt(" #n ")" ::: "memory")
; #define PG8_BAR __builtin_amdgcn_s_barrier()
; #define PG8_SCHED __builtin_amdgcn_sched_barrier(0)
; template <bool GATHER, bool F8, class Epi, class Sched>
; __device__ __forceinline__ void gemm_phase(LAS unsigned char* lds, const int nt, const unsigned lda, const unsigned ldb, const Sched& S, const Epi& E) {
;     ...
;             PG8_LDB(B0, 1, 0); PG8_LDB(B1, 1, 1); PG8_SCHED; PG8_LDA(At, 1, 0); PG8_STAGE(PG8_SA(0, 1), a2 + hA, w1);
;             PG8_WAIT_V(8); PG8_WAIT_L(0); PG8_BAR; PG8_MMA(0, 0, At, B0); PG8_MMA(0, 1, At, B1); PG8_BAR; PG8_SCHED;
;             PG8_LDA(At, 1, 1); PG8_STAGE(PG8_SB(1, 0), b3, voffB); PG8_STAGE(PG8_SB(1, 1), b3 + hB, voffB); PG8_STAGE(PG8_SA(1, 0), a3, w0);
;             PG8_WAIT_V(8); PG8_WAIT_L(0); PG8_BAR; PG8_MMA(1, 0, At, B0); PG8_MMA(1, 1, At, B1); PG8_BAR; PG8_SCHED;
;         }
;         if (wr == 0) PG8_BAR;
	ds_read_b128 v[2:5], v186 offset:32768
	ds_read_b128 v[6:9], v186 offset:33792
	ds_read_b128 v[10:13], v186 offset:34816
	ds_read_b128 v[14:17], v186 offset:35840
	ds_read_b128 v[18:21], v186 offset:49152
	ds_read_b128 v[22:25], v186 offset:50176
	ds_read_b128 v[26:29], v186 offset:51200
	ds_read_b128 v[30:33], v186 offset:52224
	s_add_u32 s30, s30, 0x40000
	s_addc_u32 s31, s31, 0
	s_mov_b32 m0, s40
	ds_read_b128 v[190:193], v187 offset:32768
	ds_read_b128 v[194:197], v187 offset:33792
	ds_read_b128 v[200:203], v187 offset:34816
	ds_read_b128 v[204:207], v187 offset:35840
	ds_read_b128 v[208:211], v187 offset:36864
	ds_read_b128 v[212:215], v187 offset:37888
	ds_read_b128 v[216:219], v187 offset:38912
	ds_read_b128 v[220:223], v187 offset:39936
	global_load_lds_dwordx4 v168, s[30:31]
	s_mov_b32 m0, s41
	s_nop 0
	global_load_lds_dwordx4 v164, s[30:31]
	s_waitcnt vmcnt(8)
	s_waitcnt lgkmcnt(0)
	s_barrier
	s_setprio 1
	s_waitcnt lgkmcnt(0)
	v_mfma_scale_f32_16x16x128_f8f6f4 v[158:161], v[2:9], v[190:197], v[158:161], v188, v188 op_sel_hi:[0,0,0]
	v_mfma_scale_f32_16x16x128_f8f6f4 v[154:157], v[10:17], v[190:197], v[154:157], v188, v188 op_sel_hi:[0,0,0]
	v_mfma_scale_f32_16x16x128_f8f6f4 v[142:145], v[2:9], v[200:207], v[142:145], v188, v188 op_sel_hi:[0,0,0]
	v_mfma_scale_f32_16x16x128_f8f6f4 v[138:141], v[10:17], v[200:207], v[138:141], v188, v188 op_sel_hi:[0,0,0]
	v_mfma_scale_f32_16x16x128_f8f6f4 v[126:129], v[2:9], v[208:215], v[126:129], v188, v188 op_sel_hi:[0,0,0]
	v_mfma_scale_f32_16x16x128_f8f6f4 v[122:125], v[10:17], v[208:215], v[122:125], v188, v188 op_sel_hi:[0,0,0]
	v_mfma_scale_f32_16x16x128_f8f6f4 v[110:113], v[2:9], v[216:223], v[110:113], v188, v188 op_sel_hi:[0,0,0]
	v_mfma_scale_f32_16x16x128_f8f6f4 v[106:109], v[10:17], v[216:223], v[106:109], v188, v188 op_sel_hi:[0,0,0]
	s_setprio 0
	s_setprio 1
	v_mfma_scale_f32_16x16x128_f8f6f4 v[150:153], v[18:25], v[190:197], v[150:153], v188, v188 op_sel_hi:[0,0,0]
	v_mfma_scale_f32_16x16x128_f8f6f4 v[146:149], v[26:33], v[190:197], v[146:149], v188, v188 op_sel_hi:[0,0,0]
	v_mfma_scale_f32_16x16x128_f8f6f4 v[134:137], v[18:25], v[200:207], v[134:137], v188, v188 op_sel_hi:[0,0,0]
	v_mfma_scale_f32_16x16x128_f8f6f4 v[130:133], v[26:33], v[200:207], v[130:133], v188, v188 op_sel_hi:[0,0,0]
	v_mfma_scale_f32_16x16x128_f8f6f4 v[118:121], v[18:25], v[208:215], v[118:121], v188, v188 op_sel_hi:[0,0,0]
	v_mfma_scale_f32_16x16x128_f8f6f4 v[114:117], v[26:33], v[208:215], v[114:117], v188, v188 op_sel_hi:[0,0,0]
	v_mfma_scale_f32_16x16x128_f8f6f4 v[102:105], v[18:25], v[216:223], v[102:105], v188, v188 op_sel_hi:[0,0,0]
	v_mfma_scale_f32_16x16x128_f8f6f4 v[98:101], v[26:33], v[216:223], v[98:101], v188, v188 op_sel_hi:[0,0,0]
	s_setprio 0
	s_barrier
	s_add_i32 m0, s43, 0xffffff80
	ds_read_b128 v[190:193], v187 offset:49152
	ds_read_b128 v[194:197], v187 offset:50176
	ds_read_b128 v[200:203], v187 offset:51200
	ds_read_b128 v[204:207], v187 offset:52224
	ds_read_b128 v[208:211], v187 offset:53248
	ds_read_b128 v[212:215], v187 offset:54272
	ds_read_b128 v[216:219], v187 offset:55296
	ds_read_b128 v[220:223], v187 offset:56320
	global_load_lds_dwordx4 v166, s[28:29] offset:128
	s_add_i32 m0, s44, 0xffffff80
	s_nop 0
	global_load_lds_dwordx4 v162, s[28:29] offset:128
	s_add_u32 s28, s28, 0x40080
	s_addc_u32 s29, s29, 0
	s_mov_b32 m0, s47
	s_nop 0
	global_load_lds_dwordx4 v166, s[28:29]
	s_mov_b32 m0, s48
	s_nop 0
	global_load_lds_dwordx4 v162, s[28:29]
	s_add_i32 m0, s45, 0xffffff80
	s_nop 0
	global_load_lds_dwordx4 v168, s[98:99] offset:128
	s_add_i32 m0, s46, 0xffffff80
	s_nop 0
	global_load_lds_dwordx4 v164, s[98:99] offset:128
	s_waitcnt vmcnt(8)
	s_waitcnt lgkmcnt(0)
	s_barrier
	s_setprio 1
	s_waitcnt lgkmcnt(0)
	v_mfma_scale_f32_16x16x128_f8f6f4 v[86:89], v[2:9], v[190:197], v[86:89], v188, v188 op_sel_hi:[0,0,0]
	v_mfma_scale_f32_16x16x128_f8f6f4 v[82:85], v[10:17], v[190:197], v[82:85], v188, v188 op_sel_hi:[0,0,0]
	v_mfma_scale_f32_16x16x128_f8f6f4 v[70:73], v[2:9], v[200:207], v[70:73], v188, v188 op_sel_hi:[0,0,0]
	v_mfma_scale_f32_16x16x128_f8f6f4 v[66:69], v[10:17], v[200:207], v[66:69], v188, v188 op_sel_hi:[0,0,0]
	v_mfma_scale_f32_16x16x128_f8f6f4 v[54:57], v[2:9], v[208:215], v[54:57], v188, v188 op_sel_hi:[0,0,0]
	v_mfma_scale_f32_16x16x128_f8f6f4 v[42:45], v[10:17], v[208:215], v[42:45], v188, v188 op_sel_hi:[0,0,0]
	v_mfma_scale_f32_16x16x128_f8f6f4 v[38:41], v[2:9], v[216:223], v[38:41], v188, v188 op_sel_hi:[0,0,0]
	v_mfma_scale_f32_16x16x128_f8f6f4 v[34:37], v[10:17], v[216:223], v[34:37], v188, v188 op_sel_hi:[0,0,0]
	s_setprio 0
	s_setprio 1
	v_mfma_scale_f32_16x16x128_f8f6f4 v[94:97], v[18:25], v[190:197], v[94:97], v188, v188 op_sel_hi:[0,0,0]
	v_mfma_scale_f32_16x16x128_f8f6f4 v[90:93], v[26:33], v[190:197], v[90:93], v188, v188 op_sel_hi:[0,0,0]
	v_mfma_scale_f32_16x16x128_f8f6f4 v[78:81], v[18:25], v[200:207], v[78:81], v188, v188 op_sel_hi:[0,0,0]
	v_mfma_scale_f32_16x16x128_f8f6f4 v[74:77], v[26:33], v[200:207], v[74:77], v188, v188 op_sel_hi:[0,0,0]
	v_mfma_scale_f32_16x16x128_f8f6f4 v[62:65], v[18:25], v[208:215], v[62:65], v188, v188 op_sel_hi:[0,0,0]
	v_mfma_scale_f32_16x16x128_f8f6f4 v[58:61], v[26:33], v[208:215], v[58:61], v188, v188 op_sel_hi:[0,0,0]
	v_mfma_scale_f32_16x16x128_f8f6f4 v[50:53], v[18:25], v[216:223], v[50:53], v188, v188 op_sel_hi:[0,0,0]
	v_mfma_scale_f32_16x16x128_f8f6f4 v[46:49], v[26:33], v[216:223], v[46:49], v188, v188 op_sel_hi:[0,0,0]
	s_setprio 0
	s_barrier
	s_add_i32 s58, s58, 2
	s_add_u32 s26, s26, 0x100
	s_addc_u32 s27, s27, 0
	s_add_u32 s7, s7, 0x100
	s_addc_u32 s12, s12, 0
	s_cmp_gt_u32 s58, 13
	s_cbranch_scc0 .LBB0_2018
	s_and_b64 vcc, exec, s[14:15]
	s_cbranch_vccz .LBB0_2021
	s_barrier

; #define LAS __attribute__((address_space(3)))
; __device__ __forceinline__ void p12_final(const Frame& F, const KArgs& a) {
;     unsigned char* ws = F.ws; const int lane = F.lane; const LAS int* tab = (const LAS int*)(F.lds + LDS_TAB);
;     const unsigned short* X2 = (const unsigned short*)(ws + WS_X2B); const unsigned char* YB = ws + WS_YB; const int* TOPE = (const int*)(ws + WS_TOPE); const int* TOPR = (const int*)(ws + WS_TOPR);
;     for (int row = F.gw; row < NTOK; row += F.NGW) {
;         size_t so[4];
; #pragma unroll
;         for (int k = 0; k < 4; ++k) { const int e = TOPE[row * 4 + k], r = TOPR[row * 4 + k]; so[k] = (size_t)(tab[e] * 256 + r) * DM; }
;         f32x4 v[8]; float q = 0.f;
; #pragma unroll
;         for (int j = 0; j < 8; ++j) { const int c = 4 * (lane + 64 * j); { const u32x2 xr = *(const u32x2*)(X2 + (size_t)row * DM + c); v[j] = (f32x4){__builtin_bit_cast(float, xr.x << 16), __builtin_bit_cast(float, xr.x & 0xffff0000u), __builtin_bit_cast(float, xr.y << 16), __builtin_bit_cast(float, xr.y & 0xffff0000u)}; }
; #pragma unroll
;             for (int k = 0; k < 4; ++k) { const int y = *(const int*)(YB + so[k] + c);
;     ...
;         for (int j = 0; j < 8; ++j) { const int c = 4 * (lane + 64 * j); const f32x4 g = *(const f32x4*)(a.in[24] + c); *(f32x4*)(a.out + (size_t)row * DM + c) = v[j] * rs * g; }
.LBB0_2097:
	s_or_b64 exec, exec, s[0:1]
	v_readlane_b32 s0, v251, 1
	s_cmpk_gt_i32 s0, 0x3fff
	s_waitcnt lgkmcnt(0)
	s_barrier
	v_readlane_b32 s1, v251, 2
	s_cbranch_scc1 .LBB0_2100
	v_mbcnt_lo_u32_b32 v1, -1, 0
	v_mbcnt_hi_u32_b32 v1, -1, v1
	v_and_b32_e32 v2, 64, v1
	v_add_u32_e32 v2, 64, v2
	v_xor_b32_e32 v3, 1, v1
	v_cmp_lt_i32_e32 vcc, v3, v2
	s_add_u32 s8, s72, 0x39e00000
	s_addc_u32 s9, s73, 0
	v_cndmask_b32_e32 v3, v1, v3, vcc
	v_lshlrev_b32_e32 v66, 2, v3
	v_xor_b32_e32 v3, 2, v1
	v_cmp_lt_i32_e32 vcc, v3, v2
	s_add_u32 s10, s72, 0x39f00000
	s_addc_u32 s11, s73, 0
	v_cndmask_b32_e32 v3, v1, v3, vcc
	v_lshlrev_b32_e32 v67, 2, v3
	v_xor_b32_e32 v3, 4, v1
	v_cmp_lt_i32_e32 vcc, v3, v2
	s_add_u32 s0, s72, 0x4c500000
	v_lshlrev_b32_e32 v0, 2, v198
	v_cndmask_b32_e32 v3, v1, v3, vcc
	v_lshlrev_b32_e32 v68, 2, v3
	v_xor_b32_e32 v3, 8, v1
	v_cmp_lt_i32_e32 vcc, v3, v2
	v_mov_b32_e32 v5, 0
	s_addc_u32 s1, s73, 0
	v_cndmask_b32_e32 v3, v1, v3, vcc
	v_lshlrev_b32_e32 v69, 2, v3
	v_xor_b32_e32 v3, 16, v1
	v_cmp_lt_i32_e32 vcc, v3, v2
	v_readlane_b32 s4, v252, 2
	v_or_b32_e32 v14, 0x400, v0
	v_cndmask_b32_e32 v3, v1, v3, vcc
	v_lshlrev_b32_e32 v70, 2, v3
	v_xor_b32_e32 v3, 32, v1
	v_cmp_lt_i32_e32 vcc, v3, v2
	v_readlane_b32 s5, v252, 3
	v_or_b32_e32 v4, 0x100, v0
	v_cndmask_b32_e32 v1, v1, v3, vcc
	v_lshlrev_b32_e32 v71, 2, v1
	v_mov_b32_e32 v1, v5
	v_lshl_add_u64 v[8:9], s[0:1], 0, v[0:1]
	v_or_b32_e32 v10, 0x200, v0
	v_or_b32_e32 v12, 0x300, v0
	v_or_b32_e32 v16, 0x500, v0
	v_or_b32_e32 v18, 0x600, v0
	v_or_b32_e32 v20, 0x700, v0
	v_lshlrev_b32_e32 v0, 2, v14
	v_lshl_add_u64 v[22:23], s[4:5], 0, v[0:1]
	v_lshlrev_b32_e32 v0, 2, v16
	v_readlane_b32 s20, v251, 1
	v_lshl_add_u64 v[24:25], s[4:5], 0, v[0:1]
	v_lshlrev_b32_e32 v0, 2, v18
	v_readlane_b32 s21, v251, 2
	v_lshlrev_b32_e32 v2, 4, v198
	v_mov_b32_e32 v3, v5
	v_lshl_add_u64 v[26:27], s[4:5], 0, v[0:1]
	v_lshlrev_b32_e32 v0, 2, v20
	s_lshl_b32 s2, s71, 5
	s_lshl_b32 s3, s75, 2
	s_ashr_i32 s21, s20, 31
	v_readlane_b32 s6, v252, 4
	v_lshl_add_u64 v[6:7], s[4:5], 0, v[2:3]
	v_lshl_add_u64 v[28:29], s[4:5], 0, v[0:1]
	s_add_i32 s2, s2, s3
	s_lshl_b32 s12, s74, 5
	s_lshl_b64 s[4:5], s[20:21], 13
	v_readlane_b32 s7, v252, 5
	s_add_u32 s4, s6, s4
	s_addc_u32 s5, s7, s5
	v_lshl_add_u64 v[0:1], s[4:5], 0, v[2:3]
	s_mov_b64 s[4:5], 0x1000
	s_ashr_i32 s95, s94, 31
	v_lshl_add_u64 v[30:31], v[0:1], 0, s[4:5]
	s_lshl_b64 s[4:5], s[94:95], 13
	s_lshl_b64 s[6:7], s[20:21], 12
	s_add_u32 s6, s72, s6
	v_lshlrev_b32_e32 v0, 3, v198
	v_mov_b32_e32 v1, v5
	s_addc_u32 s7, s73, s7
	v_lshl_add_u64 v[0:1], s[6:7], 0, v[0:1]
	s_mov_b64 s[6:7], 0x35c00000
	v_mov_b32_e32 v11, v5
	v_mov_b32_e32 v13, v5
	v_mov_b32_e32 v15, v5
	v_mov_b32_e32 v17, v5
	v_mov_b32_e32 v19, v5
	v_mov_b32_e32 v21, v5
	v_lshl_add_u64 v[32:33], v[0:1], 0, s[6:7]
	s_lshl_b64 s[6:7], s[94:95], 12
	s_add_i32 s13, 0, 0x20100
	v_mov_b32_e32 v72, 0x358637bd
	s_mov_b32 s14, 0x800000
	global_load_dwordx4 v[204:207], v[6:7], off
	global_load_dwordx4 v[208:211], v[6:7], off offset:1024
	global_load_dwordx4 v[212:215], v[6:7], off offset:2048
	global_load_dwordx4 v[216:219], v[6:7], off offset:3072
	global_load_dwordx4 v[220:223], v[22:23], off
	global_load_dwordx4 v[224:227], v[24:25], off
	global_load_dwordx4 v[228:231], v[26:27], off
	global_load_dwordx4 v[232:235], v[28:29], off
.LBB0_2099:
	s_ashr_i32 s3, s2, 31
	s_lshl_b64 s[16:17], s[2:3], 2
	s_add_u32 s18, s8, s16
	s_addc_u32 s19, s9, s17
	global_load_dwordx2 v[34:35], v[32:33], off
	global_load_dwordx2 v[36:37], v[32:33], off offset:512
	global_load_dwordx2 v[38:39], v[32:33], off offset:1024
	global_load_dwordx2 v[40:41], v[32:33], off offset:1536
	global_load_dwordx2 v[42:43], v[32:33], off offset:2048
	global_load_dwordx2 v[56:57], v[32:33], off offset:2560
	global_load_dwordx2 v[60:61], v[32:33], off offset:3072
	global_load_dwordx2 v[64:65], v[32:33], off offset:3584
	global_load_dwordx4 v[74:77], v5, s[18:19]
	s_add_u32 s16, s10, s16
	s_addc_u32 s17, s11, s17
	global_load_dword v73, v5, s[16:17]
	s_add_i32 s18, s2, 1
	s_ashr_i32 s19, s18, 31
	s_lshl_b64 s[16:17], s[18:19], 2
	s_add_u32 s16, s10, s16
	s_addc_u32 s17, s11, s17
	global_load_dwordx3 v[78:80], v5, s[16:17]
	s_add_i32 s20, s20, s94
	s_add_i32 s2, s2, s12
	v_lshl_add_u64 v[32:33], v[32:33], 0, s[6:7]
	s_cmpk_lt_i32 s20, 0x4000
	s_waitcnt vmcnt(10)
	v_lshlrev_b32_e32 v44, 16, v34
	v_and_b32_e32 v45, 0xffff0000, v34
	v_lshlrev_b32_e32 v46, 16, v35
	v_and_b32_e32 v47, 0xffff0000, v35
	s_waitcnt vmcnt(9)
	v_lshlrev_b32_e32 v34, 16, v36
	v_and_b32_e32 v35, 0xffff0000, v36
	v_lshlrev_b32_e32 v36, 16, v37
	v_and_b32_e32 v37, 0xffff0000, v37
	s_waitcnt vmcnt(2)
	v_lshlrev_b32_e32 v74, 2, v74
	v_lshlrev_b32_e32 v75, 2, v75
	v_lshlrev_b32_e32 v76, 2, v76
	v_lshlrev_b32_e32 v77, 2, v77
	v_add_u32_e32 v74, s13, v74
	v_add_u32_e32 v75, s13, v75
	v_add_u32_e32 v76, s13, v76
	v_add_u32_e32 v77, s13, v77
	ds_read_b32 v74, v74
	ds_read_b32 v75, v75
	ds_read_b32 v76, v76
	ds_read_b32 v77, v77
	v_lshlrev_b32_e32 v48, 16, v38
	s_waitcnt lgkmcnt(3)
	v_lshlrev_b32_e32 v74, 8, v74
	s_waitcnt lgkmcnt(2)
	v_lshlrev_b32_e32 v75, 8, v75
	s_waitcnt lgkmcnt(1)
	v_lshlrev_b32_e32 v81, 8, v76
	s_waitcnt lgkmcnt(0)
	v_lshlrev_b32_e32 v77, 8, v77
	s_waitcnt vmcnt(1)
	v_add_u32_e32 v74, v74, v73
	s_waitcnt vmcnt(0)
; __device__ __forceinline__ void p12_final(const Frame& F, const KArgs& a) {
;     ...
;         for (int k = 0; k < 4; ++k) { const int e = TOPE[row * 4 + k], r = TOPR[row * 4 + k]; so[k] = (size_t)(tab[e] * 256 + r) * DM; }
;         f32x4 v[8]; float q = 0.f;
; #pragma unroll
;         for (int j = 0; j < 8; ++j) { const int c = 4 * (lane + 64 * j); { const u32x2 xr = *(const u32x2*)(X2 + (size_t)row * DM + c); v[j] = (f32x4){__builtin_bit_cast(float, xr.x << 16), __builtin_bit_cast(float, xr.x & 0xffff0000u), __builtin_bit_cast(float, xr.y << 16), __builtin_bit_cast(float, xr.y & 0xffff0000u)}; }
; #pragma unroll
;             for (int k = 0; k < 4; ++k) { const int y = *(const int*)(YB + so[k] + c);
;                 v[j][0] += __builtin_amdgcn_cvt_f32_fp8(y, 0); v[j][1] += __builtin_amdgcn_cvt_f32_fp8(y, 1); v[j][2] += __builtin_amdgcn_cvt_f32_fp8(y, 2); v[j][3] += __builtin_amdgcn_cvt_f32_fp8(y, 3); }
	v_add_u32_e32 v76, v75, v78
	v_add_u32_e32 v78, v81, v79
	v_add_u32_e32 v80, v77, v80
	v_ashrrev_i32_e32 v75, 31, v74
	v_ashrrev_i32_e32 v77, 31, v76
	v_ashrrev_i32_e32 v79, 31, v78
	v_ashrrev_i32_e32 v81, 31, v80
	v_lshlrev_b64 v[74:75], 11, v[74:75]
	v_lshlrev_b64 v[76:77], 11, v[76:77]
	v_lshlrev_b64 v[78:79], 11, v[78:79]
	v_lshlrev_b64 v[80:81], 11, v[80:81]
	v_lshl_add_u64 v[82:83], v[8:9], 0, v[74:75]
	v_lshl_add_u64 v[84:85], v[8:9], 0, v[76:77]
	v_lshl_add_u64 v[86:87], v[8:9], 0, v[78:79]
	v_lshl_add_u64 v[88:89], v[8:9], 0, v[80:81]
	global_load_dword v73, v[82:83], off
	global_load_dword v130, v[84:85], off
	global_load_dword v131, v[86:87], off
	global_load_dword v132, v[88:89], off
	v_lshl_add_u64 v[74:75], s[0:1], 0, v[74:75]
	v_lshl_add_u64 v[76:77], s[0:1], 0, v[76:77]
	v_lshl_add_u64 v[78:79], s[0:1], 0, v[78:79]
	v_lshl_add_u64 v[80:81], s[0:1], 0, v[80:81]
	v_lshl_add_u64 v[82:83], v[74:75], 0, v[4:5]
	v_lshl_add_u64 v[84:85], v[76:77], 0, v[4:5]
	v_lshl_add_u64 v[86:87], v[78:79], 0, v[4:5]
	v_lshl_add_u64 v[88:89], v[80:81], 0, v[4:5]
	v_lshl_add_u64 v[90:91], v[74:75], 0, v[10:11]
	v_lshl_add_u64 v[92:93], v[76:77], 0, v[10:11]
	v_lshl_add_u64 v[94:95], v[78:79], 0, v[10:11]
	v_lshl_add_u64 v[96:97], v[80:81], 0, v[10:11]
	v_lshl_add_u64 v[98:99], v[74:75], 0, v[12:13]
	v_lshl_add_u64 v[100:101], v[76:77], 0, v[12:13]
	v_lshl_add_u64 v[102:103], v[78:79], 0, v[12:13]
	v_lshl_add_u64 v[104:105], v[80:81], 0, v[12:13]
	v_lshl_add_u64 v[106:107], v[74:75], 0, v[14:15]
	v_lshl_add_u64 v[108:109], v[76:77], 0, v[14:15]
	v_lshl_add_u64 v[110:111], v[78:79], 0, v[14:15]
	v_lshl_add_u64 v[112:113], v[80:81], 0, v[14:15]
	v_lshl_add_u64 v[114:115], v[74:75], 0, v[16:17]
	v_lshl_add_u64 v[116:117], v[76:77], 0, v[16:17]
	v_lshl_add_u64 v[118:119], v[78:79], 0, v[16:17]
	v_lshl_add_u64 v[120:121], v[80:81], 0, v[16:17]
	v_lshl_add_u64 v[122:123], v[74:75], 0, v[18:19]
	v_lshl_add_u64 v[124:125], v[76:77], 0, v[18:19]
	v_lshl_add_u64 v[126:127], v[78:79], 0, v[18:19]
	v_lshl_add_u64 v[128:129], v[80:81], 0, v[18:19]
	v_lshl_add_u64 v[74:75], v[74:75], 0, v[20:21]
	v_lshl_add_u64 v[76:77], v[76:77], 0, v[20:21]
	v_lshl_add_u64 v[78:79], v[78:79], 0, v[20:21]
	v_lshl_add_u64 v[80:81], v[80:81], 0, v[20:21]
	global_load_dword v133, v[82:83], off
	global_load_dword v134, v[84:85], off
	global_load_dword v135, v[86:87], off
	global_load_dword v136, v[88:89], off
	global_load_dword v137, v[90:91], off
	global_load_dword v138, v[92:93], off
	global_load_dword v139, v[94:95], off
	global_load_dword v140, v[96:97], off
	global_load_dword v141, v[98:99], off
	global_load_dword v142, v[100:101], off
	global_load_dword v143, v[102:103], off
	global_load_dword v144, v[104:105], off
	global_load_dword v145, v[106:107], off
	global_load_dword v146, v[108:109], off
	global_load_dword v149, v[110:111], off
	global_load_dword v153, v[112:113], off
	global_load_dword v157, v[114:115], off
	global_load_dword v161, v[116:117], off
	global_load_dword v165, v[118:119], off
	global_load_dword v169, v[120:121], off
	global_load_dword v173, v[122:123], off
	global_load_dword v177, v[124:125], off
	global_load_dword v181, v[126:127], off
	global_load_dword v185, v[128:129], off
	global_load_dword v189, v[74:75], off
	global_load_dword v193, v[76:77], off
	global_load_dword v197, v[78:79], off
	global_load_dword v201, v[80:81], off
	v_and_b32_e32 v49, 0xffff0000, v38
	v_lshlrev_b32_e32 v38, 16, v39
	v_and_b32_e32 v39, 0xffff0000, v39
	v_lshlrev_b32_e32 v50, 16, v40
	v_and_b32_e32 v51, 0xffff0000, v40
	v_lshlrev_b32_e32 v40, 16, v41
	v_and_b32_e32 v41, 0xffff0000, v41
	v_lshlrev_b32_e32 v52, 16, v42
	v_and_b32_e32 v53, 0xffff0000, v42
	v_lshlrev_b32_e32 v42, 16, v43
	v_and_b32_e32 v43, 0xffff0000, v43
	v_lshlrev_b32_e32 v54, 16, v56
	v_and_b32_e32 v55, 0xffff0000, v56
	v_lshlrev_b32_e32 v56, 16, v57
	v_and_b32_e32 v57, 0xffff0000, v57
	v_lshlrev_b32_e32 v58, 16, v60
	v_and_b32_e32 v59, 0xffff0000, v60
	v_lshlrev_b32_e32 v60, 16, v61
	v_and_b32_e32 v61, 0xffff0000, v61
	v_lshlrev_b32_e32 v62, 16, v64
	v_and_b32_e32 v63, 0xffff0000, v64
	v_lshlrev_b32_e32 v64, 16, v65
	v_and_b32_e32 v65, 0xffff0000, v65
	s_waitcnt vmcnt(27)
	v_cvt_f32_fp8_e32 v90, v133
	v_cvt_f32_fp8_sdwa v91, v133 src0_sel:BYTE_1
	v_cvt_f32_fp8_sdwa v92, v133 src0_sel:BYTE_2
	v_cvt_f32_fp8_sdwa v93, v133 src0_sel:BYTE_3
	s_waitcnt vmcnt(26)
	v_cvt_f32_fp8_e32 v94, v134
	v_cvt_f32_fp8_e32 v74, v73
	v_cvt_f32_fp8_sdwa v75, v73 src0_sel:BYTE_1
	v_cvt_f32_fp8_sdwa v76, v73 src0_sel:BYTE_2
	v_cvt_f32_fp8_sdwa v77, v73 src0_sel:BYTE_3
	v_cvt_f32_fp8_e32 v78, v130
	v_cvt_f32_fp8_sdwa v79, v130 src0_sel:BYTE_1
	v_cvt_f32_fp8_sdwa v80, v130 src0_sel:BYTE_2
	v_cvt_f32_fp8_sdwa v81, v130 src0_sel:BYTE_3
	v_cvt_f32_fp8_sdwa v95, v134 src0_sel:BYTE_1
	v_cvt_f32_fp8_sdwa v96, v134 src0_sel:BYTE_2
	v_cvt_f32_fp8_sdwa v97, v134 src0_sel:BYTE_3
	s_waitcnt vmcnt(23)
	v_cvt_f32_fp8_e32 v106, v137
	v_cvt_f32_fp8_sdwa v107, v137 src0_sel:BYTE_1
	v_cvt_f32_fp8_sdwa v108, v137 src0_sel:BYTE_2
	v_cvt_f32_fp8_sdwa v109, v137 src0_sel:BYTE_3
	v_cvt_f32_fp8_e32 v82, v131
	v_cvt_f32_fp8_sdwa v83, v131 src0_sel:BYTE_1
	v_cvt_f32_fp8_sdwa v84, v131 src0_sel:BYTE_2
	v_cvt_f32_fp8_sdwa v85, v131 src0_sel:BYTE_3
	v_cvt_f32_fp8_e32 v98, v135
	v_cvt_f32_fp8_sdwa v99, v135 src0_sel:BYTE_1
	v_cvt_f32_fp8_sdwa v100, v135 src0_sel:BYTE_2
	v_cvt_f32_fp8_sdwa v101, v135 src0_sel:BYTE_3
	s_waitcnt vmcnt(22)
; __device__ __forceinline__ void p12_final(const Frame& F, const KArgs& a) {
;     ...
;             for (int k = 0; k < 4; ++k) { const int y = *(const int*)(YB + so[k] + c);
;                 v[j][0] += __builtin_amdgcn_cvt_f32_fp8(y, 0); v[j][1] += __builtin_amdgcn_cvt_f32_fp8(y, 1); v[j][2] += __builtin_amdgcn_cvt_f32_fp8(y, 2); v[j][3] += __builtin_amdgcn_cvt_f32_fp8(y, 3); }
;             q += (v[j][0] * v[j][0] + v[j][1] * v[j][1]) + (v[j][2] * v[j][2] + v[j][3] * v[j][3]); }
	v_cvt_f32_fp8_e32 v110, v138
	v_cvt_f32_fp8_sdwa v111, v138 src0_sel:BYTE_1
	v_cvt_f32_fp8_sdwa v112, v138 src0_sel:BYTE_2
	v_cvt_f32_fp8_sdwa v113, v138 src0_sel:BYTE_3
	v_cvt_f32_fp8_e32 v86, v132
	v_cvt_f32_fp8_sdwa v87, v132 src0_sel:BYTE_1
	v_cvt_f32_fp8_sdwa v88, v132 src0_sel:BYTE_2
	v_cvt_f32_fp8_sdwa v89, v132 src0_sel:BYTE_3
	v_cvt_f32_fp8_e32 v102, v136
	v_cvt_f32_fp8_sdwa v103, v136 src0_sel:BYTE_1
	v_cvt_f32_fp8_sdwa v104, v136 src0_sel:BYTE_2
	v_cvt_f32_fp8_sdwa v105, v136 src0_sel:BYTE_3
	s_waitcnt vmcnt(21)
	v_cvt_f32_fp8_e32 v114, v139
	v_cvt_f32_fp8_sdwa v115, v139 src0_sel:BYTE_1
	v_cvt_f32_fp8_sdwa v116, v139 src0_sel:BYTE_2
	v_cvt_f32_fp8_sdwa v117, v139 src0_sel:BYTE_3
	s_waitcnt vmcnt(19)
	v_cvt_f32_fp8_e32 v122, v141
	v_cvt_f32_fp8_sdwa v123, v141 src0_sel:BYTE_1
	v_cvt_f32_fp8_sdwa v124, v141 src0_sel:BYTE_2
	v_cvt_f32_fp8_sdwa v125, v141 src0_sel:BYTE_3
	v_cvt_f32_fp8_e32 v118, v140
	v_cvt_f32_fp8_sdwa v119, v140 src0_sel:BYTE_1
	v_cvt_f32_fp8_sdwa v120, v140 src0_sel:BYTE_2
	v_cvt_f32_fp8_sdwa v121, v140 src0_sel:BYTE_3
	s_waitcnt vmcnt(18)
	v_cvt_f32_fp8_e32 v126, v142
	v_cvt_f32_fp8_sdwa v127, v142 src0_sel:BYTE_1
	v_cvt_f32_fp8_sdwa v128, v142 src0_sel:BYTE_2
	v_cvt_f32_fp8_sdwa v129, v142 src0_sel:BYTE_3
	s_waitcnt vmcnt(15)
	v_cvt_f32_fp8_e32 v138, v145
	v_cvt_f32_fp8_sdwa v139, v145 src0_sel:BYTE_1
	v_cvt_f32_fp8_sdwa v140, v145 src0_sel:BYTE_2
	v_cvt_f32_fp8_sdwa v141, v145 src0_sel:BYTE_3
	v_pk_add_f32 v[44:45], v[74:75], v[44:45]
	v_pk_add_f32 v[46:47], v[76:77], v[46:47]
	v_pk_add_f32 v[34:35], v[90:91], v[34:35]
	v_pk_add_f32 v[36:37], v[92:93], v[36:37]
	v_cvt_f32_fp8_e32 v130, v143
	v_cvt_f32_fp8_sdwa v131, v143 src0_sel:BYTE_1
	v_cvt_f32_fp8_sdwa v132, v143 src0_sel:BYTE_2
	v_cvt_f32_fp8_sdwa v133, v143 src0_sel:BYTE_3
	v_cvt_f32_fp8_e32 v134, v144
	v_cvt_f32_fp8_sdwa v135, v144 src0_sel:BYTE_1
	v_cvt_f32_fp8_sdwa v136, v144 src0_sel:BYTE_2
	v_cvt_f32_fp8_sdwa v137, v144 src0_sel:BYTE_3
	s_waitcnt vmcnt(14)
	v_cvt_f32_fp8_e32 v142, v146
	v_cvt_f32_fp8_sdwa v143, v146 src0_sel:BYTE_1
	v_cvt_f32_fp8_sdwa v144, v146 src0_sel:BYTE_2
	v_cvt_f32_fp8_sdwa v145, v146 src0_sel:BYTE_3
	s_waitcnt vmcnt(11)
	v_cvt_f32_fp8_e32 v154, v157
	v_cvt_f32_fp8_sdwa v155, v157 src0_sel:BYTE_1
	v_cvt_f32_fp8_sdwa v156, v157 src0_sel:BYTE_2
	v_cvt_f32_fp8_sdwa v157, v157 src0_sel:BYTE_3
	v_pk_add_f32 v[44:45], v[44:45], v[78:79]
	v_pk_add_f32 v[46:47], v[46:47], v[80:81]
	v_pk_add_f32 v[48:49], v[106:107], v[48:49]
	v_pk_add_f32 v[38:39], v[108:109], v[38:39]
	v_pk_add_f32 v[34:35], v[34:35], v[94:95]
	v_pk_add_f32 v[36:37], v[36:37], v[96:97]
	v_cvt_f32_fp8_e32 v146, v149
	v_cvt_f32_fp8_sdwa v147, v149 src0_sel:BYTE_1
	v_cvt_f32_fp8_sdwa v148, v149 src0_sel:BYTE_2
	v_cvt_f32_fp8_sdwa v149, v149 src0_sel:BYTE_3
	s_waitcnt vmcnt(10)
	v_cvt_f32_fp8_e32 v158, v161
	v_cvt_f32_fp8_sdwa v159, v161 src0_sel:BYTE_1
	v_cvt_f32_fp8_sdwa v160, v161 src0_sel:BYTE_2
	v_cvt_f32_fp8_sdwa v161, v161 src0_sel:BYTE_3
	v_pk_add_f32 v[44:45], v[44:45], v[82:83]
	v_pk_add_f32 v[46:47], v[46:47], v[84:85]
	v_pk_add_f32 v[48:49], v[48:49], v[110:111]
	v_pk_add_f32 v[38:39], v[38:39], v[112:113]
	v_pk_add_f32 v[34:35], v[34:35], v[98:99]
	v_pk_add_f32 v[36:37], v[36:37], v[100:101]
	v_cvt_f32_fp8_e32 v150, v153
	v_cvt_f32_fp8_sdwa v151, v153 src0_sel:BYTE_1
	v_cvt_f32_fp8_sdwa v152, v153 src0_sel:BYTE_2
	v_cvt_f32_fp8_sdwa v153, v153 src0_sel:BYTE_3
	s_waitcnt vmcnt(9)
	v_cvt_f32_fp8_e32 v162, v165
	v_cvt_f32_fp8_sdwa v163, v165 src0_sel:BYTE_1
	v_cvt_f32_fp8_sdwa v164, v165 src0_sel:BYTE_2
	v_cvt_f32_fp8_sdwa v165, v165 src0_sel:BYTE_3
	s_waitcnt vmcnt(7)
	v_cvt_f32_fp8_e32 v170, v173
	v_cvt_f32_fp8_sdwa v171, v173 src0_sel:BYTE_1
	v_cvt_f32_fp8_sdwa v172, v173 src0_sel:BYTE_2
	v_cvt_f32_fp8_sdwa v173, v173 src0_sel:BYTE_3
	v_pk_add_f32 v[50:51], v[122:123], v[50:51]
	v_pk_add_f32 v[40:41], v[124:125], v[40:41]
	v_pk_add_f32 v[44:45], v[44:45], v[86:87]
	v_pk_add_f32 v[46:47], v[46:47], v[88:89]
	v_pk_add_f32 v[48:49], v[48:49], v[114:115]
	v_pk_add_f32 v[38:39], v[38:39], v[116:117]
	v_pk_add_f32 v[34:35], v[34:35], v[102:103]
	v_pk_add_f32 v[36:37], v[36:37], v[104:105]
	v_cvt_f32_fp8_e32 v166, v169
	v_cvt_f32_fp8_sdwa v167, v169 src0_sel:BYTE_1
	v_cvt_f32_fp8_sdwa v168, v169 src0_sel:BYTE_2
	v_cvt_f32_fp8_sdwa v169, v169 src0_sel:BYTE_3
	s_waitcnt vmcnt(6)
	v_cvt_f32_fp8_e32 v174, v177
	v_cvt_f32_fp8_sdwa v175, v177 src0_sel:BYTE_1
	v_cvt_f32_fp8_sdwa v176, v177 src0_sel:BYTE_2
	v_cvt_f32_fp8_sdwa v177, v177 src0_sel:BYTE_3
	s_waitcnt vmcnt(3)
	v_cvt_f32_fp8_e32 v186, v189
	v_cvt_f32_fp8_sdwa v187, v189 src0_sel:BYTE_1
	v_cvt_f32_fp8_sdwa v188, v189 src0_sel:BYTE_2
	v_cvt_f32_fp8_sdwa v189, v189 src0_sel:BYTE_3
	v_pk_add_f32 v[52:53], v[138:139], v[52:53]
	v_pk_add_f32 v[42:43], v[140:141], v[42:43]
	v_pk_add_f32 v[50:51], v[50:51], v[126:127]
	v_pk_add_f32 v[40:41], v[40:41], v[128:129]
	v_mov_b32_e32 v76, v45
	v_mov_b32_e32 v80, v47
	v_pk_add_f32 v[48:49], v[48:49], v[118:119]
	v_pk_add_f32 v[38:39], v[38:39], v[120:121]
	v_mov_b32_e32 v77, v35
	v_mov_b32_e32 v81, v37
	v_cvt_f32_fp8_e32 v178, v181
	v_cvt_f32_fp8_sdwa v179, v181 src0_sel:BYTE_1
	v_cvt_f32_fp8_sdwa v180, v181 src0_sel:BYTE_2
	v_cvt_f32_fp8_sdwa v181, v181 src0_sel:BYTE_3
	s_waitcnt vmcnt(2)
; __device__ __forceinline__ float wave_sum(float v) {
; #pragma unroll
;     for (int o = 1; o < 64; o <<= 1) v += __shfl_xor(v, o);
;     return v;
; __device__ __forceinline__ void p12_final(const Frame& F, const KArgs& a) {
;     ...
;                 v[j][0] += __builtin_amdgcn_cvt_f32_fp8(y, 0); v[j][1] += __builtin_amdgcn_cvt_f32_fp8(y, 1); v[j][2] += __builtin_amdgcn_cvt_f32_fp8(y, 2); v[j][3] += __builtin_amdgcn_cvt_f32_fp8(y, 3); }
;             q += (v[j][0] * v[j][0] + v[j][1] * v[j][1]) + (v[j][2] * v[j][2] + v[j][3] * v[j][3]); }
;         const float rs = rsqrtf(wave_sum(q) * (1.f / DM) + RMS_EPS);
	v_cvt_f32_fp8_e32 v190, v193
	v_cvt_f32_fp8_sdwa v191, v193 src0_sel:BYTE_1
	v_cvt_f32_fp8_sdwa v192, v193 src0_sel:BYTE_2
	v_cvt_f32_fp8_sdwa v193, v193 src0_sel:BYTE_3
	v_pk_add_f32 v[54:55], v[154:155], v[54:55]
	v_pk_add_f32 v[56:57], v[156:157], v[56:57]
	v_pk_add_f32 v[52:53], v[52:53], v[142:143]
	v_pk_add_f32 v[42:43], v[42:43], v[144:145]
	v_pk_add_f32 v[50:51], v[50:51], v[130:131]
	v_pk_add_f32 v[40:41], v[40:41], v[132:133]
	v_mov_b32_e32 v74, v44
	v_mov_b32_e32 v78, v46
	v_mov_b32_e32 v75, v34
	v_mov_b32_e32 v79, v36
	v_mov_b32_e32 v84, v49
	v_mov_b32_e32 v85, v39
	v_pk_mul_f32 v[76:77], v[76:77], v[76:77]
	v_pk_mul_f32 v[80:81], v[80:81], v[80:81]
	v_cvt_f32_fp8_e32 v182, v185
	v_cvt_f32_fp8_sdwa v183, v185 src0_sel:BYTE_1
	v_cvt_f32_fp8_sdwa v184, v185 src0_sel:BYTE_2
	v_cvt_f32_fp8_sdwa v185, v185 src0_sel:BYTE_3
	s_waitcnt vmcnt(1)
	v_cvt_f32_fp8_e32 v194, v197
	v_cvt_f32_fp8_sdwa v195, v197 src0_sel:BYTE_1
	v_cvt_f32_fp8_sdwa v196, v197 src0_sel:BYTE_2
	v_cvt_f32_fp8_sdwa v197, v197 src0_sel:BYTE_3
	v_pk_add_f32 v[54:55], v[54:55], v[158:159]
	v_pk_add_f32 v[56:57], v[56:57], v[160:161]
	v_pk_add_f32 v[52:53], v[52:53], v[146:147]
	v_pk_add_f32 v[42:43], v[42:43], v[148:149]
	v_pk_add_f32 v[50:51], v[50:51], v[134:135]
	v_pk_add_f32 v[40:41], v[40:41], v[136:137]
	v_mov_b32_e32 v82, v48
	v_mov_b32_e32 v83, v38
	v_pk_mul_f32 v[84:85], v[84:85], v[84:85]
	v_pk_fma_f32 v[74:75], v[74:75], v[74:75], v[76:77]
	v_pk_fma_f32 v[76:77], v[78:79], v[78:79], v[80:81]
	s_waitcnt vmcnt(0)
	v_cvt_f32_fp8_e32 v198, v201
	v_cvt_f32_fp8_sdwa v199, v201 src0_sel:BYTE_1
	v_cvt_f32_fp8_sdwa v200, v201 src0_sel:BYTE_2
	v_cvt_f32_fp8_sdwa v201, v201 src0_sel:BYTE_3
	v_pk_add_f32 v[58:59], v[170:171], v[58:59]
	v_pk_add_f32 v[60:61], v[172:173], v[60:61]
	v_pk_add_f32 v[54:55], v[54:55], v[162:163]
	v_pk_add_f32 v[56:57], v[56:57], v[164:165]
	v_pk_add_f32 v[52:53], v[52:53], v[150:151]
	v_pk_add_f32 v[42:43], v[42:43], v[152:153]
	v_mul_f32_e32 v86, v51, v51
	v_mul_f32_e32 v88, v41, v41
	v_pk_fma_f32 v[78:79], v[82:83], v[82:83], v[84:85]
	v_pk_add_f32 v[74:75], v[74:75], v[76:77]
	v_pk_add_f32 v[62:63], v[186:187], v[62:63]
	v_pk_add_f32 v[64:65], v[188:189], v[64:65]
	v_pk_add_f32 v[58:59], v[58:59], v[174:175]
	v_pk_add_f32 v[60:61], v[60:61], v[176:177]
	v_pk_add_f32 v[54:55], v[54:55], v[166:167]
	v_pk_add_f32 v[56:57], v[56:57], v[168:169]
	v_pk_mul_f32 v[90:91], v[52:53], v[52:53]
	v_pk_mul_f32 v[92:93], v[42:43], v[42:43]
	v_pk_fma_f32 v[86:87], v[50:51], v[50:51], v[86:87] op_sel_hi:[1,1,0]
	v_pk_fma_f32 v[88:89], v[40:41], v[40:41], v[88:89] op_sel_hi:[1,1,0]
	v_pk_add_f32 v[76:77], v[78:79], v[78:79] op_sel:[0,1] op_sel_hi:[1,0]
	v_pk_add_f32 v[74:75], v[74:75], v[74:75] op_sel:[0,1] op_sel_hi:[1,0]
	v_pk_add_f32 v[62:63], v[62:63], v[190:191]
	v_pk_add_f32 v[64:65], v[64:65], v[192:193]
	v_pk_add_f32 v[58:59], v[58:59], v[178:179]
	v_pk_add_f32 v[60:61], v[60:61], v[180:181]
	v_mov_b32_e32 v96, v55
	v_mov_b32_e32 v97, v57
	v_mov_b32_e32 v87, v92
	v_mov_b32_e32 v89, v93
	v_mov_b32_e32 v77, v91
	v_mov_b32_e32 v75, v90
	v_pk_add_f32 v[62:63], v[62:63], v[194:195]
	v_pk_add_f32 v[64:65], v[64:65], v[196:197]
	v_pk_add_f32 v[58:59], v[58:59], v[182:183]
	v_pk_add_f32 v[60:61], v[60:61], v[184:185]
	v_mov_b32_e32 v94, v54
	v_mov_b32_e32 v95, v56
	v_pk_mul_f32 v[96:97], v[96:97], v[96:97]
	v_pk_add_f32 v[78:79], v[86:87], v[88:89]
	v_pk_add_f32 v[74:75], v[74:75], v[76:77]
	v_pk_add_f32 v[62:63], v[62:63], v[198:199]
	v_pk_add_f32 v[64:65], v[64:65], v[200:201]
	v_mul_f32_e32 v98, v59, v59
	v_mul_f32_e32 v100, v61, v61
	v_pk_fma_f32 v[80:81], v[94:95], v[94:95], v[96:97]
	v_pk_add_f32 v[74:75], v[74:75], v[78:79]
	v_pk_mul_f32 v[102:103], v[62:63], v[62:63]
	v_pk_mul_f32 v[104:105], v[64:65], v[64:65]
	v_pk_fma_f32 v[98:99], v[58:59], v[58:59], v[98:99] op_sel_hi:[1,1,0]
	v_pk_fma_f32 v[100:101], v[60:61], v[60:61], v[100:101] op_sel_hi:[1,1,0]
	v_pk_add_f32 v[80:81], v[80:81], v[80:81] op_sel:[0,1] op_sel_hi:[1,0]
	v_pk_add_f32 v[74:75], v[74:75], v[74:75] op_sel:[0,1] op_sel_hi:[1,0]
	v_mov_b32_e32 v99, v104
	v_mov_b32_e32 v101, v105
	v_mov_b32_e32 v81, v103
	v_mov_b32_e32 v75, v102
	v_pk_add_f32 v[82:83], v[98:99], v[100:101]
	v_pk_add_f32 v[74:75], v[74:75], v[80:81]
	s_nop 0
	v_pk_add_f32 v[74:75], v[74:75], v[82:83]
	s_nop 0
	v_add_f32_e32 v73, v74, v75
	ds_bpermute_b32 v74, v66, v73
	s_waitcnt lgkmcnt(0)
; __device__ __forceinline__ float wave_sum(float v) {
; #pragma unroll
;     for (int o = 1; o < 64; o <<= 1) v += __shfl_xor(v, o);
;     return v;
; __device__ __forceinline__ void p12_final(const Frame& F, const KArgs& a) {
;     ...
;         const float rs = rsqrtf(wave_sum(q) * (1.f / DM) + RMS_EPS);
; #pragma unroll
;         for (int j = 0; j < 8; ++j) { const int c = 4 * (lane + 64 * j); const f32x4 g = *(const f32x4*)(a.in[24] + c); *(f32x4*)(a.out + (size_t)row * DM + c) = v[j] * rs * g; }
	v_add_f32_e32 v73, v73, v74
	ds_bpermute_b32 v74, v67, v73
	s_waitcnt lgkmcnt(0)
	v_add_f32_e32 v73, v73, v74
	ds_bpermute_b32 v74, v68, v73
	s_waitcnt lgkmcnt(0)
	v_add_f32_e32 v73, v73, v74
	ds_bpermute_b32 v74, v69, v73
	s_waitcnt lgkmcnt(0)
	v_add_f32_e32 v73, v73, v74
	ds_bpermute_b32 v74, v70, v73
	s_waitcnt lgkmcnt(0)
	v_add_f32_e32 v73, v73, v74
	ds_bpermute_b32 v74, v71, v73
	s_waitcnt lgkmcnt(0)
	v_add_f32_e32 v73, v73, v74
	v_fmamk_f32 v73, v73, 0x3a000000, v72
	v_mul_f32_e32 v74, 0x4b800000, v73
	v_cmp_gt_f32_e32 vcc, s14, v73
	s_nop 1
	v_cndmask_b32_e32 v73, v73, v74, vcc
	v_rsq_f32_e32 v73, v73
	s_nop 0
	v_mul_f32_e32 v74, 0x45800000, v73
	v_cndmask_b32_e32 v74, v73, v74, vcc
	v_pk_mul_f32 v[44:45], v[44:45], v[74:75] op_sel_hi:[1,0]
	v_pk_mul_f32 v[46:47], v[46:47], v[74:75] op_sel_hi:[1,0]
	v_pk_mul_f32 v[0:1], v[204:205], v[44:45]
	v_pk_mul_f32 v[2:3], v[206:207], v[46:47]
	global_store_dwordx4 v[30:31], v[0:3], off offset:-4096
	v_pk_mul_f32 v[36:37], v[36:37], v[74:75] op_sel_hi:[1,0]
	v_pk_mul_f32 v[34:35], v[34:35], v[74:75] op_sel_hi:[1,0]
	v_pk_mul_f32 v[238:239], v[210:211], v[36:37]
	v_pk_mul_f32 v[236:237], v[208:209], v[34:35]
	global_store_dwordx4 v[30:31], v[236:239], off offset:-3072
	v_pk_mul_f32 v[34:35], v[38:39], v[74:75] op_sel_hi:[1,0]
	v_pk_mul_f32 v[36:37], v[48:49], v[74:75] op_sel_hi:[1,0]
	v_pk_mul_f32 v[2:3], v[214:215], v[34:35]
	v_pk_mul_f32 v[0:1], v[212:213], v[36:37]
	global_store_dwordx4 v[30:31], v[0:3], off offset:-2048
	v_pk_mul_f32 v[34:35], v[40:41], v[74:75] op_sel_hi:[1,0]
	v_pk_mul_f32 v[36:37], v[50:51], v[74:75] op_sel_hi:[1,0]
	v_pk_mul_f32 v[238:239], v[218:219], v[34:35]
	v_pk_mul_f32 v[236:237], v[216:217], v[36:37]
	global_store_dwordx4 v[30:31], v[236:239], off offset:-1024
	v_pk_mul_f32 v[34:35], v[42:43], v[74:75] op_sel_hi:[1,0]
	v_pk_mul_f32 v[36:37], v[52:53], v[74:75] op_sel_hi:[1,0]
	v_pk_mul_f32 v[2:3], v[222:223], v[34:35]
	v_pk_mul_f32 v[0:1], v[220:221], v[36:37]
	global_store_dwordx4 v[30:31], v[0:3], off
	v_pk_mul_f32 v[34:35], v[56:57], v[74:75] op_sel_hi:[1,0]
	v_pk_mul_f32 v[36:37], v[54:55], v[74:75] op_sel_hi:[1,0]
	v_pk_mul_f32 v[238:239], v[226:227], v[34:35]
	v_pk_mul_f32 v[236:237], v[224:225], v[36:37]
	global_store_dwordx4 v[30:31], v[236:239], off offset:1024
	v_pk_mul_f32 v[34:35], v[60:61], v[74:75] op_sel_hi:[1,0]
	v_pk_mul_f32 v[36:37], v[58:59], v[74:75] op_sel_hi:[1,0]
	v_pk_mul_f32 v[2:3], v[230:231], v[34:35]
	v_pk_mul_f32 v[0:1], v[228:229], v[36:37]
	global_store_dwordx4 v[30:31], v[0:3], off offset:2048
	v_pk_mul_f32 v[34:35], v[64:65], v[74:75] op_sel_hi:[1,0]
	v_pk_mul_f32 v[36:37], v[62:63], v[74:75] op_sel_hi:[1,0]
	v_pk_mul_f32 v[238:239], v[34:35], v[234:235]
	v_pk_mul_f32 v[236:237], v[36:37], v[232:233]
	global_store_dwordx4 v[30:31], v[236:239], off offset:3072
	v_lshl_add_u64 v[30:31], v[30:31], 0, s[4:5]
	s_cbranch_scc1 .LBB0_2099

; #define LAS __attribute__((address_space(3)))
; __global__ void __launch_bounds__(NTHREADS, 2) mega_fwd(KArgs args) {
;     extern __shared__ __attribute__((aligned(16))) unsigned char lds_raw[];
;     Frame F;
;     F.lds = (LAS unsigned char*)lds_raw; F.MISC = (volatile LAS unsigned*)(F.lds + LDS_MISC);
;     F.tid = threadIdx.x; F.lane = F.tid & 63; F.wave = __builtin_amdgcn_readfirstlane(F.tid >> 6);
;     F.G = gridDim.x; F.gw = blockIdx.x * NWAVES + F.wave; F.NGW = F.G * NWAVES;
;     F.ws = args.ws; F.ctl = (unsigned*)(args.ws + WS_CTL);
;     unsigned char* ws = args.ws;
;     for (int u = F.tid; u < (LDS_BYTES - LDS_MISC) / 4; u += NTHREADS) ((LAS unsigned*)(F.lds + LDS_MISC))[u] = 0u;
;     __syncthreads();
;     XcdBarrier bar = xcd_barrier_post(F.ctl + CW_BAR + args.li * XCD_BAR_WORDS, F.MISC + 8);
	.amdhsa_kernel _Z8mega_fwd5KArgs
		.amdhsa_group_segment_fixed_size 0
		.amdhsa_private_segment_fixed_size 0
		.amdhsa_kernarg_size 488
		.amdhsa_user_sgpr_count 2
		.amdhsa_user_sgpr_dispatch_ptr 0
		.amdhsa_user_sgpr_queue_ptr 0
		.amdhsa_user_sgpr_kernarg_segment_ptr 1
		.amdhsa_user_sgpr_dispatch_id 0
		.amdhsa_user_sgpr_kernarg_preload_length 0
		.amdhsa_user_sgpr_kernarg_preload_offset 0
		.amdhsa_user_sgpr_private_segment_size 0
		.amdhsa_uses_dynamic_stack 0
		.amdhsa_enable_private_segment 0
		.amdhsa_system_sgpr_workgroup_id_x 1
		.amdhsa_system_sgpr_workgroup_id_y 0
		.amdhsa_system_sgpr_workgroup_id_z 0
		.amdhsa_system_sgpr_workgroup_info 0
		.amdhsa_system_vgpr_workitem_id 0
		.amdhsa_next_free_vgpr 253
		.amdhsa_next_free_sgpr 102
		.amdhsa_accum_offset 256
		.amdhsa_reserve_vcc 1
		.amdhsa_float_round_mode_32 0
		.amdhsa_float_round_mode_16_64 0
		.amdhsa_float_denorm_mode_32 3
		.amdhsa_float_denorm_mode_16_64 3
		.amdhsa_dx10_clamp 1
		.amdhsa_ieee_mode 1
		.amdhsa_fp16_overflow 0
		.amdhsa_tg_split 0
		.amdhsa_exception_fp_ieee_invalid_op 0
		.amdhsa_exception_fp_denorm_src 0
		.amdhsa_exception_fp_ieee_div_zero 0
		.amdhsa_exception_fp_ieee_overflow 0
		.amdhsa_exception_fp_ieee_underflow 0
		.amdhsa_exception_fp_ieee_inexact 0
		.amdhsa_exception_int_div_zero 0
	.end_amdhsa_kernel

; #define LAS __attribute__((address_space(3)))
; __global__ void __launch_bounds__(NTHREADS, 2) mega_fwd(KArgs args) {
;     extern __shared__ __attribute__((aligned(16))) unsigned char lds_raw[];
;     Frame F;
;     F.lds = (LAS unsigned char*)lds_raw; F.MISC = (volatile LAS unsigned*)(F.lds + LDS_MISC);
;     F.tid = threadIdx.x; F.lane = F.tid & 63; F.wave = __builtin_amdgcn_readfirstlane(F.tid >> 6);
;     F.G = gridDim.x; F.gw = blockIdx.x * NWAVES + F.wave; F.NGW = F.G * NWAVES;
;     F.ws = args.ws; F.ctl = (unsigned*)(args.ws + WS_CTL);
amdhsa.kernels:
  - .agpr_count:     0
    .args:
      - .offset:         0
        .size:           232
        .value_kind:     by_value
      - .offset:         232
        .size:           4
        .value_kind:     hidden_block_count_x
      - .offset:         236
        .size:           4
        .value_kind:     hidden_block_count_y
      - .offset:         240
        .size:           4
        .value_kind:     hidden_block_count_z
      - .offset:         244
        .size:           2
        .value_kind:     hidden_group_size_x
      - .offset:         246
        .size:           2
        .value_kind:     hidden_group_size_y
      - .offset:         248
        .size:           2
        .value_kind:     hidden_group_size_z
      - .offset:         250
        .size:           2
        .value_kind:     hidden_remainder_x
      - .offset:         252
        .size:           2
        .value_kind:     hidden_remainder_y
      - .offset:         254
        .size:           2
        .value_kind:     hidden_remainder_z
      - .offset:         272
        .size:           8
        .value_kind:     hidden_global_offset_x
      - .offset:         280
        .size:           8
        .value_kind:     hidden_global_offset_y
      - .offset:         288
        .size:           8
        .value_kind:     hidden_global_offset_z
      - .offset:         296
        .size:           2
        .value_kind:     hidden_grid_dims
      - .offset:         352
        .size:           4
        .value_kind:     hidden_dynamic_lds_size
    .group_segment_fixed_size: 0
    .kernarg_segment_align: 8
    .kernarg_segment_size: 488
    .language:       OpenCL C
    .language_version:
      - 2
      - 0
    .max_flat_workgroup_size: 512
    .name:           _Z8mega_fwd5KArgs
    .private_segment_fixed_size: 0
    .sgpr_count:     108
    .sgpr_spill_count: 336
    .symbol:         _Z8mega_fwd5KArgs.kd
    .uniform_work_group_size: 1
    .uses_dynamic_stack: false
    .vgpr_count:     253
    .vgpr_spill_count: 0
    .wavefront_size: 64
